# fp8 loops restructured + attention HALFU half-step stagger for waves 4-7 + unscaled v_mfma_f32_16x16x128_f8f6f4 (unit scales dropped, same fp8 e4m3 operands)
# speedup vs baseline: 1.0091x; 1.0091x over previous
; template <int KB, bool EXT>
; __device__ __forceinline__ void qkt(f32x16& p0, f32x16& p1, const char* lds, int r32, int hi, const bf16x8* qr, bf16x8 qx) {
;     p0 = f32x16{}; p1 = f32x16{};
;     const char* kb[4];
; #pragma unroll
;     for (int dd = 0; dd < 4; ++dd) kb[dd] = lds + OFF_K + KB * SHM_K + KSWZ(r32, (dd * 16 + hi * 8) * 2);
; #pragma unroll
;     for (int d0 = 0; d0 < 8; ++d0) { const char* a = kb[d0 & 3] + (d0 >> 2) * 128;
;         bf16x8 b0 = *reinterpret_cast<const bf16x8*>(a);
;         bf16x8 b1 = *reinterpret_cast<const bf16x8*>(a + 32 * 256);
;         p0 = __builtin_amdgcn_mfma_f32_32x32x16_bf16(b0, qr[d0], p0, 0, 0, 0);
;         p1 = __builtin_amdgcn_mfma_f32_32x32x16_bf16(b1, qr[d0], p1, 0, 0, 0); }
; template <int MODE> ...
;     ...
;         const int tdiag = P0 / KVBLK; int r = 1;
;         for (; r + 1 < NTr && jb + r + 1 <= tdiag; r += 2) {
;             HALFU(pB0, pB1, mnB, alB, pA0, pA1, alA, jb + r, 1, 0);
;             HALFU(pA0, pA1, mnA, alA, pB0, pB1, alB, jb + r + 1, 0, 1);
.LBB0_1158:
	s_cmp_eq_u32 s58, 1
	s_cselect_b32 s69, s3, s2
	s_lshl_b32 s1, s4, 2
	s_add_i32 s62, s1, 0
	s_add_i32 s62, s62, 0x11000
	v_lshlrev_b32_e32 v3, 1, v192
	v_lshlrev_b32_e32 v2, 4, v192
	v_and_b32_e32 v3, 32, v3
	s_movk_i32 s1, 0xc0
	s_cmp_lg_u32 0, -1
	v_and_or_b32 v2, v2, s1, v3
	s_cselect_b32 s1, 0, 0
	v_and_b32_e32 v3, 0x100, v36
	s_sub_i32 s2, s69, s61
	s_waitcnt vmcnt(0)
	s_add_i32 s33, s1, s72
	v_or3_b32 v2, v2, v3, v37
	s_add_i32 s70, s2, -1
	s_addk_i32 s33, 0x4000
	s_mov_b32 s26, 1
	v_add_u32_e32 v194, s1, v2
	s_cmp_lt_i32 s2, 3
	s_barrier
	s_cbranch_scc1 .LBB0_1175
	s_or_b32 s1, s61, 1
	s_cmp_ge_u32 s1, s71
	s_mov_b32 s74, 0
	s_cbranch_scc1 .LBB0_1177
	s_cmp_lg_u32 0, -1
	s_cselect_b32 s1, 0, 0
	s_add_i32 s1, s1, s72
	v_and_b32_e32 v2, 0x70, v199
	s_add_i32 s75, s1, 0x6000
	v_xad_u32 v18, v2, v207, 0
	v_xad_u32 v19, v203, v2, 0
	v_xad_u32 v20, v201, v2, 0
	v_xad_u32 v21, v200, v2, 0
	s_add_u32 s0, s45, s0
	v_mov_b32_e32 v16, v179
	v_mov_b32_e32 v17, v179
	s_addc_u32 s1, s46, 0
	v_mov_b32_e32 v2, v179
	v_mov_b32_e32 v3, v179
	v_mov_b32_e32 v4, v179
	v_mov_b32_e32 v5, v179
	v_mov_b32_e32 v6, v179
	v_mov_b32_e32 v7, v179
	v_mov_b32_e32 v8, v179
	v_mov_b32_e32 v9, v179
	v_mov_b32_e32 v10, v179
	v_mov_b32_e32 v11, v179
	v_mov_b32_e32 v12, v179
	v_mov_b32_e32 v13, v179
	v_mov_b32_e32 v14, v179
	v_mov_b32_e32 v15, v179
	v_add_u32_e32 v210, v18, v198
	v_add_u32_e32 v211, v19, v198
	v_add_u32_e32 v212, v20, v198
	v_add_u32_e32 v213, v21, v198
	v_mov_b64_e32 v[64:65], v[16:17]
	s_waitcnt vmcnt(0)
	v_mov_b64_e32 v[48:49], v[16:17]
	v_mov_b64_e32 v[32:33], v[16:17]
	v_cmp_gt_u32_e64 s[2:3], 32, v192
	v_lshl_add_u32 v208, v190, 2, s62
	v_add_u32_e32 v209, s62, v207
	v_lshl_add_u64 v[182:183], s[0:1], 0, v[178:179]
	v_mov_b32_e32 v181, 0
	s_mov_b64 s[0:1], s[18:19]
	s_mov_b64 s[6:7], s[20:21]
	v_mov_b32_e32 v214, v206
	v_mov_b64_e32 v[62:63], v[14:15]
	v_mov_b64_e32 v[60:61], v[12:13]
	v_mov_b64_e32 v[58:59], v[10:11]
	v_mov_b64_e32 v[56:57], v[8:9]
	v_mov_b64_e32 v[54:55], v[6:7]
	v_mov_b64_e32 v[52:53], v[4:5]
	v_mov_b64_e32 v[50:51], v[2:3]
	v_mov_b64_e32 v[46:47], v[14:15]
	v_mov_b64_e32 v[44:45], v[12:13]
	v_mov_b64_e32 v[42:43], v[10:11]
	v_mov_b64_e32 v[40:41], v[8:9]
	v_mov_b64_e32 v[38:39], v[6:7]
	v_mov_b64_e32 v[36:37], v[4:5]
	v_mov_b64_e32 v[34:35], v[2:3]
	v_mov_b64_e32 v[30:31], v[14:15]
	v_mov_b64_e32 v[28:29], v[12:13]
	v_mov_b64_e32 v[26:27], v[10:11]
	v_mov_b64_e32 v[24:25], v[8:9]
	v_mov_b64_e32 v[22:23], v[6:7]
	v_mov_b64_e32 v[20:21], v[4:5]
	v_mov_b64_e32 v[18:19], v[2:3]
	v_readfirstlane_b32 s99, v0
	s_nop 0
	s_lshr_b32 s99, s99, 8
.LBB0_1161:
	global_load_dwordx2 v[162:163], v[182:183], off offset:-8
	s_add_u32 s76, s0, s73
	s_addc_u32 s77, s1, 0
	s_add_u32 s4, s76, 0x8000
	s_addc_u32 s5, s77, 0
	s_add_u32 s26, s6, s73
	s_mov_b32 s24, m0
	s_mov_b32 m0, s64
	s_nop 0
	global_load_lds_dwordx4 v204, s[4:5]
	s_mov_b32 m0, s24
	s_addc_u32 s27, s7, 0
	s_mov_b32 s24, m0
	s_mov_b32 m0, s65
	s_nop 0
	global_load_lds_dwordx4 v205, s[4:5]
	s_mov_b32 m0, s24
	s_add_u32 s4, s26, 0x4000
	s_addc_u32 s5, s27, 0
	s_mov_b32 s24, m0
	s_mov_b32 m0, s33
	s_nop 0
	global_load_lds_dwordx4 v196, s[4:5]
	s_mov_b32 m0, s24
	s_nop 0
	s_mov_b32 s24, m0
	s_mov_b32 m0, s75
	s_nop 0
	global_load_lds_dwordx4 v197, s[4:5]
	s_mov_b32 m0, s24
	ds_read_b128 v[66:69], v210 offset:49152
	ds_read_b128 v[82:85], v210 offset:57344
	ds_read_b128 v[164:167], v211 offset:49152
	ds_read_b128 v[168:171], v211 offset:57344
	v_exp_f32_e32 v114, v114
	v_exp_f32_e32 v115, v115
	s_waitcnt lgkmcnt(3)
	v_mfma_f32_32x32x16_bf16 v[66:81], v[66:69], v[146:149], 0
	v_exp_f32_e32 v116, v116
	v_exp_f32_e32 v117, v117
	v_exp_f32_e32 v118, v118
	v_exp_f32_e32 v119, v119
	v_exp_f32_e32 v120, v120
	v_exp_f32_e32 v121, v121
	v_exp_f32_e32 v122, v122
	s_waitcnt lgkmcnt(2)
	v_mfma_f32_32x32x16_bf16 v[82:97], v[82:85], v[146:149], 0
	v_exp_f32_e32 v123, v123
	v_exp_f32_e32 v124, v124
	v_exp_f32_e32 v125, v125
	v_exp_f32_e32 v126, v126
	v_exp_f32_e32 v127, v127
	v_exp_f32_e32 v128, v128
	v_exp_f32_e32 v129, v129
	s_waitcnt lgkmcnt(1)
	v_mfma_f32_32x32x16_bf16 v[66:81], v[164:167], v[150:153], v[66:81]
	s_waitcnt lgkmcnt(0)
	v_mfma_f32_32x32x16_bf16 v[82:97], v[168:171], v[150:153], v[82:97]
	ds_read_b128 v[164:167], v212 offset:49152
	ds_read_b128 v[168:171], v212 offset:57344
	s_waitcnt lgkmcnt(1)
	v_mfma_f32_32x32x16_bf16 v[66:81], v[164:167], v[154:157], v[66:81]
	s_waitcnt lgkmcnt(0)
	v_mfma_f32_32x32x16_bf16 v[82:97], v[168:171], v[154:157], v[82:97]
	ds_read_b128 v[164:167], v213 offset:49152
	ds_read_b128 v[168:171], v213 offset:57344
	s_waitcnt lgkmcnt(1)
	v_mfma_f32_32x32x16_bf16 v[66:81], v[164:167], v[158:161], v[66:81]
	s_waitcnt lgkmcnt(0)
	v_mfma_f32_32x32x16_bf16 v[82:97], v[168:171], v[158:161], v[82:97]
	ds_read_b128 v[164:167], v210 offset:49280
	ds_read_b128 v[168:171], v210 offset:57472
	s_waitcnt lgkmcnt(1)
	v_mfma_f32_32x32x16_bf16 v[66:81], v[164:167], v[142:145], v[66:81]
	s_waitcnt lgkmcnt(0)
	v_mfma_f32_32x32x16_bf16 v[82:97], v[168:171], v[142:145], v[82:97]
	ds_read_b128 v[164:167], v211 offset:49280
	ds_read_b128 v[168:171], v211 offset:57472
	s_waitcnt lgkmcnt(1)
	v_mfma_f32_32x32x16_bf16 v[66:81], v[164:167], v[138:141], v[66:81]
	s_waitcnt lgkmcnt(0)
	v_mfma_f32_32x32x16_bf16 v[82:97], v[168:171], v[138:141], v[82:97]
	ds_read_b128 v[164:167], v212 offset:49280
	ds_read_b128 v[168:171], v212 offset:57472
	s_waitcnt lgkmcnt(1)
	v_mfma_f32_32x32x16_bf16 v[66:81], v[164:167], v[134:137], v[66:81]
	s_waitcnt lgkmcnt(0)
	v_mfma_f32_32x32x16_bf16 v[82:97], v[168:171], v[134:137], v[82:97]
	ds_read_b128 v[164:167], v213 offset:49280
	ds_read_b128 v[168:171], v213 offset:57472
	s_waitcnt lgkmcnt(1)
; __device__ __forceinline__ void finishSM(f32x16& p0, f32x16& p1, float alpha, float& l_reg, bf16x8& pa0, bf16x8& pa1, bf16x8& pa2, bf16x8& pa3) {
;     for (int r = 0; r < 16; ++r) p1[r] = __builtin_amdgcn_exp2f(p1[r]);
;     float ps = 0; for (int r = 0; r < 16; ++r) ps += p0[r]; for (int r = 0; r < 16; ++r) ps += p1[r];
;     { auto rr = __builtin_amdgcn_permlane32_swap(__float_as_uint(ps), __float_as_uint(ps), false, false);
;       ps = __uint_as_float(rr[0]) + __uint_as_float(rr[1]); }
;     l_reg = l_reg * alpha + ps;
;     ...
;     PK4(p0, 0, pa0); PK4(p0, 8, pa1); PK4(p1, 0, pa2); PK4(p1, 8, pa3);
;     ...
; }
; template <int KB, bool EXT>
; __device__ __forceinline__ void qkt(f32x16& p0, f32x16& p1, const char* lds, int r32, int hi, const bf16x8* qr, bf16x8 qx) {
;     p0 = f32x16{}; p1 = f32x16{};
;     const char* kb[4];
; #pragma unroll
;     for (int dd = 0; dd < 4; ++dd) kb[dd] = lds + OFF_K + KB * SHM_K + KSWZ(r32, (dd * 16 + hi * 8) * 2);
; #pragma unroll
;     for (int d0 = 0; d0 < 8; ++d0) { const char* a = kb[d0 & 3] + (d0 >> 2) * 128;
;         bf16x8 b0 = *reinterpret_cast<const bf16x8*>(a);
;         bf16x8 b1 = *reinterpret_cast<const bf16x8*>(a + 32 * 256);
;         p0 = __builtin_amdgcn_mfma_f32_32x32x16_bf16(b0, qr[d0], p0, 0, 0, 0);
;         p1 = __builtin_amdgcn_mfma_f32_32x32x16_bf16(b1, qr[d0], p1, 0, 0, 0); }
;     if (EXT) { const char* xa = lds + OFF_X + KB * SHM_X + r32 * 32 + hi * 16;
;         bf16x8 x0 = *reinterpret_cast<const bf16x8*>(xa), x1 = *reinterpret_cast<const bf16x8*>(xa + 32 * 32);
;         p0 = __builtin_amdgcn_mfma_f32_32x32x16_bf16(x0, qx, p0, 0, 0, 0);
;         p1 = __builtin_amdgcn_mfma_f32_32x32x16_bf16(x1, qx, p1, 0, 0, 0); }
; }
; template <int VB>
; __device__ __forceinline__ void pv_tile(f32x16* o, int vb0, bf16x8 pa0, bf16x8 pa1, bf16x8 pa2, bf16x8 pa3) {
;     ...
;     PV_D0(0); PV_D0(1); PV_D0(2); PV_D0(3);
	v_mfma_f32_32x32x16_bf16 v[66:81], v[164:167], v[130:133], v[66:81]
	v_add_f32_e32 v164, 0, v98
	v_add_f32_e32 v164, v99, v164
	v_add_f32_e32 v164, v100, v164
	v_add_f32_e32 v164, v101, v164
	v_add_f32_e32 v164, v102, v164
	v_add_f32_e32 v164, v103, v164
	v_add_f32_e32 v164, v104, v164
	v_add_f32_e32 v164, v105, v164
	v_add_f32_e32 v164, v106, v164
	v_add_f32_e32 v164, v107, v164
	v_add_f32_e32 v164, v108, v164
	v_add_f32_e32 v164, v109, v164
	v_add_f32_e32 v164, v110, v164
	v_add_f32_e32 v164, v111, v164
	v_add_f32_e32 v164, v112, v164
	v_add_f32_e32 v164, v113, v164
	v_add_f32_e32 v164, v114, v164
	v_add_f32_e32 v164, v115, v164
	v_add_f32_e32 v164, v116, v164
	v_add_f32_e32 v164, v117, v164
	v_add_f32_e32 v164, v118, v164
	v_add_f32_e32 v164, v119, v164
	v_add_f32_e32 v164, v120, v164
	v_add_f32_e32 v164, v121, v164
	v_add_f32_e32 v164, v122, v164
	v_add_f32_e32 v164, v123, v164
	s_waitcnt lgkmcnt(0)
	v_mfma_f32_32x32x16_bf16 v[82:97], v[168:171], v[130:133], v[82:97]
	v_add_f32_e32 v164, v124, v164
	v_add_f32_e32 v164, v125, v164
	v_add_f32_e32 v164, v126, v164
	v_add_f32_e32 v164, v127, v164
	v_add_f32_e32 v164, v128, v164
	v_add_f32_e32 v215, v129, v164
	v_mov_b32_e32 v216, v215
	v_cvt_pk_bf16_f32 v98, v98, v99
	v_cvt_pk_bf16_f32 v99, v100, v101
	v_cvt_pk_bf16_f32 v100, v102, v103
	s_nop 1
	v_permlane32_swap_b32_e32 v215, v216
	v_cvt_pk_bf16_f32 v101, v104, v105
	v_permlane32_swap_b32_e32 v98, v100
	v_cvt_pk_bf16_f32 v102, v106, v107
	v_cvt_pk_bf16_f32 v103, v108, v109
	v_cvt_pk_bf16_f32 v104, v110, v111
	v_cvt_pk_bf16_f32 v105, v112, v113
	v_cvt_pk_bf16_f32 v106, v114, v115
	v_cvt_pk_bf16_f32 v107, v116, v117
	v_cvt_pk_bf16_f32 v108, v118, v119
	v_cvt_pk_bf16_f32 v109, v120, v121
	v_cvt_pk_bf16_f32 v110, v122, v123
	v_cvt_pk_bf16_f32 v111, v124, v125
	v_cvt_pk_bf16_f32 v112, v126, v127
	v_cvt_pk_bf16_f32 v113, v128, v129
	v_permlane32_swap_b32_e32 v99, v101
	v_permlane32_swap_b32_e32 v102, v104
	v_permlane32_swap_b32_e32 v103, v105
	v_permlane32_swap_b32_e32 v106, v108
	v_permlane32_swap_b32_e32 v107, v109
	v_permlane32_swap_b32_e32 v110, v112
	v_permlane32_swap_b32_e32 v111, v113
	ds_read_b64_tr_b16 v[114:115], v194 offset:0
	ds_read_b64_tr_b16 v[116:117], v194 offset:0x800
	ds_read_b64_tr_b16 v[118:119], v194 offset:0x1000
	ds_read_b64_tr_b16 v[120:121], v194 offset:0x1800
	ds_read_b64_tr_b16 v[122:123], v194 offset:0x2000
	ds_read_b64_tr_b16 v[124:125], v194 offset:0x2800
	ds_read_b64_tr_b16 v[126:127], v194 offset:0x3000
	ds_read_b64_tr_b16 v[128:129], v194 offset:0x3800
	s_waitcnt lgkmcnt(0)
	s_nop 0
	v_mfma_f32_32x32x16_bf16 v[2:17], v[98:101], v[114:117], v[2:17]
	ds_read_b64_tr_b16 v[114:115], v194 offset:0x200
	ds_read_b64_tr_b16 v[116:117], v194 offset:0xa00
	v_mfma_f32_32x32x16_bf16 v[2:17], v[102:105], v[118:121], v[2:17]
	ds_read_b64_tr_b16 v[118:119], v194 offset:0x1200
	ds_read_b64_tr_b16 v[120:121], v194 offset:0x1a00
	v_mfma_f32_32x32x16_bf16 v[2:17], v[106:109], v[122:125], v[2:17]
	ds_read_b64_tr_b16 v[122:123], v194 offset:0x2200
	ds_read_b64_tr_b16 v[124:125], v194 offset:0x2a00
	v_mfma_f32_32x32x16_bf16 v[2:17], v[110:113], v[126:129], v[2:17]
	ds_read_b64_tr_b16 v[126:127], v194 offset:0x3200
	ds_read_b64_tr_b16 v[128:129], v194 offset:0x3a00
	s_waitcnt lgkmcnt(0)
	v_mfma_f32_32x32x16_bf16 v[50:65], v[98:101], v[114:117], v[50:65]
	ds_read_b64_tr_b16 v[114:115], v194 offset:0x400
	ds_read_b64_tr_b16 v[116:117], v194 offset:0xc00
	v_mfma_f32_32x32x16_bf16 v[50:65], v[102:105], v[118:121], v[50:65]
	ds_read_b64_tr_b16 v[118:119], v194 offset:0x1400
	ds_read_b64_tr_b16 v[120:121], v194 offset:0x1c00
	v_mfma_f32_32x32x16_bf16 v[50:65], v[106:109], v[122:125], v[50:65]
	ds_read_b64_tr_b16 v[122:123], v194 offset:0x2400
	ds_read_b64_tr_b16 v[124:125], v194 offset:0x2c00
	v_mfma_f32_32x32x16_bf16 v[50:65], v[110:113], v[126:129], v[50:65]
	ds_read_b64_tr_b16 v[126:127], v194 offset:0x3400
	ds_read_b64_tr_b16 v[128:129], v194 offset:0x3c00
	s_waitcnt lgkmcnt(0)
	v_mfma_f32_32x32x16_bf16 v[34:49], v[98:101], v[114:117], v[34:49]
	ds_read_b64_tr_b16 v[114:115], v194 offset:0x600
	ds_read_b64_tr_b16 v[116:117], v194 offset:0xe00
	v_mfma_f32_32x32x16_bf16 v[34:49], v[102:105], v[118:121], v[34:49]
	ds_read_b64_tr_b16 v[118:119], v194 offset:0x1600
	ds_read_b64_tr_b16 v[120:121], v194 offset:0x1e00
	v_mfma_f32_32x32x16_bf16 v[34:49], v[106:109], v[122:125], v[34:49]
	ds_read_b64_tr_b16 v[122:123], v194 offset:0x2600
	ds_read_b64_tr_b16 v[124:125], v194 offset:0x2e00
	v_mfma_f32_32x32x16_bf16 v[34:49], v[110:113], v[126:129], v[34:49]
	ds_read_b64_tr_b16 v[126:127], v194 offset:0x3600
	ds_read_b64_tr_b16 v[128:129], v194 offset:0x3e00
	s_waitcnt lgkmcnt(0)
	v_mfma_f32_32x32x16_bf16 v[18:33], v[98:101], v[114:117], v[18:33]
	s_waitcnt vmcnt(0)
	s_cmp_eq_u32 s99, 0
	s_cbranch_scc1 .Lstg_p1a
	s_barrier
; __device__ __forceinline__ void mask_bits(f32x16& p0, f32x16& p1, unsigned long long mw, int hi) {
;     const unsigned lo = (unsigned)mw >> (4 * hi), hw = (unsigned)(mw >> 32) >> (4 * hi);
; #pragma unroll
;     for (int r = 0; r < 16; ++r) { const int c = (r & 3) + 8 * (r >> 2);
;         const unsigned t0 = (unsigned)((int)(lo << (31 - c)) >> 31), t1 = (unsigned)((int)(hw << (31 - c)) >> 31);
;         p0[r] = __uint_as_float(__builtin_amdgcn_bitop3_b32(__float_as_uint(p0[r]), 0xFF800000u, t0, 0xe4));
;         p1[r] = __uint_as_float(__builtin_amdgcn_bitop3_b32(__float_as_uint(p1[r]), 0xFF800000u, t1, 0xe4)); }
; }
; __device__ __forceinline__ void partialSM(f32x16& p0, f32x16& p1, float& m_reg, float& mn, float& alpha) {
;     float pmax = p0[0]; for (int r = 1; r < 16; ++r) pmax = fmaxf(pmax, p0[r]); for (int r = 0; r < 16; ++r) pmax = fmaxf(pmax, p1[r]);
;     { auto rr = __builtin_amdgcn_permlane32_swap(__float_as_uint(pmax), __float_as_uint(pmax), false, false);
;       pmax = fmaxf(__uint_as_float(rr[0]), __uint_as_float(rr[1])); }
;     constexpr float C2 = 1.4426950408889634f * SCALE;
;     if (__builtin_expect(__all((pmax - m_reg) * SCALE <= THR), 1)) { mn = m_reg; alpha = 1.f; }
;     else { mn = fmaxf(m_reg, pmax); alpha = __builtin_amdgcn_exp2f((m_reg - mn) * C2); m_reg = mn; }
;     const float mnL = -mn * C2;
;     for (int r = 0; r < 16; ++r) p0[r] = fmaf(p0[r], C2, mnL); for (int r = 0; r < 16; ++r) p1[r] = fmaf(p1[r], C2, mnL);
;     for (int r = 0; r < 16; ++r) p0[r] = __builtin_amdgcn_exp2f(p0[r]);
; }
.Lstg_p1a:
	v_lshrrev_b32_e32 v99, v193, v162
	v_lshrrev_b32_e32 v100, v193, v163
	v_bfe_i32 v98, v99, 0, 1
	v_bfe_i32 v101, v100, 0, 1
	v_bitop3_b32 v66, v66, s52, v98 bitop3:0xe4
	v_bitop3_b32 v82, v82, s52, v101 bitop3:0xe4
	v_bfe_i32 v98, v99, 1, 1
	v_bfe_i32 v101, v100, 1, 1
	v_bitop3_b32 v67, v67, s52, v98 bitop3:0xe4
	v_bitop3_b32 v83, v83, s52, v101 bitop3:0xe4
	v_bfe_i32 v98, v99, 2, 1
	v_bfe_i32 v101, v100, 2, 1
	v_bitop3_b32 v68, v68, s52, v98 bitop3:0xe4
	v_bitop3_b32 v84, v84, s52, v101 bitop3:0xe4
	v_bfe_i32 v98, v99, 3, 1
	v_bfe_i32 v101, v100, 3, 1
	v_bitop3_b32 v69, v69, s52, v98 bitop3:0xe4
	v_bitop3_b32 v85, v85, s52, v101 bitop3:0xe4
	v_bfe_i32 v98, v99, 8, 1
	v_bfe_i32 v101, v100, 8, 1
	v_bitop3_b32 v70, v70, s52, v98 bitop3:0xe4
	v_bitop3_b32 v86, v86, s52, v101 bitop3:0xe4
	v_bfe_i32 v98, v99, 9, 1
	v_bfe_i32 v101, v100, 9, 1
	v_bitop3_b32 v71, v71, s52, v98 bitop3:0xe4
	v_bitop3_b32 v87, v87, s52, v101 bitop3:0xe4
	v_bfe_i32 v98, v99, 10, 1
	v_bfe_i32 v101, v100, 10, 1
	v_bitop3_b32 v72, v72, s52, v98 bitop3:0xe4
	v_bitop3_b32 v88, v88, s52, v101 bitop3:0xe4
	v_bfe_i32 v98, v99, 11, 1
	v_bfe_i32 v101, v100, 11, 1
	v_bitop3_b32 v73, v73, s52, v98 bitop3:0xe4
	v_bitop3_b32 v89, v89, s52, v101 bitop3:0xe4
	v_bfe_i32 v98, v99, 16, 1
	v_bfe_i32 v101, v100, 16, 1
	v_bitop3_b32 v74, v74, s52, v98 bitop3:0xe4
	v_bitop3_b32 v90, v90, s52, v101 bitop3:0xe4
	v_bfe_i32 v98, v99, 17, 1
	v_bfe_i32 v101, v100, 17, 1
	v_bitop3_b32 v75, v75, s52, v98 bitop3:0xe4
	v_bitop3_b32 v91, v91, s52, v101 bitop3:0xe4
	v_bfe_i32 v98, v99, 18, 1
	v_bfe_i32 v101, v100, 18, 1
	v_bitop3_b32 v76, v76, s52, v98 bitop3:0xe4
	v_bitop3_b32 v92, v92, s52, v101 bitop3:0xe4
	v_bfe_i32 v98, v99, 19, 1
	v_bfe_i32 v101, v100, 19, 1
	v_bitop3_b32 v77, v77, s52, v98 bitop3:0xe4
	v_bitop3_b32 v93, v93, s52, v101 bitop3:0xe4
	v_bfe_i32 v98, v99, 24, 1
	v_bfe_i32 v101, v100, 24, 1
	v_bitop3_b32 v78, v78, s52, v98 bitop3:0xe4
	v_bitop3_b32 v94, v94, s52, v101 bitop3:0xe4
	v_bfe_i32 v98, v99, 25, 1
	v_bfe_i32 v101, v100, 25, 1
	v_bitop3_b32 v79, v79, s52, v98 bitop3:0xe4
	v_bitop3_b32 v95, v95, s52, v101 bitop3:0xe4
	v_bfe_i32 v98, v99, 26, 1
	v_bfe_i32 v101, v100, 26, 1
	v_bitop3_b32 v98, v80, s52, v98 bitop3:0xe4
	v_bitop3_b32 v80, v96, s52, v101 bitop3:0xe4
	v_bfe_i32 v96, v99, 27, 1
	v_bfe_i32 v99, v100, 27, 1
	v_bitop3_b32 v96, v81, s52, v96 bitop3:0xe4
	v_bitop3_b32 v81, v97, s52, v99 bitop3:0xe4
	v_max_f32_e32 v97, v67, v67
	v_max_f32_e32 v99, v66, v66
	v_max_f32_e32 v97, v99, v97
	v_max3_f32 v97, v97, v68, v69
	v_max3_f32 v97, v97, v70, v71
	v_max3_f32 v97, v97, v72, v73
	v_max3_f32 v97, v97, v74, v75
	v_max3_f32 v97, v97, v76, v77
	v_max3_f32 v97, v97, v78, v79
	v_max3_f32 v97, v97, v98, v96
	v_mfma_f32_32x32x16_bf16 v[18:33], v[102:105], v[118:121], v[18:33]
	v_max3_f32 v97, v97, v82, v83
	v_max3_f32 v97, v97, v84, v85
	v_max3_f32 v97, v97, v86, v87
	v_max3_f32 v97, v97, v88, v89
	v_max3_f32 v97, v97, v90, v91
	v_max3_f32 v97, v97, v92, v93
	v_max3_f32 v97, v97, v94, v95
	v_max3_f32 v97, v97, v80, v81
	v_mfma_f32_32x32x16_bf16 v[18:33], v[106:109], v[122:125], v[18:33]
	v_mov_b32_e32 v99, v97
	s_nop 1
	v_permlane32_swap_b32_e32 v97, v99
	v_max_f32_e32 v99, v99, v99
	v_max_f32_e32 v97, v97, v97
	v_max_f32_e32 v97, v97, v99
	v_sub_f32_e32 v99, v97, v180
	v_mul_f32_e32 v99, 0x3db504f3, v99
	v_cmp_ge_f32_e32 vcc, s53, v99
	v_max_f32_e32 v99, v180, v180
	v_max_f32_e32 v97, v99, v97
	v_mfma_f32_32x32x16_bf16 v[18:33], v[110:113], v[126:129], v[18:33]
	v_sub_f32_e32 v99, v180, v97
	v_mul_f32_e32 v99, 0x3e0293ee, v99
	v_exp_f32_e32 v99, v99
	s_cmp_eq_u64 vcc, exec
	s_cselect_b64 s[4:5], -1, 0
	v_cndmask_b32_e64 v195, v99, 1.0, s[4:5]
	v_cmp_gt_f32_e32 vcc, 1.0, v195
	s_cbranch_vccz .LBB0_1165
	s_and_saveexec_b64 s[24:25], s[2:3]
	ds_write_b32 v208, v195 offset:128
	s_or_b64 exec, exec, s[24:25]
	s_waitcnt lgkmcnt(0)
	ds_read_b128 v[100:103], v209 offset:224
	ds_read_b128 v[104:107], v209 offset:192
	ds_read_b128 v[108:111], v209 offset:160
	ds_read_b128 v[112:115], v209 offset:128
	v_readlane_b32 s79, v241, 49
	s_waitcnt lgkmcnt(3)
	v_pk_mul_f32 v[16:17], v[16:17], v[102:103]
	s_waitcnt lgkmcnt(2)
	v_pk_mul_f32 v[12:13], v[12:13], v[106:107]
	s_waitcnt lgkmcnt(1)
	v_pk_mul_f32 v[8:9], v[8:9], v[110:111]
	s_waitcnt lgkmcnt(0)
	v_pk_mul_f32 v[4:5], v[4:5], v[114:115]
	v_pk_mul_f32 v[14:15], v[14:15], v[100:101]
	v_pk_mul_f32 v[10:11], v[10:11], v[104:105]
	v_pk_mul_f32 v[6:7], v[6:7], v[108:109]
	v_pk_mul_f32 v[2:3], v[2:3], v[112:113]
	v_pk_mul_f32 v[64:65], v[64:65], v[102:103]
	v_pk_mul_f32 v[60:61], v[60:61], v[106:107]
	v_pk_mul_f32 v[56:57], v[56:57], v[110:111]
	v_pk_mul_f32 v[52:53], v[52:53], v[114:115]
	v_pk_mul_f32 v[62:63], v[62:63], v[100:101]
	v_pk_mul_f32 v[58:59], v[58:59], v[104:105]
	v_pk_mul_f32 v[54:55], v[54:55], v[108:109]
	v_pk_mul_f32 v[50:51], v[50:51], v[112:113]
	v_pk_mul_f32 v[48:49], v[48:49], v[102:103]
	v_pk_mul_f32 v[44:45], v[44:45], v[106:107]
	v_pk_mul_f32 v[40:41], v[40:41], v[110:111]
	v_pk_mul_f32 v[36:37], v[36:37], v[114:115]
	v_pk_mul_f32 v[46:47], v[46:47], v[100:101]
	v_pk_mul_f32 v[42:43], v[42:43], v[104:105]
	v_pk_mul_f32 v[38:39], v[38:39], v[108:109]
	v_pk_mul_f32 v[34:35], v[34:35], v[112:113]
	v_pk_mul_f32 v[32:33], v[32:33], v[102:103]
	v_pk_mul_f32 v[28:29], v[28:29], v[106:107]
	v_pk_mul_f32 v[24:25], v[24:25], v[110:111]
	v_pk_mul_f32 v[20:21], v[20:21], v[114:115]
	v_pk_mul_f32 v[30:31], v[30:31], v[100:101]
	v_pk_mul_f32 v[26:27], v[26:27], v[104:105]
	v_pk_mul_f32 v[22:23], v[22:23], v[108:109]
	v_pk_mul_f32 v[18:19], v[18:19], v[112:113]
.LBB0_1165:
	s_cmp_lg_u32 s99, 0
	s_cbranch_scc1 .Lstg_e1
	s_waitcnt vmcnt(0)
	s_barrier
; __device__ __forceinline__ void partialSM(f32x16& p0, f32x16& p1, float& m_reg, float& mn, float& alpha) {
;     float pmax = p0[0]; for (int r = 1; r < 16; ++r) pmax = fmaxf(pmax, p0[r]); for (int r = 0; r < 16; ++r) pmax = fmaxf(pmax, p1[r]);
;     { auto rr = __builtin_amdgcn_permlane32_swap(__float_as_uint(pmax), __float_as_uint(pmax), false, false);
;       pmax = fmaxf(__uint_as_float(rr[0]), __uint_as_float(rr[1])); }
;     constexpr float C2 = 1.4426950408889634f * SCALE;
;     if (__builtin_expect(__all((pmax - m_reg) * SCALE <= THR), 1)) { mn = m_reg; alpha = 1.f; }
;     else { mn = fmaxf(m_reg, pmax); alpha = __builtin_amdgcn_exp2f((m_reg - mn) * C2); m_reg = mn; }
;     const float mnL = -mn * C2;
;     for (int r = 0; r < 16; ++r) p0[r] = fmaf(p0[r], C2, mnL); for (int r = 0; r < 16; ++r) p1[r] = fmaf(p1[r], C2, mnL);
;     for (int r = 0; r < 16; ++r) p0[r] = __builtin_amdgcn_exp2f(p0[r]);
; }
; __device__ __forceinline__ void finishSM(f32x16& p0, f32x16& p1, float alpha, float& l_reg, bf16x8& pa0, bf16x8& pa1, bf16x8& pa2, bf16x8& pa3) {
;     for (int r = 0; r < 16; ++r) p1[r] = __builtin_amdgcn_exp2f(p1[r]);
;     float ps = 0; for (int r = 0; r < 16; ++r) ps += p0[r]; for (int r = 0; r < 16; ++r) ps += p1[r];
;     { auto rr = __builtin_amdgcn_permlane32_swap(__float_as_uint(ps), __float_as_uint(ps), false, false);
;       ps = __uint_as_float(rr[0]) + __uint_as_float(rr[1]); }
;     l_reg = l_reg * alpha + ps;
;     ...
;     PK4(p0, 0, pa0); PK4(p0, 8, pa1); PK4(p1, 0, pa2); PK4(p1, 8, pa3);
;     ...
; }
; template <int KB, bool EXT>
; __device__ __forceinline__ void qkt(f32x16& p0, f32x16& p1, const char* lds, int r32, int hi, const bf16x8* qr, bf16x8 qx) {
;     p0 = f32x16{}; p1 = f32x16{};
;     const char* kb[4];
; #pragma unroll
;     for (int dd = 0; dd < 4; ++dd) kb[dd] = lds + OFF_K + KB * SHM_K + KSWZ(r32, (dd * 16 + hi * 8) * 2);
; #pragma unroll
;     for (int d0 = 0; d0 < 8; ++d0) { const char* a = kb[d0 & 3] + (d0 >> 2) * 128;
;         bf16x8 b0 = *reinterpret_cast<const bf16x8*>(a);
;         bf16x8 b1 = *reinterpret_cast<const bf16x8*>(a + 32 * 256);
;         p0 = __builtin_amdgcn_mfma_f32_32x32x16_bf16(b0, qr[d0], p0, 0, 0, 0);
;         p1 = __builtin_amdgcn_mfma_f32_32x32x16_bf16(b1, qr[d0], p1, 0, 0, 0); }
.Lstg_e1:
	global_load_dwordx2 v[184:185], v[182:183], off
	s_add_i32 s24, s61, s74
	s_add_i32 s24, s24, 3
	s_cmp_ge_u32 s24, s69
	s_cbranch_scc1 .LBB0_1167
	s_add_u32 s24, s76, 0xc000
	s_addc_u32 s25, s77, 0
	s_mov_b32 s76, m0
	s_mov_b32 m0, s66
	s_nop 0
	global_load_lds_dwordx4 v204, s[24:25]
	s_mov_b32 m0, s76
	s_nop 0
	s_mov_b32 s76, m0
	s_mov_b32 m0, s67
	s_nop 0
	global_load_lds_dwordx4 v205, s[24:25]
	s_mov_b32 m0, s76
.LBB0_1167:
	v_cndmask_b32_e64 v180, v97, v180, s[4:5]
	v_mul_f32_e32 v97, 0xbe0293ee, v180
	v_fmamk_f32 v66, v66, 0x3e0293ee, v97
	v_fmamk_f32 v67, v67, 0x3e0293ee, v97
	v_fmamk_f32 v68, v68, 0x3e0293ee, v97
	v_fmamk_f32 v69, v69, 0x3e0293ee, v97
	v_fmamk_f32 v70, v70, 0x3e0293ee, v97
	v_fmamk_f32 v71, v71, 0x3e0293ee, v97
	v_fmamk_f32 v72, v72, 0x3e0293ee, v97
	v_fmamk_f32 v73, v73, 0x3e0293ee, v97
	v_fmamk_f32 v74, v74, 0x3e0293ee, v97
	v_fmamk_f32 v75, v75, 0x3e0293ee, v97
	v_fmamk_f32 v76, v76, 0x3e0293ee, v97
	v_fmamk_f32 v77, v77, 0x3e0293ee, v97
	v_fmamk_f32 v78, v78, 0x3e0293ee, v97
	v_fmamk_f32 v79, v79, 0x3e0293ee, v97
	v_fmamk_f32 v98, v98, 0x3e0293ee, v97
	v_fmamk_f32 v96, v96, 0x3e0293ee, v97
	s_add_u32 s4, s26, 0x8000
	v_fmamk_f32 v162, v82, 0x3e0293ee, v97
	v_fmamk_f32 v163, v83, 0x3e0293ee, v97
	v_fmamk_f32 v164, v84, 0x3e0293ee, v97
	v_fmamk_f32 v165, v85, 0x3e0293ee, v97
	v_fmamk_f32 v166, v86, 0x3e0293ee, v97
	v_fmamk_f32 v167, v87, 0x3e0293ee, v97
	v_fmamk_f32 v168, v88, 0x3e0293ee, v97
	v_fmamk_f32 v169, v89, 0x3e0293ee, v97
	v_fmamk_f32 v90, v90, 0x3e0293ee, v97
	v_fmamk_f32 v91, v91, 0x3e0293ee, v97
	v_fmamk_f32 v92, v92, 0x3e0293ee, v97
	v_fmamk_f32 v93, v93, 0x3e0293ee, v97
	v_fmamk_f32 v94, v94, 0x3e0293ee, v97
	v_fmamk_f32 v95, v95, 0x3e0293ee, v97
	v_fmamk_f32 v170, v80, 0x3e0293ee, v97
	v_fmac_f32_e32 v97, 0x3e0293ee, v81
	v_exp_f32_e32 v66, v66
	v_exp_f32_e32 v67, v67
	v_exp_f32_e32 v68, v68
	v_exp_f32_e32 v69, v69
	v_exp_f32_e32 v70, v70
	v_exp_f32_e32 v71, v71
	v_exp_f32_e32 v72, v72
	v_exp_f32_e32 v73, v73
	v_exp_f32_e32 v74, v74
	v_exp_f32_e32 v75, v75
	v_exp_f32_e32 v76, v76
	v_exp_f32_e32 v77, v77
	v_exp_f32_e32 v78, v78
	v_exp_f32_e32 v79, v79
	v_exp_f32_e32 v80, v98
	v_exp_f32_e32 v81, v96
	s_addc_u32 s5, s27, 0
	s_mov_b32 s24, m0
	s_mov_b32 m0, s63
	s_nop 0
	global_load_lds_dwordx4 v196, s[4:5]
	s_mov_b32 m0, s24
	s_nop 0
	s_mov_b32 s24, m0
	s_mov_b32 m0, s68
	s_nop 0
	global_load_lds_dwordx4 v197, s[4:5]
	s_mov_b32 m0, s24
	ds_read_b128 v[82:85], v210 offset:32768
	ds_read_b128 v[86:89], v210 offset:40960
	v_exp_f32_e32 v90, v90
	v_exp_f32_e32 v91, v91
	v_exp_f32_e32 v92, v92
	s_waitcnt lgkmcnt(1)
	v_mfma_f32_32x32x16_bf16 v[98:113], v[82:85], v[146:149], 0
	v_exp_f32_e32 v93, v93
	v_exp_f32_e32 v94, v94
	v_exp_f32_e32 v95, v95
	v_exp_f32_e32 v96, v170
	v_exp_f32_e32 v97, v97
	s_waitcnt lgkmcnt(0)
	v_mfma_f32_32x32x16_bf16 v[114:129], v[86:89], v[146:149], 0
	ds_read_b128 v[82:85], v211 offset:32768
	ds_read_b128 v[86:89], v211 offset:40960
	s_waitcnt lgkmcnt(1)
	v_mfma_f32_32x32x16_bf16 v[98:113], v[82:85], v[150:153], v[98:113]
	s_waitcnt lgkmcnt(0)
	v_mfma_f32_32x32x16_bf16 v[114:129], v[86:89], v[150:153], v[114:129]
	ds_read_b128 v[82:85], v212 offset:32768
	ds_read_b128 v[86:89], v212 offset:40960
	s_waitcnt lgkmcnt(1)
	v_mfma_f32_32x32x16_bf16 v[98:113], v[82:85], v[154:157], v[98:113]
	s_waitcnt lgkmcnt(0)
	v_mfma_f32_32x32x16_bf16 v[114:129], v[86:89], v[154:157], v[114:129]
	ds_read_b128 v[82:85], v213 offset:32768
	ds_read_b128 v[86:89], v213 offset:40960
	s_waitcnt lgkmcnt(1)
	v_mfma_f32_32x32x16_bf16 v[98:113], v[82:85], v[158:161], v[98:113]
	s_waitcnt lgkmcnt(0)
	v_mfma_f32_32x32x16_bf16 v[114:129], v[86:89], v[158:161], v[114:129]
	ds_read_b128 v[82:85], v210 offset:32896
	ds_read_b128 v[86:89], v210 offset:41088
	s_waitcnt lgkmcnt(1)
	v_mfma_f32_32x32x16_bf16 v[98:113], v[82:85], v[142:145], v[98:113]
	s_waitcnt lgkmcnt(0)
	v_mfma_f32_32x32x16_bf16 v[114:129], v[86:89], v[142:145], v[114:129]
	ds_read_b128 v[82:85], v211 offset:32896
	ds_read_b128 v[86:89], v211 offset:41088
	s_waitcnt lgkmcnt(1)
	v_mfma_f32_32x32x16_bf16 v[98:113], v[82:85], v[138:141], v[98:113]
	s_waitcnt lgkmcnt(0)
	v_mfma_f32_32x32x16_bf16 v[114:129], v[86:89], v[138:141], v[114:129]
	ds_read_b128 v[82:85], v212 offset:32896
	ds_read_b128 v[86:89], v212 offset:41088
	s_waitcnt lgkmcnt(1)
	v_mfma_f32_32x32x16_bf16 v[98:113], v[82:85], v[134:137], v[98:113]
	s_waitcnt lgkmcnt(0)
	v_mfma_f32_32x32x16_bf16 v[114:129], v[86:89], v[134:137], v[114:129]
	ds_read_b128 v[82:85], v213 offset:32896
	ds_read_b128 v[86:89], v213 offset:41088
	s_waitcnt lgkmcnt(1)
	v_mfma_f32_32x32x16_bf16 v[98:113], v[82:85], v[130:133], v[98:113]
	v_exp_f32_e32 v82, v162
	v_add_f32_e32 v162, 0, v66
	v_add_f32_e32 v162, v67, v162
	v_add_f32_e32 v162, v68, v162
	v_add_f32_e32 v162, v69, v162
	v_add_f32_e32 v162, v70, v162
	v_add_f32_e32 v162, v71, v162
	v_add_f32_e32 v162, v72, v162
	v_add_f32_e32 v162, v73, v162
	v_add_f32_e32 v162, v74, v162
	v_add_f32_e32 v162, v75, v162
	v_add_f32_e32 v162, v76, v162
	v_add_f32_e32 v162, v77, v162
	v_add_f32_e32 v162, v78, v162
	v_exp_f32_e32 v83, v163
	v_add_f32_e32 v162, v79, v162
	v_exp_f32_e32 v84, v164
	v_add_f32_e32 v162, v80, v162
	v_exp_f32_e32 v85, v165
	v_add_f32_e32 v162, v81, v162
	s_waitcnt lgkmcnt(0)
; __device__ __forceinline__ void finishSM(f32x16& p0, f32x16& p1, float alpha, float& l_reg, bf16x8& pa0, bf16x8& pa1, bf16x8& pa2, bf16x8& pa3) {
;     for (int r = 0; r < 16; ++r) p1[r] = __builtin_amdgcn_exp2f(p1[r]);
;     float ps = 0; for (int r = 0; r < 16; ++r) ps += p0[r]; for (int r = 0; r < 16; ++r) ps += p1[r];
;     { auto rr = __builtin_amdgcn_permlane32_swap(__float_as_uint(ps), __float_as_uint(ps), false, false);
;       ps = __uint_as_float(rr[0]) + __uint_as_float(rr[1]); }
;     l_reg = l_reg * alpha + ps;
;     ...
;     PK4(p0, 0, pa0); PK4(p0, 8, pa1); PK4(p1, 0, pa2); PK4(p1, 8, pa3);
;     ...
; }
; template <int KB, bool EXT>
; __device__ __forceinline__ void qkt(f32x16& p0, f32x16& p1, const char* lds, int r32, int hi, const bf16x8* qr, bf16x8 qx) {
;     p0 = f32x16{}; p1 = f32x16{};
;     const char* kb[4];
; #pragma unroll
;     for (int dd = 0; dd < 4; ++dd) kb[dd] = lds + OFF_K + KB * SHM_K + KSWZ(r32, (dd * 16 + hi * 8) * 2);
; #pragma unroll
;     for (int d0 = 0; d0 < 8; ++d0) { const char* a = kb[d0 & 3] + (d0 >> 2) * 128;
;         bf16x8 b0 = *reinterpret_cast<const bf16x8*>(a);
;         bf16x8 b1 = *reinterpret_cast<const bf16x8*>(a + 32 * 256);
;         p0 = __builtin_amdgcn_mfma_f32_32x32x16_bf16(b0, qr[d0], p0, 0, 0, 0);
;         p1 = __builtin_amdgcn_mfma_f32_32x32x16_bf16(b1, qr[d0], p1, 0, 0, 0); }
;     if (EXT) { const char* xa = lds + OFF_X + KB * SHM_X + r32 * 32 + hi * 16;
;         bf16x8 x0 = *reinterpret_cast<const bf16x8*>(xa), x1 = *reinterpret_cast<const bf16x8*>(xa + 32 * 32);
;         p0 = __builtin_amdgcn_mfma_f32_32x32x16_bf16(x0, qx, p0, 0, 0, 0);
;         p1 = __builtin_amdgcn_mfma_f32_32x32x16_bf16(x1, qx, p1, 0, 0, 0); }
; }
; template <int VB>
; __device__ __forceinline__ void pv_tile(f32x16* o, int vb0, bf16x8 pa0, bf16x8 pa1, bf16x8 pa2, bf16x8 pa3) {
;     ...
;     PV_D0(0); PV_D0(1); PV_D0(2); PV_D0(3);
	v_mfma_f32_32x32x16_bf16 v[114:129], v[86:89], v[130:133], v[114:129]
	v_exp_f32_e32 v86, v166
	v_add_f32_e32 v162, v82, v162
	v_exp_f32_e32 v87, v167
	v_add_f32_e32 v162, v83, v162
	v_exp_f32_e32 v88, v168
	v_add_f32_e32 v162, v84, v162
	v_exp_f32_e32 v89, v169
	v_add_f32_e32 v162, v85, v162
	v_add_f32_e32 v162, v86, v162
	v_add_f32_e32 v162, v87, v162
	v_add_f32_e32 v162, v88, v162
	v_add_f32_e32 v162, v89, v162
	v_add_f32_e32 v162, v90, v162
	v_add_f32_e32 v162, v91, v162
	v_add_f32_e32 v162, v92, v162
	v_add_f32_e32 v162, v93, v162
	v_add_f32_e32 v162, v94, v162
	v_add_f32_e32 v162, v95, v162
	v_add_f32_e32 v162, v96, v162
	v_add_f32_e32 v217, v97, v162
	v_mov_b32_e32 v218, v217
	v_cvt_pk_bf16_f32 v162, v66, v67
	v_cvt_pk_bf16_f32 v163, v68, v69
	v_cvt_pk_bf16_f32 v164, v70, v71
	v_cvt_pk_bf16_f32 v165, v72, v73
	v_cvt_pk_bf16_f32 v166, v74, v75
	v_cvt_pk_bf16_f32 v167, v76, v77
	v_cvt_pk_bf16_f32 v168, v78, v79
	v_cvt_pk_bf16_f32 v169, v80, v81
	v_cvt_pk_bf16_f32 v170, v82, v83
	v_cvt_pk_bf16_f32 v171, v84, v85
	v_cvt_pk_bf16_f32 v172, v86, v87
	v_cvt_pk_bf16_f32 v173, v88, v89
	v_cvt_pk_bf16_f32 v174, v90, v91
	v_cvt_pk_bf16_f32 v175, v92, v93
	v_cvt_pk_bf16_f32 v176, v94, v95
	v_cvt_pk_bf16_f32 v177, v96, v97
	s_nop 1
	v_permlane32_swap_b32_e32 v217, v218
	v_permlane32_swap_b32_e32 v162, v164
	v_permlane32_swap_b32_e32 v163, v165
	v_permlane32_swap_b32_e32 v166, v168
	v_permlane32_swap_b32_e32 v167, v169
	v_permlane32_swap_b32_e32 v170, v172
	v_permlane32_swap_b32_e32 v171, v173
	v_permlane32_swap_b32_e32 v174, v176
	v_permlane32_swap_b32_e32 v175, v177
	ds_read_b64_tr_b16 v[222:223], v194 offset:0x4000
	ds_read_b64_tr_b16 v[224:225], v194 offset:0x4800
	ds_read_b64_tr_b16 v[226:227], v194 offset:0x5000
	ds_read_b64_tr_b16 v[228:229], v194 offset:0x5800
	ds_read_b64_tr_b16 v[230:231], v194 offset:0x6000
	ds_read_b64_tr_b16 v[232:233], v194 offset:0x6800
	ds_read_b64_tr_b16 v[234:235], v194 offset:0x7000
	ds_read_b64_tr_b16 v[236:237], v194 offset:0x7800
	s_waitcnt lgkmcnt(0)
	s_nop 0
	v_mfma_f32_32x32x16_bf16 v[2:17], v[162:165], v[222:225], v[2:17]
	ds_read_b64_tr_b16 v[222:223], v194 offset:0x4200
	ds_read_b64_tr_b16 v[224:225], v194 offset:0x4a00
	v_mfma_f32_32x32x16_bf16 v[2:17], v[166:169], v[226:229], v[2:17]
	ds_read_b64_tr_b16 v[226:227], v194 offset:0x5200
	ds_read_b64_tr_b16 v[228:229], v194 offset:0x5a00
	v_mfma_f32_32x32x16_bf16 v[2:17], v[170:173], v[230:233], v[2:17]
	ds_read_b64_tr_b16 v[230:231], v194 offset:0x6200
	ds_read_b64_tr_b16 v[232:233], v194 offset:0x6a00
	v_mfma_f32_32x32x16_bf16 v[2:17], v[174:177], v[234:237], v[2:17]
	ds_read_b64_tr_b16 v[234:235], v194 offset:0x7200
	ds_read_b64_tr_b16 v[236:237], v194 offset:0x7a00
	s_waitcnt lgkmcnt(0)
	v_mfma_f32_32x32x16_bf16 v[50:65], v[162:165], v[222:225], v[50:65]
	ds_read_b64_tr_b16 v[222:223], v194 offset:0x4400
	ds_read_b64_tr_b16 v[224:225], v194 offset:0x4c00
	v_mfma_f32_32x32x16_bf16 v[50:65], v[166:169], v[226:229], v[50:65]
	ds_read_b64_tr_b16 v[226:227], v194 offset:0x5400
	ds_read_b64_tr_b16 v[228:229], v194 offset:0x5c00
	v_mfma_f32_32x32x16_bf16 v[50:65], v[170:173], v[230:233], v[50:65]
	ds_read_b64_tr_b16 v[230:231], v194 offset:0x6400
	ds_read_b64_tr_b16 v[232:233], v194 offset:0x6c00
	v_mfma_f32_32x32x16_bf16 v[50:65], v[174:177], v[234:237], v[50:65]
	ds_read_b64_tr_b16 v[234:235], v194 offset:0x7400
	ds_read_b64_tr_b16 v[236:237], v194 offset:0x7c00
	s_waitcnt lgkmcnt(0)
	v_mfma_f32_32x32x16_bf16 v[34:49], v[162:165], v[222:225], v[34:49]
	ds_read_b64_tr_b16 v[222:223], v194 offset:0x4600
	ds_read_b64_tr_b16 v[224:225], v194 offset:0x4e00
	v_mfma_f32_32x32x16_bf16 v[34:49], v[166:169], v[226:229], v[34:49]
	ds_read_b64_tr_b16 v[226:227], v194 offset:0x5600
	ds_read_b64_tr_b16 v[228:229], v194 offset:0x5e00
	v_mfma_f32_32x32x16_bf16 v[34:49], v[170:173], v[230:233], v[34:49]
	ds_read_b64_tr_b16 v[230:231], v194 offset:0x6600
	ds_read_b64_tr_b16 v[232:233], v194 offset:0x6e00
	v_mfma_f32_32x32x16_bf16 v[34:49], v[174:177], v[234:237], v[34:49]
	ds_read_b64_tr_b16 v[234:235], v194 offset:0x7600
	ds_read_b64_tr_b16 v[236:237], v194 offset:0x7e00
	s_waitcnt lgkmcnt(0)
	s_waitcnt vmcnt(0)
	s_cmp_eq_u32 s99, 0
	s_cbranch_scc1 .Lstg_p1b
	s_barrier
; __device__ __forceinline__ void mask_bits(f32x16& p0, f32x16& p1, unsigned long long mw, int hi) {
;     const unsigned lo = (unsigned)mw >> (4 * hi), hw = (unsigned)(mw >> 32) >> (4 * hi);
; #pragma unroll
;     for (int r = 0; r < 16; ++r) { const int c = (r & 3) + 8 * (r >> 2);
;         const unsigned t0 = (unsigned)((int)(lo << (31 - c)) >> 31), t1 = (unsigned)((int)(hw << (31 - c)) >> 31);
;         p0[r] = __uint_as_float(__builtin_amdgcn_bitop3_b32(__float_as_uint(p0[r]), 0xFF800000u, t0, 0xe4));
;         p1[r] = __uint_as_float(__builtin_amdgcn_bitop3_b32(__float_as_uint(p1[r]), 0xFF800000u, t1, 0xe4)); }
; }
; __device__ __forceinline__ void partialSM(f32x16& p0, f32x16& p1, float& m_reg, float& mn, float& alpha) {
;     float pmax = p0[0]; for (int r = 1; r < 16; ++r) pmax = fmaxf(pmax, p0[r]); for (int r = 0; r < 16; ++r) pmax = fmaxf(pmax, p1[r]);
;     { auto rr = __builtin_amdgcn_permlane32_swap(__float_as_uint(pmax), __float_as_uint(pmax), false, false);
;       pmax = fmaxf(__uint_as_float(rr[0]), __uint_as_float(rr[1])); }
;     constexpr float C2 = 1.4426950408889634f * SCALE;
;     if (__builtin_expect(__all((pmax - m_reg) * SCALE <= THR), 1)) { mn = m_reg; alpha = 1.f; }
;     else { mn = fmaxf(m_reg, pmax); alpha = __builtin_amdgcn_exp2f((m_reg - mn) * C2); m_reg = mn; }
;     const float mnL = -mn * C2;
;     for (int r = 0; r < 16; ++r) p0[r] = fmaf(p0[r], C2, mnL); for (int r = 0; r < 16; ++r) p1[r] = fmaf(p1[r], C2, mnL);
;     for (int r = 0; r < 16; ++r) p0[r] = __builtin_amdgcn_exp2f(p0[r]);
; }
.Lstg_p1b:
	v_lshrrev_b32_e32 v206, v193, v184
	v_lshrrev_b32_e32 v185, v193, v185
	v_bfe_i32 v184, v206, 0, 1
	v_bfe_i32 v219, v185, 0, 1
	v_bitop3_b32 v98, v98, s52, v184 bitop3:0xe4
	v_bitop3_b32 v114, v114, s52, v219 bitop3:0xe4
	v_bfe_i32 v184, v206, 1, 1
	v_bfe_i32 v219, v185, 1, 1
	v_bitop3_b32 v99, v99, s52, v184 bitop3:0xe4
	v_bitop3_b32 v115, v115, s52, v219 bitop3:0xe4
	v_bfe_i32 v184, v206, 2, 1
	v_bfe_i32 v219, v185, 2, 1
	v_bitop3_b32 v100, v100, s52, v184 bitop3:0xe4
	v_bitop3_b32 v116, v116, s52, v219 bitop3:0xe4
	v_bfe_i32 v184, v206, 3, 1
	v_bfe_i32 v219, v185, 3, 1
	v_bitop3_b32 v101, v101, s52, v184 bitop3:0xe4
	v_bitop3_b32 v117, v117, s52, v219 bitop3:0xe4
	v_bfe_i32 v184, v206, 8, 1
	v_bfe_i32 v219, v185, 8, 1
	v_bitop3_b32 v102, v102, s52, v184 bitop3:0xe4
	v_bitop3_b32 v118, v118, s52, v219 bitop3:0xe4
	v_bfe_i32 v184, v206, 9, 1
	v_bfe_i32 v219, v185, 9, 1
	v_bitop3_b32 v103, v103, s52, v184 bitop3:0xe4
	v_bitop3_b32 v119, v119, s52, v219 bitop3:0xe4
	v_bfe_i32 v184, v206, 10, 1
	v_bfe_i32 v219, v185, 10, 1
	v_bitop3_b32 v104, v104, s52, v184 bitop3:0xe4
	v_bitop3_b32 v120, v120, s52, v219 bitop3:0xe4
	v_bfe_i32 v184, v206, 11, 1
	v_bfe_i32 v219, v185, 11, 1
	v_bitop3_b32 v105, v105, s52, v184 bitop3:0xe4
	v_bitop3_b32 v121, v121, s52, v219 bitop3:0xe4
	v_bfe_i32 v184, v206, 16, 1
	v_bfe_i32 v219, v185, 16, 1
	v_bitop3_b32 v106, v106, s52, v184 bitop3:0xe4
	v_bitop3_b32 v122, v122, s52, v219 bitop3:0xe4
	v_bfe_i32 v184, v206, 17, 1
	v_bfe_i32 v219, v185, 17, 1
	v_bitop3_b32 v107, v107, s52, v184 bitop3:0xe4
	v_bitop3_b32 v123, v123, s52, v219 bitop3:0xe4
	v_bfe_i32 v184, v206, 18, 1
	v_bfe_i32 v219, v185, 18, 1
	v_bitop3_b32 v108, v108, s52, v184 bitop3:0xe4
	v_bitop3_b32 v124, v124, s52, v219 bitop3:0xe4
	v_bfe_i32 v184, v206, 19, 1
	v_bfe_i32 v219, v185, 19, 1
	v_bitop3_b32 v109, v109, s52, v184 bitop3:0xe4
	v_bitop3_b32 v125, v125, s52, v219 bitop3:0xe4
	v_bfe_i32 v184, v206, 24, 1
	v_bfe_i32 v219, v185, 24, 1
	v_bitop3_b32 v110, v110, s52, v184 bitop3:0xe4
	v_bitop3_b32 v126, v126, s52, v219 bitop3:0xe4
	v_bfe_i32 v184, v206, 25, 1
	v_bfe_i32 v219, v185, 25, 1
	v_bitop3_b32 v111, v111, s52, v184 bitop3:0xe4
	v_bitop3_b32 v127, v127, s52, v219 bitop3:0xe4
	v_bfe_i32 v184, v206, 26, 1
	v_bfe_i32 v219, v185, 26, 1
	v_bitop3_b32 v184, v112, s52, v184 bitop3:0xe4
	v_bitop3_b32 v112, v128, s52, v219 bitop3:0xe4
	v_bfe_i32 v128, v206, 27, 1
	v_bfe_i32 v185, v185, 27, 1
	v_bitop3_b32 v128, v113, s52, v128 bitop3:0xe4
	v_bitop3_b32 v113, v129, s52, v185 bitop3:0xe4
	v_max_f32_e32 v129, v99, v99
	v_max_f32_e32 v185, v98, v98
	v_mfma_f32_32x32x16_bf16 v[18:33], v[162:165], v[222:225], v[18:33]
	v_max_f32_e32 v129, v185, v129
	v_max3_f32 v129, v129, v100, v101
	v_max3_f32 v129, v129, v102, v103
	v_max3_f32 v129, v129, v104, v105
	v_max3_f32 v129, v129, v106, v107
	v_max3_f32 v129, v129, v108, v109
	v_max3_f32 v129, v129, v110, v111
	v_max3_f32 v129, v129, v184, v128
	v_mfma_f32_32x32x16_bf16 v[18:33], v[166:169], v[226:229], v[18:33]
	v_max3_f32 v129, v129, v114, v115
	v_max3_f32 v129, v129, v116, v117
	v_max3_f32 v129, v129, v118, v119
	v_max3_f32 v129, v129, v120, v121
	v_max3_f32 v129, v129, v122, v123
	v_max3_f32 v129, v129, v124, v125
	v_max3_f32 v129, v129, v126, v127
	v_max3_f32 v129, v129, v112, v113
	v_mfma_f32_32x32x16_bf16 v[18:33], v[170:173], v[230:233], v[18:33]
	v_mov_b32_e32 v185, v129
	s_nop 1
	v_permlane32_swap_b32_e32 v129, v185
	v_max_f32_e32 v185, v185, v185
	v_max_f32_e32 v129, v129, v129
	v_max_f32_e32 v129, v129, v185
	v_sub_f32_e32 v185, v129, v180
	v_mul_f32_e32 v185, 0x3db504f3, v185
	v_cmp_ge_f32_e32 vcc, s53, v185
	v_max_f32_e32 v185, v180, v180
	v_max_f32_e32 v129, v185, v129
	v_mfma_f32_32x32x16_bf16 v[18:33], v[174:177], v[234:237], v[18:33]
	v_sub_f32_e32 v185, v180, v129
	v_mul_f32_e32 v185, 0x3e0293ee, v185
	v_exp_f32_e32 v185, v185
	s_cmp_eq_u64 vcc, exec
	s_cselect_b64 s[4:5], -1, 0
	v_cndmask_b32_e64 v206, v185, 1.0, s[4:5]
	v_cmp_gt_f32_e32 vcc, 1.0, v206
	s_cbranch_vccz .LBB0_1171
	s_and_saveexec_b64 s[24:25], s[2:3]
	ds_write_b32 v208, v206 offset:128
	s_or_b64 exec, exec, s[24:25]
	s_waitcnt lgkmcnt(0)
	ds_read_b128 v[222:225], v209 offset:224
	ds_read_b128 v[226:229], v209 offset:192
	ds_read_b128 v[230:233], v209 offset:160
	ds_read_b128 v[234:237], v209 offset:128
	s_waitcnt lgkmcnt(3)
	v_pk_mul_f32 v[16:17], v[16:17], v[224:225]
	s_waitcnt lgkmcnt(2)
	v_pk_mul_f32 v[12:13], v[12:13], v[228:229]
	s_waitcnt lgkmcnt(1)
	v_pk_mul_f32 v[8:9], v[8:9], v[232:233]
	s_waitcnt lgkmcnt(0)
	v_pk_mul_f32 v[4:5], v[4:5], v[236:237]
	v_pk_mul_f32 v[14:15], v[14:15], v[222:223]
	v_pk_mul_f32 v[10:11], v[10:11], v[226:227]
	v_pk_mul_f32 v[6:7], v[6:7], v[230:231]
	v_pk_mul_f32 v[2:3], v[2:3], v[234:235]
	v_pk_mul_f32 v[64:65], v[64:65], v[224:225]
	v_pk_mul_f32 v[60:61], v[60:61], v[228:229]
	v_pk_mul_f32 v[56:57], v[56:57], v[232:233]
	v_pk_mul_f32 v[52:53], v[52:53], v[236:237]
	v_pk_mul_f32 v[62:63], v[62:63], v[222:223]
	v_pk_mul_f32 v[58:59], v[58:59], v[226:227]
	v_pk_mul_f32 v[54:55], v[54:55], v[230:231]
	v_pk_mul_f32 v[50:51], v[50:51], v[234:235]
	v_pk_mul_f32 v[48:49], v[48:49], v[224:225]
	v_pk_mul_f32 v[44:45], v[44:45], v[228:229]
	v_pk_mul_f32 v[40:41], v[40:41], v[232:233]
	v_pk_mul_f32 v[36:37], v[36:37], v[236:237]
	v_pk_mul_f32 v[46:47], v[46:47], v[222:223]
	v_pk_mul_f32 v[42:43], v[42:43], v[226:227]
	v_pk_mul_f32 v[38:39], v[38:39], v[230:231]
	v_pk_mul_f32 v[34:35], v[34:35], v[234:235]
	v_pk_mul_f32 v[32:33], v[32:33], v[224:225]
	v_pk_mul_f32 v[28:29], v[28:29], v[228:229]
	v_pk_mul_f32 v[24:25], v[24:25], v[232:233]
	v_pk_mul_f32 v[20:21], v[20:21], v[236:237]
	v_pk_mul_f32 v[30:31], v[30:31], v[222:223]
	v_pk_mul_f32 v[26:27], v[26:27], v[226:227]
	v_pk_mul_f32 v[22:23], v[22:23], v[230:231]
	v_pk_mul_f32 v[18:19], v[18:19], v[234:235]

; template <int MODE> ...
;     ...
;         for (; r + 1 < NTr && jb + r + 1 <= tdiag; r += 2) {
;             HALFU(pB0, pB1, mnB, alB, pA0, pA1, alA, jb + r, 1, 0);
;             HALFU(pA0, pA1, mnA, alA, pB0, pB1, alB, jb + r + 1, 0, 1);
;         }
.Lstg_e2:
	s_add_i32 s76, s74, 3
	s_mov_b64 s[24:25], -1
	s_cmp_lt_i32 s76, s70
	s_mov_b64 s[26:27], -1
	s_cbranch_scc0 .LBB0_1173
	s_add_u32 s6, s6, 0x8000
	s_addc_u32 s7, s7, 0
	s_add_u32 s0, s0, 0x8000
	s_addc_u32 s1, s1, 0
	s_add_i32 s74, s74, 2
	s_add_i32 s24, s61, s74
	s_add_i32 s26, s24, 1
	s_cmp_ge_u32 s26, s71
	v_lshl_add_u64 v[182:183], v[182:183], 0, 16
	s_mov_b64 s[24:25], 0
	s_cselect_b64 s[26:27], -1, 0

; #define PG8_STAGE(bufoff, gbase, voff) do { _Pragma("unroll") for (int _i = 0; _i < 2; ++_i) glds16_s((const void*)((const char*)(gbase) + _i * r64), (voff), ldsb + (unsigned)(bufoff) + ldsw + _i * 8192u); } while (0)
; #define PG8_LDA(b, h) do { _Pragma("unroll") for (int m = 0; m < 4; ++m) { const int o_ = PG8_SA(b, h) + aoff + m * 2048; \
;         if constexpr (FP8) A8[m] = PG8_CAT8(o_); else { At[m][0] = PG8_LD16(o_); At[m][1] = PG8_LD16(o_ + 1024); } } } while (0)
; #define PG8_LDB(X, X8, b, h) do { _Pragma("unroll") for (int n = 0; n < 2; ++n) { const int o_ = PG8_SB(b, h) + boff + n * 2048; \
;         if constexpr (FP8) X8[n] = PG8_CAT8(o_); else { X[n][0] = PG8_LD16(o_); X[n][1] = PG8_LD16(o_ + 1024); } } } while (0)
; #define PG8_WAIT_V(n) asm volatile("s_waitcnt vmcnt(" #n ")" ::: "memory")
; #define PG8_WAIT_L(n) asm volatile("s_waitcnt lgkmcnt(" #n ")" ::: "memory")
; #define PG8_BAR __builtin_amdgcn_s_barrier()
; #define PG8_SCHED __builtin_amdgcn_sched_barrier(0)
; #define PG8_HI do { if constexpr (FP8) asm volatile("s_setprio 1"); } while (0)
; #define PG8_LO do { if constexpr (FP8) asm volatile("s_setprio 0"); } while (0)
; template <class Epi, class Sched, bool FP8 = false>
; __device__ __forceinline__ void gemm_phase(LAS unsigned char* lds, const int Kb, const int nt  , const Sched& S, const Epi& E) {
;     ...
;         for (int t = 0; t < nt; t += 2) {
;             const bool last = (t == nt - 2);
;             const char* a1 = cA + (size_t)(t + 1) * kstep;
;             const char* a2 = last ? nA : cA + (size_t)(t + 2) * kstep; const char* b2 = last ? nB : cB + (size_t)(t + 2) * kstep;
;             const char* a3 = a2 + kstep; const char* b3 = b2 + kstep;
;             PG8_LDB(B0, B08, 0, 0); PG8_SCHED; PG8_LDA(0, 0); PG8_STAGE(PG8_SA(1, 1), a1 + hstep, voffA);
;             PG8_WAIT_L(8); PG8_BAR; PG8_HI; PG8_WAIT_L(0); PG8_MMA(0, 0, B0, B08); PG8_BAR; PG8_LO; PG8_SCHED;
;             PG8_LDB(B1, B18, 0, 1); PG8_STAGE(PG8_SB(0, 0), b2, voffB);
;             PG8_BAR; PG8_HI; PG8_WAIT_L(0); PG8_MMA(0, 1, B1, B18); PG8_BAR; PG8_LO;
;             PG8_LDA(0, 1); PG8_STAGE(PG8_SA(0, 0), a2, voffA);
;             PG8_BAR; PG8_HI; PG8_WAIT_L(0); PG8_MMA(1, 0, B0, B08); PG8_BAR; PG8_LO; PG8_SCHED;
;             PG8_STAGE(PG8_SB(0, 1), b2 + hstep, voffB);
;             PG8_WAIT_V(6); PG8_BAR; PG8_HI; PG8_MMA(1, 1, B1, B18); PG8_BAR; PG8_LO;
.LBB0_2752:
	ds_read_b128 v[158:161], v139
	ds_read_b128 v[162:165], v140
	ds_read_b128 v[166:169], v141
	ds_read_b128 v[170:173], v142
	s_add_u32 s24, s22, 0x100
	s_addc_u32 s25, s23, 0
	s_cmp_eq_u32 s67, 12
	s_cselect_b32 s28, s14, s24
	s_cselect_b32 s29, s15, s25
	s_cselect_b32 s26, s16, s11
	s_cselect_b32 s27, s17, s13
	s_add_u32 s30, s28, 0x80
	s_addc_u32 s31, s29, 0
	ds_read_b128 v[174:177], v155
	ds_read_b128 v[178:181], v155 offset:1024
	ds_read_b128 v[182:185], v155 offset:2048
	ds_read_b128 v[186:189], v155 offset:3072
	ds_read_b128 v[194:197], v155 offset:4096
	ds_read_b128 v[198:201], v155 offset:5120
	ds_read_b128 v[202:205], v155 offset:6144
	ds_read_b128 v[206:209], v155 offset:7168
	s_add_u32 s68, s22, 0x40080
	s_addc_u32 s69, s23, 0
	s_mov_b32 s70, m0
	s_mov_b32 m0, s63
	s_nop 0
	global_load_lds_dwordx4 v1, s[68:69]
	s_mov_b32 m0, s70
	s_add_u32 s22, s22, 0x60080
	s_addc_u32 s23, s23, 0
	s_mov_b32 s68, m0
	s_mov_b32 m0, s64
	s_nop 0
	global_load_lds_dwordx4 v1, s[22:23]
	s_mov_b32 m0, s68
	s_waitcnt lgkmcnt(8)
	s_barrier
	s_waitcnt lgkmcnt(0)
	s_setprio 1
	v_mfma_f32_16x16x128_f8f6f4 v[130:133], v[158:165], v[174:181], v[130:133]
	v_mfma_f32_16x16x128_f8f6f4 v[122:125], v[166:173], v[174:181], v[122:125]
	v_mfma_f32_16x16x128_f8f6f4 v[114:117], v[158:165], v[182:189], v[114:117]
	v_mfma_f32_16x16x128_f8f6f4 v[106:109], v[166:173], v[182:189], v[106:109]
	v_mfma_f32_16x16x128_f8f6f4 v[98:101], v[158:165], v[194:201], v[98:101]
	v_mfma_f32_16x16x128_f8f6f4 v[90:93], v[166:173], v[194:201], v[90:93]
	v_mfma_f32_16x16x128_f8f6f4 v[82:85], v[158:165], v[202:209], v[82:85]
	v_mfma_f32_16x16x128_f8f6f4 v[74:77], v[166:173], v[202:209], v[74:77]
	s_setprio 0
	s_barrier
	ds_read_b128 v[210:213], v143
	ds_read_b128 v[214:217], v144
	ds_read_b128 v[218:221], v145
	ds_read_b128 v[222:225], v146
	s_mov_b32 s22, m0
	s_mov_b32 m0, s21
	s_nop 0
	global_load_lds_dwordx4 v138, s[26:27]
	s_mov_b32 m0, s22
	s_add_u32 s22, s26, 0x20000
	s_addc_u32 s23, s27, 0
	s_mov_b32 s68, m0
	s_mov_b32 m0, s48
	s_nop 0
	global_load_lds_dwordx4 v138, s[22:23]
	s_mov_b32 m0, s68
	s_barrier
	s_waitcnt lgkmcnt(0)
	s_setprio 1
	v_mfma_f32_16x16x128_f8f6f4 v[126:129], v[210:217], v[174:181], v[126:129]
	v_mfma_f32_16x16x128_f8f6f4 v[118:121], v[218:225], v[174:181], v[118:121]
	v_mfma_f32_16x16x128_f8f6f4 v[110:113], v[210:217], v[182:189], v[110:113]
	v_mfma_f32_16x16x128_f8f6f4 v[102:105], v[218:225], v[182:189], v[102:105]
	v_mfma_f32_16x16x128_f8f6f4 v[94:97], v[210:217], v[194:201], v[94:97]
	v_mfma_f32_16x16x128_f8f6f4 v[86:89], v[218:225], v[194:201], v[86:89]
	v_mfma_f32_16x16x128_f8f6f4 v[78:81], v[210:217], v[202:209], v[78:81]
	v_mfma_f32_16x16x128_f8f6f4 v[70:73], v[218:225], v[202:209], v[70:73]
	s_setprio 0
	s_barrier
	ds_read_b128 v[174:177], v155 offset:16384
	ds_read_b128 v[178:181], v155 offset:17408
	ds_read_b128 v[182:185], v155 offset:18432
	ds_read_b128 v[186:189], v155 offset:19456
	ds_read_b128 v[194:197], v155 offset:20480
	ds_read_b128 v[198:201], v155 offset:21504
	ds_read_b128 v[202:205], v155 offset:22528
	ds_read_b128 v[206:209], v155 offset:23552
	s_mov_b32 s22, m0
	s_mov_b32 m0, s19
	s_nop 0
	global_load_lds_dwordx4 v1, s[28:29]
	s_mov_b32 m0, s22
	s_add_u32 s22, s28, 0x20000
	s_addc_u32 s23, s29, 0
	s_mov_b32 s68, m0
	s_mov_b32 m0, s49
	s_nop 0
	global_load_lds_dwordx4 v1, s[22:23]
	s_mov_b32 m0, s68
	s_barrier
	s_waitcnt lgkmcnt(0)
	s_setprio 1
	v_mfma_f32_16x16x128_f8f6f4 v[66:69], v[158:165], v[174:181], v[66:69]
	v_mfma_f32_16x16x128_f8f6f4 v[58:61], v[166:173], v[174:181], v[58:61]
	v_mfma_f32_16x16x128_f8f6f4 v[50:53], v[158:165], v[182:189], v[50:53]
	v_mfma_f32_16x16x128_f8f6f4 v[42:45], v[166:173], v[182:189], v[42:45]
	v_mfma_f32_16x16x128_f8f6f4 v[34:37], v[158:165], v[194:201], v[34:37]
	v_mfma_f32_16x16x128_f8f6f4 v[26:29], v[166:173], v[194:201], v[26:29]
	v_mfma_f32_16x16x128_f8f6f4 v[18:21], v[158:165], v[202:209], v[18:21]
	v_mfma_f32_16x16x128_f8f6f4 v[10:13], v[166:173], v[202:209], v[10:13]
	s_setprio 0
	s_barrier
	s_add_u32 s22, s26, 0x40000
	s_addc_u32 s23, s27, 0
	s_mov_b32 s68, m0
	s_mov_b32 m0, s50
	s_nop 0
	global_load_lds_dwordx4 v138, s[22:23]
	s_mov_b32 m0, s68
	s_add_u32 s22, s26, 0x60000
	s_addc_u32 s23, s27, 0
	s_mov_b32 s68, m0
	s_mov_b32 m0, s51
	s_nop 0
	global_load_lds_dwordx4 v138, s[22:23]
	s_mov_b32 m0, s68
	s_waitcnt vmcnt(6)
	s_barrier
	s_setprio 1
	v_mfma_f32_16x16x128_f8f6f4 v[62:65], v[210:217], v[174:181], v[62:65]
	v_mfma_f32_16x16x128_f8f6f4 v[54:57], v[218:225], v[174:181], v[54:57]
	v_mfma_f32_16x16x128_f8f6f4 v[46:49], v[210:217], v[182:189], v[46:49]
	v_mfma_f32_16x16x128_f8f6f4 v[38:41], v[218:225], v[182:189], v[38:41]
	v_mfma_f32_16x16x128_f8f6f4 v[30:33], v[210:217], v[194:201], v[30:33]
	v_mfma_f32_16x16x128_f8f6f4 v[22:25], v[218:225], v[194:201], v[22:25]
	v_mfma_f32_16x16x128_f8f6f4 v[14:17], v[210:217], v[202:209], v[14:17]
	v_mfma_f32_16x16x128_f8f6f4 v[2:5], v[218:225], v[202:209], v[2:5]
	s_setprio 0
	s_barrier
	ds_read_b128 v[158:161], v147
	ds_read_b128 v[162:165], v148
	ds_read_b128 v[166:169], v149
	ds_read_b128 v[170:173], v150
	ds_read_b128 v[174:177], v155 offset:32768
	ds_read_b128 v[178:181], v155 offset:33792
	ds_read_b128 v[182:185], v155 offset:34816
	ds_read_b128 v[186:189], v155 offset:35840
	ds_read_b128 v[194:197], v155 offset:36864
	ds_read_b128 v[198:201], v155 offset:37888
	ds_read_b128 v[202:205], v155 offset:38912
	ds_read_b128 v[206:209], v155 offset:39936
	s_add_u32 s22, s28, 0x40000
	s_addc_u32 s23, s29, 0
	s_mov_b32 s68, m0
	s_mov_b32 m0, s52
	s_nop 0
	global_load_lds_dwordx4 v1, s[22:23]
	s_mov_b32 m0, s68
	s_add_u32 s22, s28, 0x60000
	s_addc_u32 s23, s29, 0
	s_mov_b32 s68, m0
	s_mov_b32 m0, s53
	s_nop 0
	global_load_lds_dwordx4 v1, s[22:23]
	s_mov_b32 m0, s68
	s_waitcnt lgkmcnt(8)
	s_barrier
; #define PG8_STAGE(bufoff, gbase, voff) do { _Pragma("unroll") for (int _i = 0; _i < 2; ++_i) glds16_s((const void*)((const char*)(gbase) + _i * r64), (voff), ldsb + (unsigned)(bufoff) + ldsw + _i * 8192u); } while (0)
; #define PG8_WAIT_V(n) asm volatile("s_waitcnt vmcnt(" #n ")" ::: "memory")
; #define PG8_WAIT_L(n) asm volatile("s_waitcnt lgkmcnt(" #n ")" ::: "memory")
;     __device__ __forceinline__ void operator()(const f32x4 (&acc)[2][2][4][2], const Unit& u, int wr, int wc, int fr, int fq) const {
;         const int row0 = u.pm * BM + wr * 64 + fr, col0 = u.pn * HALF + wc * 32 + 8 * fq;
; #pragma unroll
;         for (int ai = 0; ai < 2; ++ai)
; #pragma unroll
;             for (int m = 0; m < 4; ++m) { unsigned char* rowp = O + (size_t)(row0 + ai * HALF + m * 16) * ldc + col0;
;                 f32x4 v[2];
; #pragma unroll
;                 for (int n = 0; n < 2; ++n) { const f32x4 g = acc[ai][0][m][n] * sin_, up = acc[ai][1][m][n] * (sin_ * sout);
; #pragma unroll
;                     for (int j = 0; j < 4; ++j) { const float e = __builtin_amdgcn_exp2f(-1.4426950408889634f * g[j]); v[n][j] = g[j] * __builtin_amdgcn_rcpf(1.f + e) * up[j]; } }
;                 u32x2 w; w.x = pk4_fp8(v[0][0], v[0][1], v[0][2], v[0][3]); w.y = pk4_fp8(v[1][0], v[1][1], v[1][2], v[1][3]);
;                 *(u32x2*)rowp = w; }
; template <class Epi, class Sched, bool FP8 = false>
; __device__ __forceinline__ void gemm_phase(LAS unsigned char* lds, const int Kb, const int nt  , const Sched& S, const Epi& E) {
;     ...
;             PG8_LDB(B0, B08, 1, 0); PG8_SCHED; PG8_LDA(1, 0); PG8_STAGE(PG8_SA(0, 1), a2 + hstep, voffA);
;             PG8_WAIT_L(8); PG8_BAR; PG8_HI; PG8_WAIT_L(0); PG8_MMA(0, 0, B0, B08); PG8_BAR; PG8_LO; PG8_SCHED;
;             PG8_LDB(B1, B18, 1, 1); PG8_STAGE(PG8_SB(1, 0), b3, voffB);
;             PG8_BAR; PG8_HI; PG8_WAIT_L(0); PG8_MMA(0, 1, B1, B18); PG8_BAR; PG8_LO;
;             PG8_LDA(1, 1); PG8_STAGE(PG8_SA(1, 0), a3, voffA);
;             PG8_BAR; PG8_HI; PG8_WAIT_L(0); PG8_MMA(1, 0, B0, B08); PG8_BAR; PG8_LO; PG8_SCHED;
;             PG8_STAGE(PG8_SB(1, 1), b3 + hstep, voffB);
;             PG8_WAIT_V(6); PG8_BAR; PG8_HI; PG8_MMA(1, 1, B1, B18); PG8_BAR; PG8_LO;
;         }
;         { int l_; asm volatile("v_mbcnt_lo_u32_b32 %0, -1, 0\n\tv_mbcnt_hi_u32_b32 %0, -1, %0" : "=v"(l_));
;           E(acc, cur, wr, wc, l_ & 15, l_ >> 4); }
	s_waitcnt lgkmcnt(0)
	s_setprio 1
	v_mfma_f32_16x16x128_f8f6f4 v[130:133], v[158:165], v[174:181], v[130:133]
	v_mfma_f32_16x16x128_f8f6f4 v[122:125], v[166:173], v[174:181], v[122:125]
	v_mfma_f32_16x16x128_f8f6f4 v[114:117], v[158:165], v[182:189], v[114:117]
	v_mfma_f32_16x16x128_f8f6f4 v[106:109], v[166:173], v[182:189], v[106:109]
	v_mfma_f32_16x16x128_f8f6f4 v[98:101], v[158:165], v[194:201], v[98:101]
	v_mfma_f32_16x16x128_f8f6f4 v[90:93], v[166:173], v[194:201], v[90:93]
	v_mfma_f32_16x16x128_f8f6f4 v[82:85], v[158:165], v[202:209], v[82:85]
	v_mfma_f32_16x16x128_f8f6f4 v[74:77], v[166:173], v[202:209], v[74:77]
	s_setprio 0
	s_barrier
	ds_read_b128 v[210:213], v151
	ds_read_b128 v[214:217], v152
	s_add_u32 s22, s26, 0x80
	s_addc_u32 s23, s27, 0
	ds_read_b128 v[218:221], v153
	ds_read_b128 v[222:225], v154
	s_mov_b32 s68, m0
	s_mov_b32 m0, s57
	s_nop 0
	global_load_lds_dwordx4 v138, s[22:23]
	s_mov_b32 m0, s68
	s_add_u32 s22, s26, 0x20080
	s_addc_u32 s23, s27, 0
	s_mov_b32 s68, m0
	s_mov_b32 m0, s58
	s_nop 0
	global_load_lds_dwordx4 v138, s[22:23]
	s_mov_b32 m0, s68
	s_barrier
	s_waitcnt lgkmcnt(0)
	s_setprio 1
	v_mfma_f32_16x16x128_f8f6f4 v[126:129], v[210:217], v[174:181], v[126:129]
	v_mfma_f32_16x16x128_f8f6f4 v[118:121], v[218:225], v[174:181], v[118:121]
	v_mfma_f32_16x16x128_f8f6f4 v[110:113], v[210:217], v[182:189], v[110:113]
	v_mfma_f32_16x16x128_f8f6f4 v[102:105], v[218:225], v[182:189], v[102:105]
	v_mfma_f32_16x16x128_f8f6f4 v[94:97], v[210:217], v[194:201], v[94:97]
	v_mfma_f32_16x16x128_f8f6f4 v[86:89], v[218:225], v[194:201], v[86:89]
	v_mfma_f32_16x16x128_f8f6f4 v[78:81], v[210:217], v[202:209], v[78:81]
	v_mfma_f32_16x16x128_f8f6f4 v[70:73], v[218:225], v[202:209], v[70:73]
	s_setprio 0
	s_barrier
	ds_read_b128 v[174:177], v155 offset:49152
	ds_read_b128 v[178:181], v155 offset:50176
	ds_read_b128 v[182:185], v155 offset:51200
	ds_read_b128 v[186:189], v155 offset:52224
	ds_read_b128 v[194:197], v155 offset:53248
	ds_read_b128 v[198:201], v155 offset:54272
	ds_read_b128 v[202:205], v155 offset:55296
	ds_read_b128 v[206:209], v155 offset:56320
	s_mov_b32 s22, m0
	s_mov_b32 m0, s59
	s_nop 0
	global_load_lds_dwordx4 v1, s[30:31]
	s_mov_b32 m0, s22
	s_add_u32 s22, s28, 0x20080
	s_addc_u32 s23, s29, 0
	s_mov_b32 s28, m0
	s_mov_b32 m0, s60
	s_nop 0
	global_load_lds_dwordx4 v1, s[22:23]
	s_mov_b32 m0, s28
	s_barrier
	s_waitcnt lgkmcnt(0)
	s_setprio 1
	v_mfma_f32_16x16x128_f8f6f4 v[66:69], v[158:165], v[174:181], v[66:69]
	v_mfma_f32_16x16x128_f8f6f4 v[58:61], v[166:173], v[174:181], v[58:61]
	v_mfma_f32_16x16x128_f8f6f4 v[50:53], v[158:165], v[182:189], v[50:53]
	v_mfma_f32_16x16x128_f8f6f4 v[42:45], v[166:173], v[182:189], v[42:45]
	v_mfma_f32_16x16x128_f8f6f4 v[34:37], v[158:165], v[194:201], v[34:37]
	v_mfma_f32_16x16x128_f8f6f4 v[26:29], v[166:173], v[194:201], v[26:29]
	v_mfma_f32_16x16x128_f8f6f4 v[18:21], v[158:165], v[202:209], v[18:21]
	v_mfma_f32_16x16x128_f8f6f4 v[10:13], v[166:173], v[202:209], v[10:13]
	s_setprio 0
	s_barrier
	s_add_u32 s22, s26, 0x40080
	s_addc_u32 s23, s27, 0
	s_mov_b32 s28, m0
	s_mov_b32 m0, s61
	s_nop 0
	global_load_lds_dwordx4 v138, s[22:23]
	s_mov_b32 m0, s28
	s_add_u32 s22, s26, 0x60080
	s_addc_u32 s23, s27, 0
	s_mov_b32 s26, m0
	s_mov_b32 m0, s62
	s_nop 0
	global_load_lds_dwordx4 v138, s[22:23]
	s_mov_b32 m0, s26
	s_add_i32 s67, s67, 2
	s_add_u32 s11, s11, 0x100
	s_addc_u32 s13, s13, 0
	s_cmp_gt_u32 s67, 13
	s_mov_b64 s[22:23], s[24:25]
	s_waitcnt vmcnt(6)
	s_barrier
	s_setprio 1
	v_mfma_f32_16x16x128_f8f6f4 v[62:65], v[210:217], v[174:181], v[62:65]
	v_mfma_f32_16x16x128_f8f6f4 v[54:57], v[218:225], v[174:181], v[54:57]
	v_mfma_f32_16x16x128_f8f6f4 v[46:49], v[210:217], v[182:189], v[46:49]
	v_mfma_f32_16x16x128_f8f6f4 v[38:41], v[218:225], v[182:189], v[38:41]
	v_mfma_f32_16x16x128_f8f6f4 v[30:33], v[210:217], v[194:201], v[30:33]
	v_mfma_f32_16x16x128_f8f6f4 v[22:25], v[218:225], v[194:201], v[22:25]
	v_mfma_f32_16x16x128_f8f6f4 v[14:17], v[210:217], v[202:209], v[14:17]
	v_mfma_f32_16x16x128_f8f6f4 v[2:5], v[218:225], v[202:209], v[2:5]
	s_setprio 0
	s_barrier
	s_cbranch_scc0 .LBB0_2752
	v_mov_b32_e32 v8, v130
	v_mov_b32_e32 v9, v126
	s_nop 3
	v_pk_mul_f32 v[136:137], v[8:9], s[6:7]
	v_mov_b32_e32 v126, v131
	v_mul_f32_e32 v8, 0xbfb8aa3b, v136
	v_exp_f32_e32 v130, v8
	v_pk_mul_f32 v[126:127], v[126:127], s[6:7]
	s_lshl_b32 s11, s20, 8
	v_mul_f32_e32 v8, 0xbfb8aa3b, v126
	v_add_f32_e32 v130, 1.0, v130
	v_rcp_f32_e32 v135, v130
	v_exp_f32_e32 v131, v8
	v_mbcnt_lo_u32_b32 v6, -1, 0
	v_mbcnt_hi_u32_b32 v6, -1, v6
	s_add_i32 s11, s11, s54
	v_mul_f32_e32 v135, v136, v135
	v_mul_f32_e32 v135, v135, v137
	v_mov_b32_e32 v136, v132
	v_mov_b32_e32 v137, v128
	v_pk_mul_f32 v[136:137], v[136:137], s[6:7]
	v_add_f32_e32 v130, 1.0, v131
	v_mul_f32_e32 v128, 0xbfb8aa3b, v136
	v_exp_f32_e32 v132, v128
	v_mov_b32_e32 v128, v133
	v_rcp_f32_e32 v158, v130
	v_pk_mul_f32 v[128:129], v[128:129], s[6:7]
	v_and_or_b32 v134, v6, 15, s11
	v_mul_f32_e32 v133, 0xbfb8aa3b, v128
	v_exp_f32_e32 v133, v133
	v_mul_f32_e32 v126, v126, v158
	v_mul_f32_e32 v158, v126, v127
	v_add_f32_e32 v126, 1.0, v132
	v_rcp_f32_e32 v132, v126
	v_add_f32_e32 v126, 1.0, v133
	v_rcp_f32_e32 v133, v126
	v_mov_b32_e32 v126, v122
	v_mov_b32_e32 v127, v118
	v_pk_mul_f32 v[126:127], v[126:127], s[6:7]
	v_mul_f32_e32 v122, v136, v132
	v_mul_f32_e32 v118, 0xbfb8aa3b, v126
	v_exp_f32_e32 v118, v118
	v_mul_f32_e32 v132, v122, v137
	v_mul_f32_e32 v122, v128, v133
	v_mul_f32_e32 v129, v122, v129
	v_add_f32_e32 v118, 1.0, v118
	v_rcp_f32_e32 v128, v118
	v_mov_b32_e32 v118, v123
	v_pk_mul_f32 v[118:119], v[118:119], s[6:7]
	s_lshl_b32 s11, s18, 7
;     __device__ __forceinline__ void operator()(const f32x4 (&acc)[2][2][4][2], const Unit& u, int wr, int wc, int fr, int fq) const {
;         const int row0 = u.pm * BM + wr * 64 + fr, col0 = u.pn * HALF + wc * 32 + 8 * fq;
; #pragma unroll
;         for (int ai = 0; ai < 2; ++ai)
; #pragma unroll
;             for (int m = 0; m < 4; ++m) { unsigned char* rowp = O + (size_t)(row0 + ai * HALF + m * 16) * ldc + col0;
;                 f32x4 v[2];
; #pragma unroll
;                 for (int n = 0; n < 2; ++n) { const f32x4 g = acc[ai][0][m][n] * sin_, up = acc[ai][1][m][n] * (sin_ * sout);
; #pragma unroll
;                     for (int j = 0; j < 4; ++j) { const float e = __builtin_amdgcn_exp2f(-1.4426950408889634f * g[j]); v[n][j] = g[j] * __builtin_amdgcn_rcpf(1.f + e) * up[j]; } }
;                 u32x2 w; w.x = pk4_fp8(v[0][0], v[0][1], v[0][2], v[0][3]); w.y = pk4_fp8(v[1][0], v[1][1], v[1][2], v[1][3]);
;                 *(u32x2*)rowp = w; }
;     }
	v_mul_f32_e32 v123, 0xbfb8aa3b, v118
	v_exp_f32_e32 v123, v123
	v_mul_f32_e32 v122, v126, v128
	v_mul_f32_e32 v126, v122, v127
	v_ashrrev_i32_e32 v6, 1, v6
	v_add_f32_e32 v122, 1.0, v123
	v_rcp_f32_e32 v127, v122
	v_mov_b32_e32 v122, v124
	v_mov_b32_e32 v123, v120
	v_pk_mul_f32 v[122:123], v[122:123], s[6:7]
	v_mul_f32_e32 v118, v118, v127
	v_mul_f32_e32 v120, 0xbfb8aa3b, v122
	v_exp_f32_e32 v124, v120
	v_mov_b32_e32 v120, v125
	v_pk_mul_f32 v[120:121], v[120:121], s[6:7]
	v_mul_f32_e32 v127, v118, v119
	v_mul_f32_e32 v125, 0xbfb8aa3b, v120
	v_exp_f32_e32 v125, v125
	v_add_f32_e32 v124, 1.0, v124
	v_rcp_f32_e32 v124, v124
	v_med3_f32 v128, v129, s66, v157
	v_add_f32_e32 v125, 1.0, v125
	v_rcp_f32_e32 v125, v125
	v_mul_f32_e32 v118, v122, v124
	v_mul_f32_e32 v122, v118, v123
	v_med3_f32 v124, v158, s66, v157
	v_mul_f32_e32 v118, v120, v125
	v_mul_f32_e32 v123, v118, v121
	v_med3_f32 v121, v135, s66, v157
	v_mov_b32_e32 v120, 0
	v_cvt_pk_fp8_f32 v120, v121, v124
	v_med3_f32 v124, v126, s66, v157
	v_med3_f32 v126, v127, s66, v157
	v_mov_b32_e32 v121, 0
	v_cvt_pk_fp8_f32 v121, v124, v126
	v_med3_f32 v122, v122, s66, v157
	v_med3_f32 v123, v123, s66, v157
	v_med3_f32 v125, v132, s66, v157
	v_cvt_pk_fp8_f32 v121, v122, v123 op_sel:[0,0,1]
	v_mov_b32_e32 v122, v114
	v_mov_b32_e32 v123, v110
	v_pk_mul_f32 v[122:123], v[122:123], s[6:7]
	s_or_b32 s11, s11, s55
	v_mul_f32_e32 v110, 0xbfb8aa3b, v122
	v_exp_f32_e32 v114, v110
	v_mov_b32_e32 v110, v115
	v_pk_mul_f32 v[110:111], v[110:111], s[6:7]
	v_and_b32_e32 v6, -8, v6
	v_mul_f32_e32 v115, 0xbfb8aa3b, v110
	v_exp_f32_e32 v115, v115
	v_add_f32_e32 v114, 1.0, v114
	v_rcp_f32_e32 v114, v114
	v_cvt_pk_fp8_f32 v120, v125, v128 op_sel:[0,0,1]
	v_add_f32_e32 v115, 1.0, v115
	v_rcp_f32_e32 v115, v115
	v_add_u32_e32 v6, s11, v6
	v_mov_b64_e32 v[8:9], s[2:3]
	v_ashrrev_i32_e32 v7, 31, v6
	v_mad_i64_i32 v[130:131], s[22:23], v134, s65, v[8:9]
	v_lshl_add_u64 v[118:119], v[130:131], 0, v[6:7]
	v_mul_f32_e32 v114, v122, v114
	global_store_dwordx2 v[118:119], v[120:121], off
	v_mul_f32_e32 v119, v114, v123
	v_mul_f32_e32 v110, v110, v115
	v_mov_b32_e32 v114, v116
	v_mov_b32_e32 v115, v112
	v_pk_mul_f32 v[114:115], v[114:115], s[6:7]
	v_mul_f32_e32 v120, v110, v111
	v_mul_f32_e32 v112, 0xbfb8aa3b, v114
	v_exp_f32_e32 v116, v112
	v_mov_b32_e32 v112, v117
	v_pk_mul_f32 v[112:113], v[112:113], s[6:7]
	v_mov_b32_e32 v111, v102
	v_mul_f32_e32 v117, 0xbfb8aa3b, v112
	v_exp_f32_e32 v117, v117
	v_add_f32_e32 v110, 1.0, v116
	v_rcp_f32_e32 v116, v110
	v_or_b32_e32 v118, 16, v134
	v_add_f32_e32 v110, 1.0, v117
	v_rcp_f32_e32 v117, v110
	v_mov_b32_e32 v110, v106
	v_pk_mul_f32 v[110:111], v[110:111], s[6:7]
	v_mul_f32_e32 v106, v114, v116
	v_mul_f32_e32 v102, 0xbfb8aa3b, v110
	v_exp_f32_e32 v102, v102
	v_mul_f32_e32 v114, v106, v115
	v_mul_f32_e32 v106, v112, v117
	v_mul_f32_e32 v113, v106, v113
	v_add_f32_e32 v102, 1.0, v102
	v_rcp_f32_e32 v112, v102
	v_mov_b32_e32 v102, v107
	v_pk_mul_f32 v[102:103], v[102:103], s[6:7]
	s_and_b64 vcc, exec, s[8:9]
	v_mul_f32_e32 v107, 0xbfb8aa3b, v102
	v_exp_f32_e32 v107, v107
	v_mul_f32_e32 v106, v110, v112
	v_mul_f32_e32 v110, v106, v111
	s_mov_b32 s18, s10
	v_add_f32_e32 v106, 1.0, v107
	v_rcp_f32_e32 v111, v106
	v_mov_b32_e32 v106, v108
	v_mov_b32_e32 v107, v104
	v_pk_mul_f32 v[106:107], v[106:107], s[6:7]
	v_mul_f32_e32 v102, v102, v111
	v_mul_f32_e32 v104, 0xbfb8aa3b, v106
	v_exp_f32_e32 v108, v104
	v_mov_b32_e32 v104, v109
	v_pk_mul_f32 v[104:105], v[104:105], s[6:7]
	v_mul_f32_e32 v103, v102, v103
	v_mul_f32_e32 v109, 0xbfb8aa3b, v104
	v_exp_f32_e32 v109, v109
	v_add_f32_e32 v108, 1.0, v108
	v_rcp_f32_e32 v108, v108
	s_mov_b32 s20, s12
	v_add_f32_e32 v109, 1.0, v109
	v_rcp_f32_e32 v109, v109
	v_mul_f32_e32 v102, v106, v108
	v_mul_f32_e32 v106, v102, v107
	v_med3_f32 v107, v120, s66, v157
	v_mul_f32_e32 v102, v104, v109
	v_mul_f32_e32 v104, v102, v105
	v_med3_f32 v105, v119, s66, v157
	v_mov_b32_e32 v102, 0
	v_cvt_pk_fp8_f32 v102, v105, v107
	v_med3_f32 v105, v110, s66, v157
	v_med3_f32 v107, v103, s66, v157
	v_mov_b32_e32 v103, 0
	v_cvt_pk_fp8_f32 v103, v105, v107
	v_med3_f32 v108, v114, s66, v157
	v_med3_f32 v109, v113, s66, v157
	v_med3_f32 v105, v106, s66, v157
	v_med3_f32 v104, v104, s66, v157
	v_cvt_pk_fp8_f32 v102, v108, v109 op_sel:[0,0,1]
	v_cvt_pk_fp8_f32 v103, v105, v104 op_sel:[0,0,1]
	v_mad_i64_i32 v[104:105], s[22:23], v118, s65, v[8:9]
	v_lshl_add_u64 v[104:105], v[104:105], 0, v[6:7]
	global_store_dwordx2 v[104:105], v[102:103], off
	v_mov_b32_e32 v102, v98
	v_mov_b32_e32 v103, v94
	v_pk_mul_f32 v[102:103], v[102:103], s[6:7]
	v_or_b32_e32 v104, 32, v134
	v_mul_f32_e32 v94, 0xbfb8aa3b, v102
	v_exp_f32_e32 v98, v94
	v_mov_b32_e32 v94, v99
	v_pk_mul_f32 v[94:95], v[94:95], s[6:7]
	s_mov_b64 s[24:25], s[16:17]
	v_mul_f32_e32 v99, 0xbfb8aa3b, v94
	v_add_f32_e32 v98, 1.0, v98
	v_exp_f32_e32 v99, v99
	v_rcp_f32_e32 v105, v98
	v_add_f32_e32 v98, 1.0, v99
	v_mul_f32_e32 v102, v102, v105
	v_rcp_f32_e32 v106, v98
	v_mad_i64_i32 v[98:99], s[22:23], v104, s65, v[8:9]
	v_mul_f32_e32 v104, v102, v103
	v_mov_b32_e32 v102, v100
	v_mov_b32_e32 v103, v96
	v_pk_mul_f32 v[102:103], v[102:103], s[6:7]
	v_mul_f32_e32 v94, v94, v106
	v_mul_f32_e32 v96, 0xbfb8aa3b, v102
	v_exp_f32_e32 v100, v96
	v_mov_b32_e32 v96, v101
	v_pk_mul_f32 v[96:97], v[96:97], s[6:7]
	v_mul_f32_e32 v105, v94, v95
	v_mul_f32_e32 v101, 0xbfb8aa3b, v96
	v_exp_f32_e32 v101, v101
	v_add_f32_e32 v94, 1.0, v100
	v_rcp_f32_e32 v100, v94
	v_mov_b32_e32 v95, v86
	v_add_f32_e32 v94, 1.0, v101
	v_rcp_f32_e32 v101, v94
	v_mov_b32_e32 v94, v90
	v_pk_mul_f32 v[94:95], v[94:95], s[6:7]
	v_mul_f32_e32 v90, v102, v100
;     __device__ __forceinline__ void operator()(const f32x4 (&acc)[2][2][4][2], const Unit& u, int wr, int wc, int fr, int fq) const {
;         const int row0 = u.pm * BM + wr * 64 + fr, col0 = u.pn * HALF + wc * 32 + 8 * fq;
; #pragma unroll
;         for (int ai = 0; ai < 2; ++ai)
; #pragma unroll
;             for (int m = 0; m < 4; ++m) { unsigned char* rowp = O + (size_t)(row0 + ai * HALF + m * 16) * ldc + col0;
;                 f32x4 v[2];
; #pragma unroll
;                 for (int n = 0; n < 2; ++n) { const f32x4 g = acc[ai][0][m][n] * sin_, up = acc[ai][1][m][n] * (sin_ * sout);
; #pragma unroll
;                     for (int j = 0; j < 4; ++j) { const float e = __builtin_amdgcn_exp2f(-1.4426950408889634f * g[j]); v[n][j] = g[j] * __builtin_amdgcn_rcpf(1.f + e) * up[j]; } }
;                 u32x2 w; w.x = pk4_fp8(v[0][0], v[0][1], v[0][2], v[0][3]); w.y = pk4_fp8(v[1][0], v[1][1], v[1][2], v[1][3]);
;                 *(u32x2*)rowp = w; }
;     }
	v_mul_f32_e32 v86, 0xbfb8aa3b, v94
	v_exp_f32_e32 v86, v86
	v_mul_f32_e32 v100, v90, v103
	v_mul_f32_e32 v90, v96, v101
	v_mul_f32_e32 v97, v90, v97
	v_add_f32_e32 v86, 1.0, v86
	v_rcp_f32_e32 v96, v86
	v_mov_b32_e32 v86, v91
	v_pk_mul_f32 v[86:87], v[86:87], s[6:7]
	v_mul_f32_e32 v90, v94, v96
	v_mul_f32_e32 v91, 0xbfb8aa3b, v86
	v_exp_f32_e32 v91, v91
	v_mul_f32_e32 v94, v90, v95
	v_med3_f32 v96, v97, s66, v157
	v_add_f32_e32 v90, 1.0, v91
	v_rcp_f32_e32 v95, v90
	v_mov_b32_e32 v90, v92
	v_mov_b32_e32 v91, v88
	v_pk_mul_f32 v[90:91], v[90:91], s[6:7]
	v_mul_f32_e32 v86, v86, v95
	v_mul_f32_e32 v88, 0xbfb8aa3b, v90
	v_exp_f32_e32 v92, v88
	v_mov_b32_e32 v88, v93
	v_pk_mul_f32 v[88:89], v[88:89], s[6:7]
	v_mul_f32_e32 v95, v86, v87
	v_mul_f32_e32 v93, 0xbfb8aa3b, v88
	v_exp_f32_e32 v93, v93
	v_add_f32_e32 v92, 1.0, v92
	v_rcp_f32_e32 v92, v92
	v_add_f32_e32 v93, 1.0, v93
	v_rcp_f32_e32 v93, v93
	v_mul_f32_e32 v86, v90, v92
	v_mul_f32_e32 v90, v86, v91
	v_med3_f32 v92, v105, s66, v157
	v_mul_f32_e32 v86, v88, v93
	v_mul_f32_e32 v91, v86, v89
	v_med3_f32 v89, v104, s66, v157
	v_mov_b32_e32 v88, 0
	v_cvt_pk_fp8_f32 v88, v89, v92
	v_med3_f32 v92, v94, s66, v157
	v_med3_f32 v94, v95, s66, v157
	v_mov_b32_e32 v89, 0
	v_cvt_pk_fp8_f32 v89, v92, v94
	v_med3_f32 v90, v90, s66, v157
	v_med3_f32 v91, v91, s66, v157
	v_med3_f32 v93, v100, s66, v157
	v_cvt_pk_fp8_f32 v89, v90, v91 op_sel:[0,0,1]
	v_mov_b32_e32 v90, v82
	v_mov_b32_e32 v91, v78
	v_pk_mul_f32 v[90:91], v[90:91], s[6:7]
	v_cvt_pk_fp8_f32 v88, v93, v96 op_sel:[0,0,1]
	v_mul_f32_e32 v78, 0xbfb8aa3b, v90
	v_exp_f32_e32 v82, v78
	v_mov_b32_e32 v78, v83
	v_pk_mul_f32 v[78:79], v[78:79], s[6:7]
	v_lshl_add_u64 v[86:87], v[98:99], 0, v[6:7]
	v_mul_f32_e32 v83, 0xbfb8aa3b, v78
	v_exp_f32_e32 v83, v83
	v_add_f32_e32 v82, 1.0, v82
	v_rcp_f32_e32 v82, v82
	global_store_dwordx2 v[86:87], v[88:89], off
	v_add_f32_e32 v83, 1.0, v83
	v_rcp_f32_e32 v83, v83
	v_mul_f32_e32 v82, v90, v82
	v_mul_f32_e32 v87, v82, v91
	v_mov_b32_e32 v82, v84
	v_mul_f32_e32 v78, v78, v83
	v_mov_b32_e32 v83, v80
	v_pk_mul_f32 v[82:83], v[82:83], s[6:7]
	v_mul_f32_e32 v88, v78, v79
	v_mul_f32_e32 v80, 0xbfb8aa3b, v82
	v_exp_f32_e32 v84, v80
	v_mov_b32_e32 v80, v85
	v_pk_mul_f32 v[80:81], v[80:81], s[6:7]
	v_mov_b32_e32 v79, v70
	v_mul_f32_e32 v85, 0xbfb8aa3b, v80
	v_exp_f32_e32 v85, v85
	v_add_f32_e32 v78, 1.0, v84
	v_rcp_f32_e32 v84, v78
	v_or_b32_e32 v86, 48, v134
	v_add_f32_e32 v78, 1.0, v85
	v_rcp_f32_e32 v85, v78
	v_mov_b32_e32 v78, v74
	v_pk_mul_f32 v[78:79], v[78:79], s[6:7]
	v_mul_f32_e32 v74, v82, v84
	v_mul_f32_e32 v70, 0xbfb8aa3b, v78
	v_exp_f32_e32 v70, v70
	v_mul_f32_e32 v82, v74, v83
	v_mul_f32_e32 v74, v80, v85
	v_mul_f32_e32 v81, v74, v81
	v_add_f32_e32 v70, 1.0, v70
	v_rcp_f32_e32 v80, v70
	v_mov_b32_e32 v70, v75
	v_pk_mul_f32 v[70:71], v[70:71], s[6:7]
	v_mul_f32_e32 v74, v78, v80
	v_mul_f32_e32 v75, 0xbfb8aa3b, v70
	v_exp_f32_e32 v75, v75
	v_mul_f32_e32 v78, v74, v79
	v_add_f32_e32 v74, 1.0, v75
	v_rcp_f32_e32 v79, v74
	v_mov_b32_e32 v74, v76
	v_mov_b32_e32 v75, v72
	v_pk_mul_f32 v[74:75], v[74:75], s[6:7]
	v_mul_f32_e32 v70, v70, v79
	v_mul_f32_e32 v72, 0xbfb8aa3b, v74
	v_exp_f32_e32 v76, v72
	v_mov_b32_e32 v72, v77
	v_pk_mul_f32 v[72:73], v[72:73], s[6:7]
	v_mul_f32_e32 v71, v70, v71
	v_mul_f32_e32 v77, 0xbfb8aa3b, v72
	v_exp_f32_e32 v77, v77
	v_add_f32_e32 v76, 1.0, v76
	v_rcp_f32_e32 v76, v76
	v_add_f32_e32 v77, 1.0, v77
	v_rcp_f32_e32 v77, v77
	v_mul_f32_e32 v70, v74, v76
	v_mul_f32_e32 v74, v70, v75
	v_med3_f32 v75, v88, s66, v157
	v_mul_f32_e32 v70, v72, v77
	v_mul_f32_e32 v72, v70, v73
	v_med3_f32 v73, v87, s66, v157
	v_mov_b32_e32 v70, 0
	v_cvt_pk_fp8_f32 v70, v73, v75
	v_med3_f32 v73, v78, s66, v157
	v_med3_f32 v75, v71, s66, v157
	v_mov_b32_e32 v71, 0
	v_cvt_pk_fp8_f32 v71, v73, v75
	v_med3_f32 v76, v82, s66, v157
	v_med3_f32 v77, v81, s66, v157
	v_med3_f32 v73, v74, s66, v157
	v_med3_f32 v72, v72, s66, v157
	v_cvt_pk_fp8_f32 v70, v76, v77 op_sel:[0,0,1]
	v_cvt_pk_fp8_f32 v71, v73, v72 op_sel:[0,0,1]
	v_mad_i64_i32 v[72:73], s[22:23], v86, s65, v[8:9]
	v_lshl_add_u64 v[72:73], v[72:73], 0, v[6:7]
	global_store_dwordx2 v[72:73], v[70:71], off
	v_mov_b32_e32 v70, v66
	v_mov_b32_e32 v71, v62
	v_pk_mul_f32 v[70:71], v[70:71], s[6:7]
	v_add_u32_e32 v72, 0x80, v134
	v_mul_f32_e32 v62, 0xbfb8aa3b, v70
	v_exp_f32_e32 v66, v62
	v_mov_b32_e32 v62, v67
	v_pk_mul_f32 v[62:63], v[62:63], s[6:7]
	v_add_f32_e32 v66, 1.0, v66
	v_mul_f32_e32 v67, 0xbfb8aa3b, v62
	v_exp_f32_e32 v67, v67
	v_rcp_f32_e32 v73, v66
	v_add_f32_e32 v66, 1.0, v67
	v_mul_f32_e32 v70, v70, v73
	v_rcp_f32_e32 v74, v66
	v_mad_i64_i32 v[66:67], s[22:23], v72, s65, v[8:9]
	v_mul_f32_e32 v72, v70, v71
	v_mov_b32_e32 v70, v68
	v_mov_b32_e32 v71, v64
	v_pk_mul_f32 v[70:71], v[70:71], s[6:7]
	v_mul_f32_e32 v62, v62, v74
	v_mul_f32_e32 v64, 0xbfb8aa3b, v70
	v_exp_f32_e32 v68, v64
	v_mov_b32_e32 v64, v69
	v_pk_mul_f32 v[64:65], v[64:65], s[6:7]
	v_mul_f32_e32 v73, v62, v63
	v_mul_f32_e32 v69, 0xbfb8aa3b, v64
	v_exp_f32_e32 v69, v69
	v_add_f32_e32 v62, 1.0, v68
	v_rcp_f32_e32 v68, v62
	v_mov_b32_e32 v63, v54
	v_add_f32_e32 v62, 1.0, v69
	v_rcp_f32_e32 v69, v62
	v_mov_b32_e32 v62, v58
	v_pk_mul_f32 v[62:63], v[62:63], s[6:7]
	v_mul_f32_e32 v58, v70, v68
	v_mul_f32_e32 v54, 0xbfb8aa3b, v62
	v_exp_f32_e32 v54, v54
	v_mul_f32_e32 v68, v58, v71
	v_mul_f32_e32 v58, v64, v69
	v_mul_f32_e32 v65, v58, v65
	v_add_f32_e32 v54, 1.0, v54
	v_rcp_f32_e32 v64, v54
	v_mov_b32_e32 v54, v59
	v_pk_mul_f32 v[54:55], v[54:55], s[6:7]
	v_mul_f32_e32 v58, v62, v64
	v_mul_f32_e32 v59, 0xbfb8aa3b, v54
	v_exp_f32_e32 v59, v59
	v_mul_f32_e32 v62, v58, v63
	v_med3_f32 v64, v65, s66, v157
;     __device__ __forceinline__ void operator()(const f32x4 (&acc)[2][2][4][2], const Unit& u, int wr, int wc, int fr, int fq) const {
;         const int row0 = u.pm * BM + wr * 64 + fr, col0 = u.pn * HALF + wc * 32 + 8 * fq;
; #pragma unroll
;         for (int ai = 0; ai < 2; ++ai)
; #pragma unroll
;             for (int m = 0; m < 4; ++m) { unsigned char* rowp = O + (size_t)(row0 + ai * HALF + m * 16) * ldc + col0;
;                 f32x4 v[2];
; #pragma unroll
;                 for (int n = 0; n < 2; ++n) { const f32x4 g = acc[ai][0][m][n] * sin_, up = acc[ai][1][m][n] * (sin_ * sout);
; #pragma unroll
;                     for (int j = 0; j < 4; ++j) { const float e = __builtin_amdgcn_exp2f(-1.4426950408889634f * g[j]); v[n][j] = g[j] * __builtin_amdgcn_rcpf(1.f + e) * up[j]; } }
;                 u32x2 w; w.x = pk4_fp8(v[0][0], v[0][1], v[0][2], v[0][3]); w.y = pk4_fp8(v[1][0], v[1][1], v[1][2], v[1][3]);
;                 *(u32x2*)rowp = w; }
;     }
	v_add_f32_e32 v58, 1.0, v59
	v_rcp_f32_e32 v63, v58
	v_mov_b32_e32 v58, v60
	v_mov_b32_e32 v59, v56
	v_pk_mul_f32 v[58:59], v[58:59], s[6:7]
	v_mul_f32_e32 v54, v54, v63
	v_mul_f32_e32 v56, 0xbfb8aa3b, v58
	v_exp_f32_e32 v60, v56
	v_mov_b32_e32 v56, v61
	v_pk_mul_f32 v[56:57], v[56:57], s[6:7]
	v_mul_f32_e32 v63, v54, v55
	v_mul_f32_e32 v61, 0xbfb8aa3b, v56
	v_exp_f32_e32 v61, v61
	v_add_f32_e32 v60, 1.0, v60
	v_rcp_f32_e32 v60, v60
	v_add_f32_e32 v61, 1.0, v61
	v_rcp_f32_e32 v61, v61
	v_mul_f32_e32 v54, v58, v60
	v_mul_f32_e32 v58, v54, v59
	v_med3_f32 v60, v73, s66, v157
	v_mul_f32_e32 v54, v56, v61
	v_mul_f32_e32 v59, v54, v57
	v_med3_f32 v57, v72, s66, v157
	v_mov_b32_e32 v56, 0
	v_cvt_pk_fp8_f32 v56, v57, v60
	v_med3_f32 v60, v62, s66, v157
	v_med3_f32 v62, v63, s66, v157
	v_mov_b32_e32 v57, 0
	v_cvt_pk_fp8_f32 v57, v60, v62
	v_med3_f32 v58, v58, s66, v157
	v_med3_f32 v59, v59, s66, v157
	v_med3_f32 v61, v68, s66, v157
	v_cvt_pk_fp8_f32 v57, v58, v59 op_sel:[0,0,1]
	v_mov_b32_e32 v58, v50
	v_mov_b32_e32 v59, v46
	v_pk_mul_f32 v[58:59], v[58:59], s[6:7]
	v_cvt_pk_fp8_f32 v56, v61, v64 op_sel:[0,0,1]
	v_mul_f32_e32 v46, 0xbfb8aa3b, v58
	v_exp_f32_e32 v50, v46
	v_mov_b32_e32 v46, v51
	v_pk_mul_f32 v[46:47], v[46:47], s[6:7]
	v_lshl_add_u64 v[54:55], v[66:67], 0, v[6:7]
	v_mul_f32_e32 v51, 0xbfb8aa3b, v46
	v_exp_f32_e32 v51, v51
	v_add_f32_e32 v50, 1.0, v50
	v_rcp_f32_e32 v50, v50
	global_store_dwordx2 v[54:55], v[56:57], off
	v_add_f32_e32 v51, 1.0, v51
	v_rcp_f32_e32 v51, v51
	v_mul_f32_e32 v50, v58, v50
	v_mul_f32_e32 v55, v50, v59
	v_mov_b32_e32 v50, v52
	v_mul_f32_e32 v46, v46, v51
	v_mov_b32_e32 v51, v48
	v_pk_mul_f32 v[50:51], v[50:51], s[6:7]
	v_mul_f32_e32 v56, v46, v47
	v_mul_f32_e32 v48, 0xbfb8aa3b, v50
	v_exp_f32_e32 v52, v48
	v_mov_b32_e32 v48, v53
	v_pk_mul_f32 v[48:49], v[48:49], s[6:7]
	v_mov_b32_e32 v47, v38
	v_mul_f32_e32 v53, 0xbfb8aa3b, v48
	v_exp_f32_e32 v53, v53
	v_add_f32_e32 v46, 1.0, v52
	v_rcp_f32_e32 v52, v46
	v_add_u32_e32 v54, 0x90, v134
	v_add_f32_e32 v46, 1.0, v53
	v_rcp_f32_e32 v53, v46
	v_mov_b32_e32 v46, v42
	v_pk_mul_f32 v[46:47], v[46:47], s[6:7]
	v_mul_f32_e32 v42, v50, v52
	v_mul_f32_e32 v38, 0xbfb8aa3b, v46
	v_exp_f32_e32 v38, v38
	v_mul_f32_e32 v50, v42, v51
	v_mul_f32_e32 v42, v48, v53
	v_mul_f32_e32 v49, v42, v49
	v_add_f32_e32 v38, 1.0, v38
	v_rcp_f32_e32 v48, v38
	v_mov_b32_e32 v38, v43
	v_pk_mul_f32 v[38:39], v[38:39], s[6:7]
	v_mul_f32_e32 v42, v46, v48
	v_mul_f32_e32 v43, 0xbfb8aa3b, v38
	v_exp_f32_e32 v43, v43
	v_mul_f32_e32 v46, v42, v47
	v_add_f32_e32 v42, 1.0, v43
	v_rcp_f32_e32 v47, v42
	v_mov_b32_e32 v42, v44
	v_mov_b32_e32 v43, v40
	v_pk_mul_f32 v[42:43], v[42:43], s[6:7]
	v_mul_f32_e32 v38, v38, v47
	v_mul_f32_e32 v40, 0xbfb8aa3b, v42
	v_exp_f32_e32 v44, v40
	v_mov_b32_e32 v40, v45
	v_pk_mul_f32 v[40:41], v[40:41], s[6:7]
	v_mul_f32_e32 v39, v38, v39
	v_mul_f32_e32 v45, 0xbfb8aa3b, v40
	v_exp_f32_e32 v45, v45
	v_add_f32_e32 v44, 1.0, v44
	v_rcp_f32_e32 v44, v44
	v_add_f32_e32 v45, 1.0, v45
	v_rcp_f32_e32 v45, v45
	v_mul_f32_e32 v38, v42, v44
	v_mul_f32_e32 v42, v38, v43
	v_med3_f32 v43, v56, s66, v157
	v_mul_f32_e32 v38, v40, v45
	v_mul_f32_e32 v40, v38, v41
	v_med3_f32 v41, v55, s66, v157
	v_mov_b32_e32 v38, 0
	v_cvt_pk_fp8_f32 v38, v41, v43
	v_med3_f32 v41, v46, s66, v157
	v_med3_f32 v43, v39, s66, v157
	v_mov_b32_e32 v39, 0
	v_cvt_pk_fp8_f32 v39, v41, v43
	v_med3_f32 v44, v50, s66, v157
	v_med3_f32 v45, v49, s66, v157
	v_med3_f32 v41, v42, s66, v157
	v_med3_f32 v40, v40, s66, v157
	v_cvt_pk_fp8_f32 v38, v44, v45 op_sel:[0,0,1]
	v_cvt_pk_fp8_f32 v39, v41, v40 op_sel:[0,0,1]
	v_mad_i64_i32 v[40:41], s[22:23], v54, s65, v[8:9]
	v_lshl_add_u64 v[40:41], v[40:41], 0, v[6:7]
	global_store_dwordx2 v[40:41], v[38:39], off
	v_mov_b32_e32 v38, v34
	v_mov_b32_e32 v39, v30
	v_pk_mul_f32 v[38:39], v[38:39], s[6:7]
	v_add_u32_e32 v40, 0xa0, v134
	v_mul_f32_e32 v30, 0xbfb8aa3b, v38
	v_exp_f32_e32 v34, v30
	v_mov_b32_e32 v30, v35
	v_pk_mul_f32 v[30:31], v[30:31], s[6:7]
	v_add_f32_e32 v34, 1.0, v34
	v_mul_f32_e32 v35, 0xbfb8aa3b, v30
	v_exp_f32_e32 v35, v35
	v_rcp_f32_e32 v41, v34
	v_add_f32_e32 v34, 1.0, v35
	v_mul_f32_e32 v38, v38, v41
	v_rcp_f32_e32 v42, v34
	v_mad_i64_i32 v[34:35], s[22:23], v40, s65, v[8:9]
	v_mul_f32_e32 v40, v38, v39
	v_mov_b32_e32 v38, v36
	v_mov_b32_e32 v39, v32
	v_pk_mul_f32 v[38:39], v[38:39], s[6:7]
	v_mul_f32_e32 v30, v30, v42
	v_mul_f32_e32 v32, 0xbfb8aa3b, v38
	v_exp_f32_e32 v36, v32
	v_mov_b32_e32 v32, v37
	v_pk_mul_f32 v[32:33], v[32:33], s[6:7]
	v_mul_f32_e32 v41, v30, v31
; #define PG8_WAIT_V(n) asm volatile("s_waitcnt vmcnt(" #n ")" ::: "memory")
; #define PG8_BAR __builtin_amdgcn_s_barrier()
;     __device__ __forceinline__ void operator()(const f32x4 (&acc)[2][2][4][2], const Unit& u, int wr, int wc, int fr, int fq) const {
;         const int row0 = u.pm * BM + wr * 64 + fr, col0 = u.pn * HALF + wc * 32 + 8 * fq;
; #pragma unroll
;         for (int ai = 0; ai < 2; ++ai)
; #pragma unroll
;             for (int m = 0; m < 4; ++m) { unsigned char* rowp = O + (size_t)(row0 + ai * HALF + m * 16) * ldc + col0;
;                 f32x4 v[2];
; #pragma unroll
;                 for (int n = 0; n < 2; ++n) { const f32x4 g = acc[ai][0][m][n] * sin_, up = acc[ai][1][m][n] * (sin_ * sout);
; #pragma unroll
;                     for (int j = 0; j < 4; ++j) { const float e = __builtin_amdgcn_exp2f(-1.4426950408889634f * g[j]); v[n][j] = g[j] * __builtin_amdgcn_rcpf(1.f + e) * up[j]; } }
;                 u32x2 w; w.x = pk4_fp8(v[0][0], v[0][1], v[0][2], v[0][3]); w.y = pk4_fp8(v[1][0], v[1][1], v[1][2], v[1][3]);
;                 *(u32x2*)rowp = w; }
;     }
; template <class Epi, class Sched, bool FP8 = false>
; __device__ __forceinline__ void gemm_phase(LAS unsigned char* lds, const int Kb, const int nt  , const Sched& S, const Epi& E) {
;     ...
;     PG8_WAIT_V(0);
;     if (wr == 0) PG8_BAR;
;     PG8_BAR;
	v_mul_f32_e32 v37, 0xbfb8aa3b, v32
	v_exp_f32_e32 v37, v37
	v_add_f32_e32 v30, 1.0, v36
	v_rcp_f32_e32 v36, v30
	v_mov_b32_e32 v31, v22
	v_add_f32_e32 v30, 1.0, v37
	v_rcp_f32_e32 v37, v30
	v_mov_b32_e32 v30, v26
	v_pk_mul_f32 v[30:31], v[30:31], s[6:7]
	v_mul_f32_e32 v26, v38, v36
	v_mul_f32_e32 v22, 0xbfb8aa3b, v30
	v_exp_f32_e32 v22, v22
	v_mul_f32_e32 v36, v26, v39
	v_mul_f32_e32 v26, v32, v37
	v_mul_f32_e32 v33, v26, v33
	v_add_f32_e32 v22, 1.0, v22
	v_rcp_f32_e32 v32, v22
	v_mov_b32_e32 v22, v27
	v_pk_mul_f32 v[22:23], v[22:23], s[6:7]
	v_mul_f32_e32 v26, v30, v32
	v_mul_f32_e32 v27, 0xbfb8aa3b, v22
	v_exp_f32_e32 v27, v27
	v_mul_f32_e32 v30, v26, v31
	v_med3_f32 v32, v33, s66, v157
	v_add_f32_e32 v26, 1.0, v27
	v_rcp_f32_e32 v31, v26
	v_mov_b32_e32 v26, v28
	v_mov_b32_e32 v27, v24
	v_pk_mul_f32 v[26:27], v[26:27], s[6:7]
	v_mul_f32_e32 v22, v22, v31
	v_mul_f32_e32 v24, 0xbfb8aa3b, v26
	v_exp_f32_e32 v28, v24
	v_mov_b32_e32 v24, v29
	v_pk_mul_f32 v[24:25], v[24:25], s[6:7]
	v_mul_f32_e32 v31, v22, v23
	v_mul_f32_e32 v29, 0xbfb8aa3b, v24
	v_exp_f32_e32 v29, v29
	v_add_f32_e32 v28, 1.0, v28
	v_rcp_f32_e32 v28, v28
	v_add_f32_e32 v29, 1.0, v29
	v_rcp_f32_e32 v29, v29
	v_mul_f32_e32 v22, v26, v28
	v_mul_f32_e32 v26, v22, v27
	v_med3_f32 v28, v41, s66, v157
	v_mul_f32_e32 v22, v24, v29
	v_mul_f32_e32 v27, v22, v25
	v_med3_f32 v25, v40, s66, v157
	v_mov_b32_e32 v24, 0
	v_cvt_pk_fp8_f32 v24, v25, v28
	v_med3_f32 v28, v30, s66, v157
	v_med3_f32 v30, v31, s66, v157
	v_mov_b32_e32 v25, 0
	v_cvt_pk_fp8_f32 v25, v28, v30
	v_med3_f32 v26, v26, s66, v157
	v_med3_f32 v27, v27, s66, v157
	v_med3_f32 v29, v36, s66, v157
	v_cvt_pk_fp8_f32 v25, v26, v27 op_sel:[0,0,1]
	v_mov_b32_e32 v26, v18
	v_mov_b32_e32 v27, v14
	v_pk_mul_f32 v[26:27], v[26:27], s[6:7]
	v_cvt_pk_fp8_f32 v24, v29, v32 op_sel:[0,0,1]
	v_mul_f32_e32 v14, 0xbfb8aa3b, v26
	v_exp_f32_e32 v18, v14
	v_mov_b32_e32 v14, v19
	v_pk_mul_f32 v[14:15], v[14:15], s[6:7]
	v_lshl_add_u64 v[22:23], v[34:35], 0, v[6:7]
	v_mul_f32_e32 v19, 0xbfb8aa3b, v14
	v_exp_f32_e32 v19, v19
	v_add_f32_e32 v18, 1.0, v18
	v_rcp_f32_e32 v18, v18
	global_store_dwordx2 v[22:23], v[24:25], off
	v_add_f32_e32 v19, 1.0, v19
	v_rcp_f32_e32 v19, v19
	v_mul_f32_e32 v18, v26, v18
	v_mul_f32_e32 v23, v18, v27
	v_mov_b32_e32 v18, v20
	v_mul_f32_e32 v14, v14, v19
	v_mov_b32_e32 v19, v16
	v_pk_mul_f32 v[18:19], v[18:19], s[6:7]
	v_mul_f32_e32 v24, v14, v15
	v_mul_f32_e32 v16, 0xbfb8aa3b, v18
	v_exp_f32_e32 v20, v16
	v_mov_b32_e32 v16, v21
	v_pk_mul_f32 v[16:17], v[16:17], s[6:7]
	v_mov_b32_e32 v15, v2
	v_mul_f32_e32 v21, 0xbfb8aa3b, v16
	v_exp_f32_e32 v21, v21
	v_add_f32_e32 v14, 1.0, v20
	v_rcp_f32_e32 v20, v14
	v_add_u32_e32 v22, 0xb0, v134
	v_add_f32_e32 v14, 1.0, v21
	v_rcp_f32_e32 v21, v14
	v_mov_b32_e32 v14, v10
	v_pk_mul_f32 v[14:15], v[14:15], s[6:7]
	v_mul_f32_e32 v10, v18, v20
	v_mul_f32_e32 v2, 0xbfb8aa3b, v14
	v_exp_f32_e32 v2, v2
	v_mul_f32_e32 v18, v10, v19
	v_mul_f32_e32 v10, v16, v21
	v_mul_f32_e32 v17, v10, v17
	v_add_f32_e32 v2, 1.0, v2
	v_rcp_f32_e32 v16, v2
	v_mov_b32_e32 v2, v11
	v_pk_mul_f32 v[2:3], v[2:3], s[6:7]
	v_mul_f32_e32 v10, v14, v16
	v_mul_f32_e32 v11, 0xbfb8aa3b, v2
	v_exp_f32_e32 v11, v11
	v_mul_f32_e32 v14, v10, v15
	v_add_f32_e32 v10, 1.0, v11
	v_rcp_f32_e32 v15, v10
	v_mov_b32_e32 v10, v12
	v_mov_b32_e32 v11, v4
	v_pk_mul_f32 v[10:11], v[10:11], s[6:7]
	v_mul_f32_e32 v2, v2, v15
	v_mul_f32_e32 v4, 0xbfb8aa3b, v10
	v_exp_f32_e32 v12, v4
	v_mov_b32_e32 v4, v13
	v_pk_mul_f32 v[4:5], v[4:5], s[6:7]
	v_mul_f32_e32 v3, v2, v3
	v_mul_f32_e32 v13, 0xbfb8aa3b, v4
	v_exp_f32_e32 v13, v13
	v_add_f32_e32 v12, 1.0, v12
	v_rcp_f32_e32 v12, v12
	v_add_f32_e32 v13, 1.0, v13
	v_rcp_f32_e32 v13, v13
	v_mul_f32_e32 v2, v10, v12
	v_mul_f32_e32 v10, v2, v11
	v_med3_f32 v11, v24, s66, v157
	v_mul_f32_e32 v2, v4, v13
	v_mul_f32_e32 v4, v2, v5
	v_med3_f32 v5, v23, s66, v157
	v_mov_b32_e32 v2, 0
	v_cvt_pk_fp8_f32 v2, v5, v11
	v_med3_f32 v5, v14, s66, v157
	v_med3_f32 v11, v3, s66, v157
	v_mov_b32_e32 v3, 0
	v_cvt_pk_fp8_f32 v3, v5, v11
	v_med3_f32 v12, v18, s66, v157
	v_med3_f32 v13, v17, s66, v157
	v_med3_f32 v5, v10, s66, v157
	v_med3_f32 v4, v4, s66, v157
	v_cvt_pk_fp8_f32 v2, v12, v13 op_sel:[0,0,1]
	v_cvt_pk_fp8_f32 v3, v5, v4 op_sel:[0,0,1]
	v_mad_i64_i32 v[4:5], s[22:23], v22, s65, v[8:9]
	v_lshl_add_u64 v[4:5], v[4:5], 0, v[6:7]
	s_mov_b64 s[22:23], s[14:15]
	global_store_dwordx2 v[4:5], v[2:3], off
	s_cbranch_vccz .LBB0_2749
	s_waitcnt vmcnt(0)
	s_cmpk_gt_u32 s42, 0xff
	s_cbranch_scc1 .LBB0_2756
	s_barrier

; #define PG8_STAGE(bufoff, gbase, voff) do { _Pragma("unroll") for (int _i = 0; _i < 2; ++_i) glds16_s((const void*)((const char*)(gbase) + _i * r64), (voff), ldsb + (unsigned)(bufoff) + ldsw + _i * 8192u); } while (0)
; #define PG8_LDA(b, h) do { _Pragma("unroll") for (int m = 0; m < 4; ++m) { const int o_ = PG8_SA(b, h) + aoff + m * 2048; \
;         if constexpr (FP8) A8[m] = PG8_CAT8(o_); else { At[m][0] = PG8_LD16(o_); At[m][1] = PG8_LD16(o_ + 1024); } } } while (0)
; #define PG8_LDB(X, X8, b, h) do { _Pragma("unroll") for (int n = 0; n < 2; ++n) { const int o_ = PG8_SB(b, h) + boff + n * 2048; \
;         if constexpr (FP8) X8[n] = PG8_CAT8(o_); else { X[n][0] = PG8_LD16(o_); X[n][1] = PG8_LD16(o_ + 1024); } } } while (0)
; #define PG8_WAIT_V(n) asm volatile("s_waitcnt vmcnt(" #n ")" ::: "memory")
; #define PG8_WAIT_L(n) asm volatile("s_waitcnt lgkmcnt(" #n ")" ::: "memory")
; #define PG8_BAR __builtin_amdgcn_s_barrier()
; #define PG8_SCHED __builtin_amdgcn_sched_barrier(0)
; #define PG8_HI do { if constexpr (FP8) asm volatile("s_setprio 1"); } while (0)
; #define PG8_LO do { if constexpr (FP8) asm volatile("s_setprio 0"); } while (0)
; template <class Epi, class Sched, bool FP8 = false>
; __device__ __forceinline__ void gemm_phase(LAS unsigned char* lds, const int Kb, const int nt  , const Sched& S, const Epi& E) {
;     ...
;         for (int t = 0; t < nt; t += 2) {
;             const bool last = (t == nt - 2);
;             const char* a1 = cA + (size_t)(t + 1) * kstep;
;             const char* a2 = last ? nA : cA + (size_t)(t + 2) * kstep; const char* b2 = last ? nB : cB + (size_t)(t + 2) * kstep;
;             const char* a3 = a2 + kstep; const char* b3 = b2 + kstep;
;             PG8_LDB(B0, B08, 0, 0); PG8_SCHED; PG8_LDA(0, 0); PG8_STAGE(PG8_SA(1, 1), a1 + hstep, voffA);
;             PG8_WAIT_L(8); PG8_BAR; PG8_HI; PG8_WAIT_L(0); PG8_MMA(0, 0, B0, B08); PG8_BAR; PG8_LO; PG8_SCHED;
;             PG8_LDB(B1, B18, 0, 1); PG8_STAGE(PG8_SB(0, 0), b2, voffB);
;             PG8_BAR; PG8_HI; PG8_WAIT_L(0); PG8_MMA(0, 1, B1, B18); PG8_BAR; PG8_LO;
;             PG8_LDA(0, 1); PG8_STAGE(PG8_SA(0, 0), a2, voffA);
;             PG8_BAR; PG8_HI; PG8_WAIT_L(0); PG8_MMA(1, 0, B0, B08); PG8_BAR; PG8_LO; PG8_SCHED;
;             PG8_STAGE(PG8_SB(0, 1), b2 + hstep, voffB);
;             PG8_WAIT_V(6); PG8_BAR; PG8_HI; PG8_MMA(1, 1, B1, B18); PG8_BAR; PG8_LO;
.LBB0_2837:
	ds_read_b128 v[162:165], v143
	ds_read_b128 v[166:169], v144
	ds_read_b128 v[170:173], v145
	ds_read_b128 v[174:177], v146
	s_add_u32 s24, s22, 0x100
	s_addc_u32 s25, s23, 0
	s_cmp_eq_u32 s75, 52
	s_cselect_b32 s28, s18, s24
	s_cselect_b32 s29, s19, s25
	s_cselect_b32 s26, s20, s73
	s_cselect_b32 s27, s21, s74
	s_add_u32 s30, s28, 0x80
	s_addc_u32 s31, s29, 0
	ds_read_b128 v[178:181], v159
	ds_read_b128 v[182:185], v159 offset:1024
	ds_read_b128 v[192:195], v159 offset:2048
	ds_read_b128 v[196:199], v159 offset:3072
	ds_read_b128 v[200:203], v159 offset:4096
	ds_read_b128 v[204:207], v159 offset:5120
	ds_read_b128 v[208:211], v159 offset:6144
	ds_read_b128 v[212:215], v159 offset:7168
	s_add_u32 s76, s22, 0xe0080
	s_addc_u32 s77, s23, 0
	s_mov_b32 s78, m0
	s_mov_b32 m0, s63
	s_nop 0
	global_load_lds_dwordx4 v138, s[76:77]
	s_mov_b32 m0, s78
	s_add_u32 s22, s22, 0x150080
	s_addc_u32 s23, s23, 0
	s_mov_b32 s76, m0
	s_mov_b32 m0, s64
	s_nop 0
	global_load_lds_dwordx4 v138, s[22:23]
	s_mov_b32 m0, s76
	s_waitcnt lgkmcnt(8)
	s_barrier
	s_waitcnt lgkmcnt(0)
	s_setprio 1
	v_mfma_f32_16x16x128_f8f6f4 v[130:133], v[162:169], v[178:185], v[130:133]
	v_mfma_f32_16x16x128_f8f6f4 v[126:129], v[170:177], v[178:185], v[126:129]
	v_mfma_f32_16x16x128_f8f6f4 v[114:117], v[162:169], v[192:199], v[114:117]
	v_mfma_f32_16x16x128_f8f6f4 v[110:113], v[170:177], v[192:199], v[110:113]
	v_mfma_f32_16x16x128_f8f6f4 v[98:101], v[162:169], v[200:207], v[98:101]
	v_mfma_f32_16x16x128_f8f6f4 v[94:97], v[170:177], v[200:207], v[94:97]
	v_mfma_f32_16x16x128_f8f6f4 v[82:85], v[162:169], v[208:215], v[82:85]
	v_mfma_f32_16x16x128_f8f6f4 v[78:81], v[170:177], v[208:215], v[78:81]
	s_setprio 0
	s_barrier
	ds_read_b128 v[216:219], v147
	ds_read_b128 v[220:223], v148
	ds_read_b128 v[224:227], v149
	ds_read_b128 v[228:231], v150
	s_mov_b32 s22, m0
	s_mov_b32 m0, s47
	s_nop 0
	global_load_lds_dwordx4 v142, s[26:27]
	s_mov_b32 m0, s22
	s_add_u32 s22, s26, 0x70000
	s_addc_u32 s23, s27, 0
	s_mov_b32 s76, m0
	s_mov_b32 m0, s48
	s_nop 0
	global_load_lds_dwordx4 v142, s[22:23]
	s_mov_b32 m0, s76
	s_barrier
	s_waitcnt lgkmcnt(0)
	s_setprio 1
	v_mfma_f32_16x16x128_f8f6f4 v[122:125], v[216:223], v[178:185], v[122:125]
	v_mfma_f32_16x16x128_f8f6f4 v[118:121], v[224:231], v[178:185], v[118:121]
	v_mfma_f32_16x16x128_f8f6f4 v[106:109], v[216:223], v[192:199], v[106:109]
	v_mfma_f32_16x16x128_f8f6f4 v[102:105], v[224:231], v[192:199], v[102:105]
	v_mfma_f32_16x16x128_f8f6f4 v[90:93], v[216:223], v[200:207], v[90:93]
	v_mfma_f32_16x16x128_f8f6f4 v[86:89], v[224:231], v[200:207], v[86:89]
	v_mfma_f32_16x16x128_f8f6f4 v[74:77], v[216:223], v[208:215], v[74:77]
	v_mfma_f32_16x16x128_f8f6f4 v[70:73], v[224:231], v[208:215], v[70:73]
	s_setprio 0
	s_barrier
	ds_read_b128 v[178:181], v159 offset:16384
	ds_read_b128 v[182:185], v159 offset:17408
	ds_read_b128 v[192:195], v159 offset:18432
	ds_read_b128 v[196:199], v159 offset:19456
	ds_read_b128 v[200:203], v159 offset:20480
	ds_read_b128 v[204:207], v159 offset:21504
	ds_read_b128 v[208:211], v159 offset:22528
	ds_read_b128 v[212:215], v159 offset:23552
	s_mov_b32 s22, m0
	s_mov_b32 m0, s46
	s_nop 0
	global_load_lds_dwordx4 v138, s[28:29]
	s_mov_b32 m0, s22
	s_add_u32 s22, s28, 0x70000
	s_addc_u32 s23, s29, 0
	s_mov_b32 s76, m0
	s_mov_b32 m0, s49
	s_nop 0
	global_load_lds_dwordx4 v138, s[22:23]
	s_mov_b32 m0, s76
	s_barrier
	s_waitcnt lgkmcnt(0)
	s_setprio 1
	v_mfma_f32_16x16x128_f8f6f4 v[66:69], v[162:169], v[178:185], v[66:69]
	v_mfma_f32_16x16x128_f8f6f4 v[62:65], v[170:177], v[178:185], v[62:65]
	v_mfma_f32_16x16x128_f8f6f4 v[54:57], v[162:169], v[192:199], v[54:57]
	v_mfma_f32_16x16x128_f8f6f4 v[46:49], v[170:177], v[192:199], v[46:49]
	v_mfma_f32_16x16x128_f8f6f4 v[38:41], v[162:169], v[200:207], v[38:41]
	v_mfma_f32_16x16x128_f8f6f4 v[30:33], v[170:177], v[200:207], v[30:33]
	v_mfma_f32_16x16x128_f8f6f4 v[22:25], v[162:169], v[208:215], v[22:25]
	v_mfma_f32_16x16x128_f8f6f4 v[14:17], v[170:177], v[208:215], v[14:17]
	s_setprio 0
	s_barrier
	s_add_u32 s22, s26, 0xe0000
	s_addc_u32 s23, s27, 0
	s_mov_b32 s76, m0
	s_mov_b32 m0, s50
	s_nop 0
	global_load_lds_dwordx4 v142, s[22:23]
	s_mov_b32 m0, s76
	s_add_u32 s22, s26, 0x150000
	s_addc_u32 s23, s27, 0
	s_mov_b32 s76, m0
	s_mov_b32 m0, s51
	s_nop 0
	global_load_lds_dwordx4 v142, s[22:23]
	s_mov_b32 m0, s76
	s_waitcnt vmcnt(6)
	s_barrier
	s_setprio 1
	v_mfma_f32_16x16x128_f8f6f4 v[58:61], v[216:223], v[178:185], v[58:61]
	v_mfma_f32_16x16x128_f8f6f4 v[50:53], v[224:231], v[178:185], v[50:53]
	v_mfma_f32_16x16x128_f8f6f4 v[42:45], v[216:223], v[192:199], v[42:45]
	v_mfma_f32_16x16x128_f8f6f4 v[34:37], v[224:231], v[192:199], v[34:37]
	v_mfma_f32_16x16x128_f8f6f4 v[26:29], v[216:223], v[200:207], v[26:29]
	v_mfma_f32_16x16x128_f8f6f4 v[18:21], v[224:231], v[200:207], v[18:21]
	v_mfma_f32_16x16x128_f8f6f4 v[10:13], v[216:223], v[208:215], v[10:13]
	v_mfma_f32_16x16x128_f8f6f4 v[2:5], v[224:231], v[208:215], v[2:5]
	s_setprio 0
	s_barrier
	ds_read_b128 v[162:165], v151
	ds_read_b128 v[166:169], v152
	ds_read_b128 v[170:173], v153
	ds_read_b128 v[174:177], v154
	ds_read_b128 v[178:181], v159 offset:32768
	ds_read_b128 v[182:185], v159 offset:33792
	ds_read_b128 v[192:195], v159 offset:34816
	ds_read_b128 v[196:199], v159 offset:35840
	ds_read_b128 v[200:203], v159 offset:36864
	ds_read_b128 v[204:207], v159 offset:37888
	ds_read_b128 v[208:211], v159 offset:38912
	ds_read_b128 v[212:215], v159 offset:39936
	s_add_u32 s22, s28, 0xe0000
	s_addc_u32 s23, s29, 0
	s_mov_b32 s76, m0
	s_mov_b32 m0, s52
	s_nop 0
	global_load_lds_dwordx4 v138, s[22:23]
	s_mov_b32 m0, s76
	s_add_u32 s22, s28, 0x150000
	s_addc_u32 s23, s29, 0
	s_mov_b32 s76, m0
	s_mov_b32 m0, s53
	s_nop 0
	global_load_lds_dwordx4 v138, s[22:23]
	s_mov_b32 m0, s76
	s_waitcnt lgkmcnt(8)
	s_barrier
; __device__ __forceinline__ unsigned cvt_pk_bf16(float lo, float hi) { unsigned r; asm volatile("v_cvt_pk_bf16_f32 %0, %1, %2" : "=v"(r) : "v"(lo), "v"(hi)); return r; }
; #define PG8_STAGE(bufoff, gbase, voff) do { _Pragma("unroll") for (int _i = 0; _i < 2; ++_i) glds16_s((const void*)((const char*)(gbase) + _i * r64), (voff), ldsb + (unsigned)(bufoff) + ldsw + _i * 8192u); } while (0)
; #define PG8_WAIT_V(n) asm volatile("s_waitcnt vmcnt(" #n ")" ::: "memory")
; #define PG8_WAIT_L(n) asm volatile("s_waitcnt lgkmcnt(" #n ")" ::: "memory")
;     __device__ __forceinline__ void operator()(const f32x4 (&acc)[2][2][4][2], const Unit& u, int wr, int wc, int fr, int fq) const {
;         const int row0 = u.pm * BM + wr * 64 + fr, col0 = u.pn * BM + wc * 32 + 8 * fq;
; #pragma unroll
;         for (int ai = 0; ai < 2; ++ai)
; #pragma unroll
;             for (int m = 0; m < 4; ++m) { bf16_t* rowp = O + (size_t)(row0 + ai * HALF + m * 16) * ldc + col0;
; #pragma unroll
;                 for (int bj = 0; bj < 2; ++bj) { const f32x4 v0 = acc[ai][bj][m][0] * scale, v1 = acc[ai][bj][m][1] * scale;
;                     u32x4 w; w.x = cvt_pk_bf16(v0[0], v0[1]); w.y = cvt_pk_bf16(v0[2], v0[3]); w.z = cvt_pk_bf16(v1[0], v1[1]); w.w = cvt_pk_bf16(v1[2], v1[3]);
;                     *(u32x4*)(rowp + bj * HALF) = w; } }
;     }
; template <class Epi, class Sched, bool FP8 = false>
; __device__ __forceinline__ void gemm_phase(LAS unsigned char* lds, const int Kb, const int nt  , const Sched& S, const Epi& E) {
;     ...
;             PG8_LDB(B0, B08, 1, 0); PG8_SCHED; PG8_LDA(1, 0); PG8_STAGE(PG8_SA(0, 1), a2 + hstep, voffA);
;             PG8_WAIT_L(8); PG8_BAR; PG8_HI; PG8_WAIT_L(0); PG8_MMA(0, 0, B0, B08); PG8_BAR; PG8_LO; PG8_SCHED;
;             PG8_LDB(B1, B18, 1, 1); PG8_STAGE(PG8_SB(1, 0), b3, voffB);
;             PG8_BAR; PG8_HI; PG8_WAIT_L(0); PG8_MMA(0, 1, B1, B18); PG8_BAR; PG8_LO;
;             PG8_LDA(1, 1); PG8_STAGE(PG8_SA(1, 0), a3, voffA);
;             PG8_BAR; PG8_HI; PG8_WAIT_L(0); PG8_MMA(1, 0, B0, B08); PG8_BAR; PG8_LO; PG8_SCHED;
;             PG8_STAGE(PG8_SB(1, 1), b3 + hstep, voffB);
;             PG8_WAIT_V(6); PG8_BAR; PG8_HI; PG8_MMA(1, 1, B1, B18); PG8_BAR; PG8_LO;
;         }
;         { int l_; asm volatile("v_mbcnt_lo_u32_b32 %0, -1, 0\n\tv_mbcnt_hi_u32_b32 %0, -1, %0" : "=v"(l_));
;           E(acc, cur, wr, wc, l_ & 15, l_ >> 4); }
	s_waitcnt lgkmcnt(0)
	s_setprio 1
	v_mfma_f32_16x16x128_f8f6f4 v[130:133], v[162:169], v[178:185], v[130:133]
	v_mfma_f32_16x16x128_f8f6f4 v[126:129], v[170:177], v[178:185], v[126:129]
	v_mfma_f32_16x16x128_f8f6f4 v[114:117], v[162:169], v[192:199], v[114:117]
	v_mfma_f32_16x16x128_f8f6f4 v[110:113], v[170:177], v[192:199], v[110:113]
	v_mfma_f32_16x16x128_f8f6f4 v[98:101], v[162:169], v[200:207], v[98:101]
	v_mfma_f32_16x16x128_f8f6f4 v[94:97], v[170:177], v[200:207], v[94:97]
	v_mfma_f32_16x16x128_f8f6f4 v[82:85], v[162:169], v[208:215], v[82:85]
	v_mfma_f32_16x16x128_f8f6f4 v[78:81], v[170:177], v[208:215], v[78:81]
	s_setprio 0
	s_barrier
	ds_read_b128 v[216:219], v155
	ds_read_b128 v[220:223], v156
	s_add_u32 s22, s26, 0x80
	s_addc_u32 s23, s27, 0
	ds_read_b128 v[224:227], v157
	ds_read_b128 v[228:231], v158
	s_mov_b32 s76, m0
	s_mov_b32 m0, s57
	s_nop 0
	global_load_lds_dwordx4 v142, s[22:23]
	s_mov_b32 m0, s76
	s_add_u32 s22, s26, 0x70080
	s_addc_u32 s23, s27, 0
	s_mov_b32 s76, m0
	s_mov_b32 m0, s58
	s_nop 0
	global_load_lds_dwordx4 v142, s[22:23]
	s_mov_b32 m0, s76
	s_barrier
	s_waitcnt lgkmcnt(0)
	s_setprio 1
	v_mfma_f32_16x16x128_f8f6f4 v[122:125], v[216:223], v[178:185], v[122:125]
	v_mfma_f32_16x16x128_f8f6f4 v[118:121], v[224:231], v[178:185], v[118:121]
	v_mfma_f32_16x16x128_f8f6f4 v[106:109], v[216:223], v[192:199], v[106:109]
	v_mfma_f32_16x16x128_f8f6f4 v[102:105], v[224:231], v[192:199], v[102:105]
	v_mfma_f32_16x16x128_f8f6f4 v[90:93], v[216:223], v[200:207], v[90:93]
	v_mfma_f32_16x16x128_f8f6f4 v[86:89], v[224:231], v[200:207], v[86:89]
	v_mfma_f32_16x16x128_f8f6f4 v[74:77], v[216:223], v[208:215], v[74:77]
	v_mfma_f32_16x16x128_f8f6f4 v[70:73], v[224:231], v[208:215], v[70:73]
	s_setprio 0
	s_barrier
	ds_read_b128 v[178:181], v159 offset:49152
	ds_read_b128 v[182:185], v159 offset:50176
	ds_read_b128 v[192:195], v159 offset:51200
	ds_read_b128 v[196:199], v159 offset:52224
	ds_read_b128 v[200:203], v159 offset:53248
	ds_read_b128 v[204:207], v159 offset:54272
	ds_read_b128 v[208:211], v159 offset:55296
	ds_read_b128 v[212:215], v159 offset:56320
	s_mov_b32 s22, m0
	s_mov_b32 m0, s59
	s_nop 0
	global_load_lds_dwordx4 v138, s[30:31]
	s_mov_b32 m0, s22
	s_add_u32 s22, s28, 0x70080
	s_addc_u32 s23, s29, 0
	s_mov_b32 s28, m0
	s_mov_b32 m0, s60
	s_nop 0
	global_load_lds_dwordx4 v138, s[22:23]
	s_mov_b32 m0, s28
	s_barrier
	s_waitcnt lgkmcnt(0)
	s_setprio 1
	v_mfma_f32_16x16x128_f8f6f4 v[66:69], v[162:169], v[178:185], v[66:69]
	v_mfma_f32_16x16x128_f8f6f4 v[62:65], v[170:177], v[178:185], v[62:65]
	v_mfma_f32_16x16x128_f8f6f4 v[54:57], v[162:169], v[192:199], v[54:57]
	v_mfma_f32_16x16x128_f8f6f4 v[46:49], v[170:177], v[192:199], v[46:49]
	v_mfma_f32_16x16x128_f8f6f4 v[38:41], v[162:169], v[200:207], v[38:41]
	v_mfma_f32_16x16x128_f8f6f4 v[30:33], v[170:177], v[200:207], v[30:33]
	v_mfma_f32_16x16x128_f8f6f4 v[22:25], v[162:169], v[208:215], v[22:25]
	v_mfma_f32_16x16x128_f8f6f4 v[14:17], v[170:177], v[208:215], v[14:17]
	s_setprio 0
	s_barrier
	s_add_u32 s22, s26, 0xe0080
	s_addc_u32 s23, s27, 0
	s_mov_b32 s28, m0
	s_mov_b32 m0, s61
	s_nop 0
	global_load_lds_dwordx4 v142, s[22:23]
	s_mov_b32 m0, s28
	s_add_u32 s22, s26, 0x150080
	s_addc_u32 s23, s27, 0
	s_mov_b32 s26, m0
	s_mov_b32 m0, s62
	s_nop 0
	global_load_lds_dwordx4 v142, s[22:23]
	s_mov_b32 m0, s26
	s_add_i32 s75, s75, 2
	s_add_u32 s73, s73, 0x100
	s_addc_u32 s74, s74, 0
	s_cmp_gt_u32 s75, 53
	s_mov_b64 s[22:23], s[24:25]
	s_waitcnt vmcnt(6)
	s_barrier
	s_setprio 1
	v_mfma_f32_16x16x128_f8f6f4 v[58:61], v[216:223], v[178:185], v[58:61]
	v_mfma_f32_16x16x128_f8f6f4 v[50:53], v[224:231], v[178:185], v[50:53]
	v_mfma_f32_16x16x128_f8f6f4 v[42:45], v[216:223], v[192:199], v[42:45]
	v_mfma_f32_16x16x128_f8f6f4 v[34:37], v[224:231], v[192:199], v[34:37]
	v_mfma_f32_16x16x128_f8f6f4 v[26:29], v[216:223], v[200:207], v[26:29]
	v_mfma_f32_16x16x128_f8f6f4 v[18:21], v[224:231], v[200:207], v[18:21]
	v_mfma_f32_16x16x128_f8f6f4 v[10:13], v[216:223], v[208:215], v[10:13]
	v_mfma_f32_16x16x128_f8f6f4 v[2:5], v[224:231], v[208:215], v[2:5]
	s_setprio 0
	s_barrier
	s_cbranch_scc0 .LBB0_2837
	s_lshl_b32 s22, s72, 8
	v_mbcnt_lo_u32_b32 v6, -1, 0
	v_mbcnt_hi_u32_b32 v6, -1, v6
	s_add_i32 s22, s22, s54
	v_and_or_b32 v8, v6, 15, s22
	s_lshl_b32 s22, s71, 8
	v_ashrrev_i32_e32 v6, 1, v6
	s_or_b32 s22, s22, s55
	v_and_b32_e32 v6, -8, v6
	v_add_u32_e32 v6, s22, v6
	v_ashrrev_i32_e32 v9, 31, v8
	v_ashrrev_i32_e32 v7, 31, v6
	v_lshlrev_b64 v[134:135], 12, v[8:9]
	v_lshl_add_u64 v[134:135], s[4:5], 0, v[134:135]
	v_lshlrev_b64 v[136:137], 1, v[6:7]
	v_lshl_add_u64 v[6:7], v[134:135], 0, v[136:137]
	v_pk_mul_f32 v[132:133], v[132:133], s[6:7] op_sel_hi:[1,0]
	v_pk_mul_f32 v[130:131], v[130:131], s[6:7] op_sel_hi:[1,0]
	v_pk_mul_f32 v[134:135], v[128:129], s[6:7] op_sel_hi:[1,0]
	v_pk_mul_f32 v[128:129], v[126:127], s[6:7] op_sel_hi:[1,0]
	v_cvt_pk_bf16_f32 v126, v130, v131
	v_cvt_pk_bf16_f32 v127, v132, v133
	v_pk_mul_f32 v[122:123], v[122:123], s[6:7] op_sel_hi:[1,0]
	v_cvt_pk_bf16_f32 v128, v128, v129
	v_cvt_pk_bf16_f32 v129, v134, v135
	global_store_dwordx4 v[6:7], v[126:129], off
	v_pk_mul_f32 v[124:125], v[124:125], s[6:7] op_sel_hi:[1,0]
	v_pk_mul_f32 v[116:117], v[116:117], s[6:7] op_sel_hi:[1,0]
	v_pk_mul_f32 v[126:127], v[120:121], s[6:7] op_sel_hi:[1,0]
	v_pk_mul_f32 v[120:121], v[118:119], s[6:7] op_sel_hi:[1,0]
	v_cvt_pk_bf16_f32 v118, v122, v123
	v_cvt_pk_bf16_f32 v119, v124, v125
	v_pk_mul_f32 v[114:115], v[114:115], s[6:7] op_sel_hi:[1,0]
	v_cvt_pk_bf16_f32 v120, v120, v121
	v_cvt_pk_bf16_f32 v121, v126, v127
	global_store_dwordx4 v[6:7], v[118:121], off offset:256
; __device__ __forceinline__ unsigned cvt_pk_bf16(float lo, float hi) { unsigned r; asm volatile("v_cvt_pk_bf16_f32 %0, %1, %2" : "=v"(r) : "v"(lo), "v"(hi)); return r; }
;     __device__ __forceinline__ void operator()(const f32x4 (&acc)[2][2][4][2], const Unit& u, int wr, int wc, int fr, int fq) const {
;         const int row0 = u.pm * BM + wr * 64 + fr, col0 = u.pn * BM + wc * 32 + 8 * fq;
; #pragma unroll
;         for (int ai = 0; ai < 2; ++ai)
; #pragma unroll
;             for (int m = 0; m < 4; ++m) { bf16_t* rowp = O + (size_t)(row0 + ai * HALF + m * 16) * ldc + col0;
; #pragma unroll
;                 for (int bj = 0; bj < 2; ++bj) { const f32x4 v0 = acc[ai][bj][m][0] * scale, v1 = acc[ai][bj][m][1] * scale;
;                     u32x4 w; w.x = cvt_pk_bf16(v0[0], v0[1]); w.y = cvt_pk_bf16(v0[2], v0[3]); w.z = cvt_pk_bf16(v1[0], v1[1]); w.w = cvt_pk_bf16(v1[2], v1[3]);
;                     *(u32x4*)(rowp + bj * HALF) = w; } }
;     }
	v_pk_mul_f32 v[106:107], v[106:107], s[6:7] op_sel_hi:[1,0]
	v_pk_mul_f32 v[108:109], v[108:109], s[6:7] op_sel_hi:[1,0]
	v_or_b32_e32 v118, 16, v8
	v_ashrrev_i32_e32 v119, 31, v118
	v_lshlrev_b64 v[118:119], 12, v[118:119]
	v_lshl_add_u64 v[118:119], s[4:5], 0, v[118:119]
	v_lshl_add_u64 v[118:119], v[118:119], 0, v[136:137]
	v_pk_mul_f32 v[120:121], v[112:113], s[6:7] op_sel_hi:[1,0]
	v_pk_mul_f32 v[112:113], v[110:111], s[6:7] op_sel_hi:[1,0]
	v_cvt_pk_bf16_f32 v110, v114, v115
	v_cvt_pk_bf16_f32 v111, v116, v117
	v_pk_mul_f32 v[100:101], v[100:101], s[6:7] op_sel_hi:[1,0]
	v_cvt_pk_bf16_f32 v112, v112, v113
	v_cvt_pk_bf16_f32 v113, v120, v121
	global_store_dwordx4 v[118:119], v[110:113], off
	v_pk_mul_f32 v[98:99], v[98:99], s[6:7] op_sel_hi:[1,0]
	v_pk_mul_f32 v[92:93], v[92:93], s[6:7] op_sel_hi:[1,0]
	v_pk_mul_f32 v[110:111], v[104:105], s[6:7] op_sel_hi:[1,0]
	v_pk_mul_f32 v[104:105], v[102:103], s[6:7] op_sel_hi:[1,0]
	v_cvt_pk_bf16_f32 v102, v106, v107
	v_cvt_pk_bf16_f32 v103, v108, v109
	v_pk_mul_f32 v[90:91], v[90:91], s[6:7] op_sel_hi:[1,0]
	v_cvt_pk_bf16_f32 v104, v104, v105
	v_cvt_pk_bf16_f32 v105, v110, v111
	global_store_dwordx4 v[118:119], v[102:105], off offset:256
	v_pk_mul_f32 v[84:85], v[84:85], s[6:7] op_sel_hi:[1,0]
	v_pk_mul_f32 v[82:83], v[82:83], s[6:7] op_sel_hi:[1,0]
	v_or_b32_e32 v102, 32, v8
	v_ashrrev_i32_e32 v103, 31, v102
	v_lshlrev_b64 v[102:103], 12, v[102:103]
	v_or_b32_e32 v8, 48, v8
	v_lshl_add_u64 v[102:103], s[4:5], 0, v[102:103]
	v_ashrrev_i32_e32 v9, 31, v8
	v_lshl_add_u64 v[102:103], v[102:103], 0, v[136:137]
	v_pk_mul_f32 v[104:105], v[96:97], s[6:7] op_sel_hi:[1,0]
	v_pk_mul_f32 v[96:97], v[94:95], s[6:7] op_sel_hi:[1,0]
	v_cvt_pk_bf16_f32 v94, v98, v99
	v_cvt_pk_bf16_f32 v95, v100, v101
	v_lshlrev_b64 v[8:9], 12, v[8:9]
	v_cvt_pk_bf16_f32 v96, v96, v97
	v_cvt_pk_bf16_f32 v97, v104, v105
	global_store_dwordx4 v[102:103], v[94:97], off
	v_lshl_add_u64 v[8:9], s[4:5], 0, v[8:9]
	v_lshl_add_u64 v[8:9], v[8:9], 0, v[136:137]
	v_pk_mul_f32 v[94:95], v[88:89], s[6:7] op_sel_hi:[1,0]
	v_pk_mul_f32 v[88:89], v[86:87], s[6:7] op_sel_hi:[1,0]
	v_cvt_pk_bf16_f32 v86, v90, v91
	v_cvt_pk_bf16_f32 v87, v92, v93
	v_pk_mul_f32 v[76:77], v[76:77], s[6:7] op_sel_hi:[1,0]
	v_cvt_pk_bf16_f32 v88, v88, v89
	v_cvt_pk_bf16_f32 v89, v94, v95
	global_store_dwordx4 v[102:103], v[86:89], off offset:256
	v_pk_mul_f32 v[74:75], v[74:75], s[6:7] op_sel_hi:[1,0]
	v_pk_mul_f32 v[66:67], v[66:67], s[6:7] op_sel_hi:[1,0]
	v_pk_mul_f32 v[86:87], v[80:81], s[6:7] op_sel_hi:[1,0]
	v_pk_mul_f32 v[80:81], v[78:79], s[6:7] op_sel_hi:[1,0]
	v_cvt_pk_bf16_f32 v78, v82, v83
	v_cvt_pk_bf16_f32 v79, v84, v85
	v_pk_mul_f32 v[68:69], v[68:69], s[6:7] op_sel_hi:[1,0]
	v_cvt_pk_bf16_f32 v80, v80, v81
	v_cvt_pk_bf16_f32 v81, v86, v87
	global_store_dwordx4 v[8:9], v[78:81], off
	v_pk_mul_f32 v[60:61], v[60:61], s[6:7] op_sel_hi:[1,0]
	v_pk_mul_f32 v[58:59], v[58:59], s[6:7] op_sel_hi:[1,0]
	v_pk_mul_f32 v[78:79], v[72:73], s[6:7] op_sel_hi:[1,0]
	v_pk_mul_f32 v[72:73], v[70:71], s[6:7] op_sel_hi:[1,0]
	v_cvt_pk_bf16_f32 v70, v74, v75
	v_cvt_pk_bf16_f32 v71, v76, v77
	v_pk_mul_f32 v[44:45], v[44:45], s[6:7] op_sel_hi:[1,0]
	v_cvt_pk_bf16_f32 v72, v72, v73
	v_cvt_pk_bf16_f32 v73, v78, v79
	global_store_dwordx4 v[8:9], v[70:73], off offset:256
	v_lshl_add_u64 v[8:9], v[6:7], 0, s[8:9]
	v_pk_mul_f32 v[42:43], v[42:43], s[6:7] op_sel_hi:[1,0]
	v_pk_mul_f32 v[70:71], v[64:65], s[6:7] op_sel_hi:[1,0]
	v_pk_mul_f32 v[64:65], v[62:63], s[6:7] op_sel_hi:[1,0]
	v_cvt_pk_bf16_f32 v62, v66, v67
	v_add_co_u32_e32 v66, vcc, s65, v6
	v_cvt_pk_bf16_f32 v63, v68, v69
	v_cvt_pk_bf16_f32 v64, v64, v65
	v_cvt_pk_bf16_f32 v65, v70, v71
	v_pk_mul_f32 v[28:29], v[28:29], s[6:7] op_sel_hi:[1,0]
	s_nop 0
	v_addc_co_u32_e32 v67, vcc, 0, v7, vcc
	global_store_dwordx4 v[66:67], v[62:65], off
	v_pk_mul_f32 v[26:27], v[26:27], s[6:7] op_sel_hi:[1,0]
	s_mov_b32 s71, s69
	v_pk_mul_f32 v[62:63], v[52:53], s[6:7] op_sel_hi:[1,0]
	v_pk_mul_f32 v[52:53], v[50:51], s[6:7] op_sel_hi:[1,0]
	v_cvt_pk_bf16_f32 v50, v58, v59
	v_cvt_pk_bf16_f32 v51, v60, v61
	s_mov_b32 s72, s70
	v_cvt_pk_bf16_f32 v52, v52, v53
	v_cvt_pk_bf16_f32 v53, v62, v63
	global_store_dwordx4 v[8:9], v[50:53], off offset:256
	v_lshl_add_u64 v[8:9], v[6:7], 0, s[10:11]
	s_mov_b64 s[24:25], s[20:21]
	v_pk_mul_f32 v[50:51], v[56:57], s[6:7] op_sel_hi:[1,0]
	v_pk_mul_f32 v[52:53], v[54:55], s[6:7] op_sel_hi:[1,0]
	v_pk_mul_f32 v[54:55], v[48:49], s[6:7] op_sel_hi:[1,0]
	v_pk_mul_f32 v[48:49], v[46:47], s[6:7] op_sel_hi:[1,0]
	v_cvt_pk_bf16_f32 v46, v52, v53
	v_cvt_pk_bf16_f32 v47, v50, v51
	v_add_co_u32_e32 v50, vcc, s66, v6
	v_cvt_pk_bf16_f32 v48, v48, v49
	v_cvt_pk_bf16_f32 v49, v54, v55
	s_mov_b64 s[22:23], s[18:19]
	s_nop 0
	v_addc_co_u32_e32 v51, vcc, 0, v7, vcc
	global_store_dwordx4 v[50:51], v[46:49], off
	v_pk_mul_f32 v[10:11], v[10:11], s[6:7] op_sel_hi:[1,0]
	s_nop 0
	v_pk_mul_f32 v[46:47], v[36:37], s[6:7] op_sel_hi:[1,0]
	v_pk_mul_f32 v[36:37], v[34:35], s[6:7] op_sel_hi:[1,0]
	v_cvt_pk_bf16_f32 v34, v42, v43
	v_cvt_pk_bf16_f32 v35, v44, v45
	s_nop 0
	v_cvt_pk_bf16_f32 v36, v36, v37
	v_cvt_pk_bf16_f32 v37, v46, v47
	global_store_dwordx4 v[8:9], v[34:37], off offset:256
	v_lshl_add_u64 v[8:9], v[6:7], 0, s[12:13]
	s_nop 0
	v_pk_mul_f32 v[34:35], v[40:41], s[6:7] op_sel_hi:[1,0]
	v_pk_mul_f32 v[36:37], v[38:39], s[6:7] op_sel_hi:[1,0]
	v_pk_mul_f32 v[38:39], v[32:33], s[6:7] op_sel_hi:[1,0]
	v_pk_mul_f32 v[32:33], v[30:31], s[6:7] op_sel_hi:[1,0]
	v_cvt_pk_bf16_f32 v30, v36, v37
	v_cvt_pk_bf16_f32 v31, v34, v35
	v_add_co_u32_e32 v34, vcc, s67, v6
	v_cvt_pk_bf16_f32 v32, v32, v33
	v_cvt_pk_bf16_f32 v33, v38, v39
	s_nop 1
	v_addc_co_u32_e32 v35, vcc, 0, v7, vcc
	global_store_dwordx4 v[34:35], v[30:33], off
	s_nop 1
	v_pk_mul_f32 v[30:31], v[20:21], s[6:7] op_sel_hi:[1,0]
	v_pk_mul_f32 v[20:21], v[18:19], s[6:7] op_sel_hi:[1,0]
	v_cvt_pk_bf16_f32 v18, v26, v27
	v_cvt_pk_bf16_f32 v19, v28, v29
	s_nop 0
	v_cvt_pk_bf16_f32 v20, v20, v21
	v_cvt_pk_bf16_f32 v21, v30, v31
	global_store_dwordx4 v[8:9], v[18:21], off offset:256
	v_lshl_add_u64 v[8:9], v[6:7], 0, s[14:15]
	v_add_co_u32_e32 v6, vcc, s68, v6
	v_pk_mul_f32 v[20:21], v[22:23], s[6:7] op_sel_hi:[1,0]
	v_pk_mul_f32 v[22:23], v[16:17], s[6:7] op_sel_hi:[1,0]
	v_pk_mul_f32 v[16:17], v[14:15], s[6:7] op_sel_hi:[1,0]
	v_addc_co_u32_e32 v7, vcc, 0, v7, vcc
	v_pk_mul_f32 v[18:19], v[24:25], s[6:7] op_sel_hi:[1,0]
	v_cvt_pk_bf16_f32 v14, v20, v21
	s_and_b64 vcc, exec, s[16:17]
	v_cvt_pk_bf16_f32 v15, v18, v19
	v_cvt_pk_bf16_f32 v16, v16, v17
	v_cvt_pk_bf16_f32 v17, v22, v23
	global_store_dwordx4 v[6:7], v[14:17], off
	v_pk_mul_f32 v[6:7], v[12:13], s[6:7] op_sel_hi:[1,0]
	v_pk_mul_f32 v[12:13], v[4:5], s[6:7] op_sel_hi:[1,0]
	v_pk_mul_f32 v[4:5], v[2:3], s[6:7] op_sel_hi:[1,0]
	v_cvt_pk_bf16_f32 v2, v10, v11
	v_cvt_pk_bf16_f32 v3, v6, v7
	s_nop 0
	v_cvt_pk_bf16_f32 v4, v4, v5
	v_cvt_pk_bf16_f32 v5, v12, v13
	global_store_dwordx4 v[8:9], v[2:5], off offset:256
	s_cbranch_vccz .LBB0_2834
; #define PG8_WAIT_V(n) asm volatile("s_waitcnt vmcnt(" #n ")" ::: "memory")
; #define PG8_BAR __builtin_amdgcn_s_barrier()
; template <class Epi, class Sched, bool FP8 = false>
; __device__ __forceinline__ void gemm_phase(LAS unsigned char* lds, const int Kb, const int nt  , const Sched& S, const Epi& E) {
;     ...
;     PG8_WAIT_V(0);
;     if (wr == 0) PG8_BAR;
;     PG8_BAR;
	s_waitcnt vmcnt(0)
	s_cmpk_gt_u32 s3, 0xff
	s_cbranch_scc1 .LBB0_2841
	s_barrier

; #define PG8_STAGE(bufoff, gbase, voff) do { _Pragma("unroll") for (int _i = 0; _i < 2; ++_i) glds16_s((const void*)((const char*)(gbase) + _i * r64), (voff), ldsb + (unsigned)(bufoff) + ldsw + _i * 8192u); } while (0)
; #define PG8_LDA(b, h) do { _Pragma("unroll") for (int m = 0; m < 4; ++m) { const int o_ = PG8_SA(b, h) + aoff + m * 2048; \
;         if constexpr (FP8) A8[m] = PG8_CAT8(o_); else { At[m][0] = PG8_LD16(o_); At[m][1] = PG8_LD16(o_ + 1024); } } } while (0)
; #define PG8_LDB(X, X8, b, h) do { _Pragma("unroll") for (int n = 0; n < 2; ++n) { const int o_ = PG8_SB(b, h) + boff + n * 2048; \
;         if constexpr (FP8) X8[n] = PG8_CAT8(o_); else { X[n][0] = PG8_LD16(o_); X[n][1] = PG8_LD16(o_ + 1024); } } } while (0)
; #define PG8_WAIT_V(n) asm volatile("s_waitcnt vmcnt(" #n ")" ::: "memory")
; #define PG8_WAIT_L(n) asm volatile("s_waitcnt lgkmcnt(" #n ")" ::: "memory")
; #define PG8_BAR __builtin_amdgcn_s_barrier()
; #define PG8_SCHED __builtin_amdgcn_sched_barrier(0)
; #define PG8_HI do { if constexpr (FP8) asm volatile("s_setprio 1"); } while (0)
; #define PG8_LO do { if constexpr (FP8) asm volatile("s_setprio 0"); } while (0)
; template <class Epi, class Sched, bool FP8 = false>
; __device__ __forceinline__ void gemm_phase(LAS unsigned char* lds, const int Kb, const int nt  , const Sched& S, const Epi& E) {
;     ...
;         for (int t = 0; t < nt; t += 2) {
;             const bool last = (t == nt - 2);
;             const char* a1 = cA + (size_t)(t + 1) * kstep;
;             const char* a2 = last ? nA : cA + (size_t)(t + 2) * kstep; const char* b2 = last ? nB : cB + (size_t)(t + 2) * kstep;
;             const char* a3 = a2 + kstep; const char* b3 = b2 + kstep;
;             PG8_LDB(B0, B08, 0, 0); PG8_SCHED; PG8_LDA(0, 0); PG8_STAGE(PG8_SA(1, 1), a1 + hstep, voffA);
;             PG8_WAIT_L(8); PG8_BAR; PG8_HI; PG8_WAIT_L(0); PG8_MMA(0, 0, B0, B08); PG8_BAR; PG8_LO; PG8_SCHED;
;             PG8_LDB(B1, B18, 0, 1); PG8_STAGE(PG8_SB(0, 0), b2, voffB);
;             PG8_BAR; PG8_HI; PG8_WAIT_L(0); PG8_MMA(0, 1, B1, B18); PG8_BAR; PG8_LO;
;             PG8_LDA(0, 1); PG8_STAGE(PG8_SA(0, 0), a2, voffA);
;             PG8_BAR; PG8_HI; PG8_WAIT_L(0); PG8_MMA(1, 0, B0, B08); PG8_BAR; PG8_LO; PG8_SCHED;
;             PG8_STAGE(PG8_SB(0, 1), b2 + hstep, voffB);
;             PG8_WAIT_V(6); PG8_BAR; PG8_HI; PG8_MMA(1, 1, B1, B18); PG8_BAR; PG8_LO;
.LBB0_2851:
	ds_read_b128 v[162:165], v143
	ds_read_b128 v[166:169], v144
	ds_read_b128 v[170:173], v145
	ds_read_b128 v[174:177], v146
	s_add_u32 s24, s22, 0x100
	s_addc_u32 s25, s23, 0
	s_cmp_eq_u32 s77, 52
	s_cselect_b32 s28, s18, s24
	s_cselect_b32 s29, s19, s25
	s_cselect_b32 s26, s20, s75
	s_cselect_b32 s27, s21, s76
	s_add_u32 s30, s28, 0x80
	s_addc_u32 s31, s29, 0
	ds_read_b128 v[178:181], v159
	ds_read_b128 v[182:185], v159 offset:1024
	ds_read_b128 v[192:195], v159 offset:2048
	ds_read_b128 v[196:199], v159 offset:3072
	ds_read_b128 v[200:203], v159 offset:4096
	ds_read_b128 v[204:207], v159 offset:5120
	ds_read_b128 v[208:211], v159 offset:6144
	ds_read_b128 v[212:215], v159 offset:7168
	s_add_u32 s78, s22, 0xe0080
	s_addc_u32 s79, s23, 0
	s_mov_b32 s80, m0
	s_mov_b32 m0, s65
	s_nop 0
	global_load_lds_dwordx4 v138, s[78:79]
	s_mov_b32 m0, s80
	s_add_u32 s22, s22, 0x150080
	s_addc_u32 s23, s23, 0
	s_mov_b32 s78, m0
	s_mov_b32 m0, s66
	s_nop 0
	global_load_lds_dwordx4 v138, s[22:23]
	s_mov_b32 m0, s78
	s_waitcnt lgkmcnt(8)
	s_barrier
	s_waitcnt lgkmcnt(0)
	s_setprio 1
	v_mfma_f32_16x16x128_f8f6f4 v[130:133], v[162:169], v[178:185], v[130:133]
	v_mfma_f32_16x16x128_f8f6f4 v[126:129], v[170:177], v[178:185], v[126:129]
	v_mfma_f32_16x16x128_f8f6f4 v[114:117], v[162:169], v[192:199], v[114:117]
	v_mfma_f32_16x16x128_f8f6f4 v[110:113], v[170:177], v[192:199], v[110:113]
	v_mfma_f32_16x16x128_f8f6f4 v[98:101], v[162:169], v[200:207], v[98:101]
	v_mfma_f32_16x16x128_f8f6f4 v[94:97], v[170:177], v[200:207], v[94:97]
	v_mfma_f32_16x16x128_f8f6f4 v[82:85], v[162:169], v[208:215], v[82:85]
	v_mfma_f32_16x16x128_f8f6f4 v[78:81], v[170:177], v[208:215], v[78:81]
	s_setprio 0
	s_barrier
	ds_read_b128 v[216:219], v147
	ds_read_b128 v[220:223], v148
	ds_read_b128 v[224:227], v149
	ds_read_b128 v[228:231], v150
	s_mov_b32 s22, m0
	s_mov_b32 m0, s51
	s_nop 0
	global_load_lds_dwordx4 v142, s[26:27]
	s_mov_b32 m0, s22
	s_add_u32 s22, s26, 0x70000
	s_addc_u32 s23, s27, 0
	s_mov_b32 s78, m0
	s_mov_b32 m0, s52
	s_nop 0
	global_load_lds_dwordx4 v142, s[22:23]
	s_mov_b32 m0, s78
	s_barrier
	s_waitcnt lgkmcnt(0)
	s_setprio 1
	v_mfma_f32_16x16x128_f8f6f4 v[122:125], v[216:223], v[178:185], v[122:125]
	v_mfma_f32_16x16x128_f8f6f4 v[118:121], v[224:231], v[178:185], v[118:121]
	v_mfma_f32_16x16x128_f8f6f4 v[106:109], v[216:223], v[192:199], v[106:109]
	v_mfma_f32_16x16x128_f8f6f4 v[102:105], v[224:231], v[192:199], v[102:105]
	v_mfma_f32_16x16x128_f8f6f4 v[90:93], v[216:223], v[200:207], v[90:93]
	v_mfma_f32_16x16x128_f8f6f4 v[86:89], v[224:231], v[200:207], v[86:89]
	v_mfma_f32_16x16x128_f8f6f4 v[74:77], v[216:223], v[208:215], v[74:77]
	v_mfma_f32_16x16x128_f8f6f4 v[70:73], v[224:231], v[208:215], v[70:73]
	s_setprio 0
	s_barrier
	ds_read_b128 v[178:181], v159 offset:16384
	ds_read_b128 v[182:185], v159 offset:17408
	ds_read_b128 v[192:195], v159 offset:18432
	ds_read_b128 v[196:199], v159 offset:19456
	ds_read_b128 v[200:203], v159 offset:20480
	ds_read_b128 v[204:207], v159 offset:21504
	ds_read_b128 v[208:211], v159 offset:22528
	ds_read_b128 v[212:215], v159 offset:23552
	s_mov_b32 s22, m0
	s_mov_b32 m0, s50
	s_nop 0
	global_load_lds_dwordx4 v138, s[28:29]
	s_mov_b32 m0, s22
	s_add_u32 s22, s28, 0x70000
	s_addc_u32 s23, s29, 0
	s_mov_b32 s78, m0
	s_mov_b32 m0, s53
	s_nop 0
	global_load_lds_dwordx4 v138, s[22:23]
	s_mov_b32 m0, s78
	s_barrier
	s_waitcnt lgkmcnt(0)
	s_setprio 1
	v_mfma_f32_16x16x128_f8f6f4 v[66:69], v[162:169], v[178:185], v[66:69]
	v_mfma_f32_16x16x128_f8f6f4 v[62:65], v[170:177], v[178:185], v[62:65]
	v_mfma_f32_16x16x128_f8f6f4 v[54:57], v[162:169], v[192:199], v[54:57]
	v_mfma_f32_16x16x128_f8f6f4 v[46:49], v[170:177], v[192:199], v[46:49]
	v_mfma_f32_16x16x128_f8f6f4 v[38:41], v[162:169], v[200:207], v[38:41]
	v_mfma_f32_16x16x128_f8f6f4 v[30:33], v[170:177], v[200:207], v[30:33]
	v_mfma_f32_16x16x128_f8f6f4 v[22:25], v[162:169], v[208:215], v[22:25]
	v_mfma_f32_16x16x128_f8f6f4 v[14:17], v[170:177], v[208:215], v[14:17]
	s_setprio 0
	s_barrier
	s_add_u32 s22, s26, 0xe0000
	s_addc_u32 s23, s27, 0
	s_mov_b32 s78, m0
	s_mov_b32 m0, s54
	s_nop 0
	global_load_lds_dwordx4 v142, s[22:23]
	s_mov_b32 m0, s78
	s_add_u32 s22, s26, 0x150000
	s_addc_u32 s23, s27, 0
	s_mov_b32 s78, m0
	s_mov_b32 m0, s55
	s_nop 0
	global_load_lds_dwordx4 v142, s[22:23]
	s_mov_b32 m0, s78
	s_waitcnt vmcnt(6)
	s_barrier
	s_setprio 1
	v_mfma_f32_16x16x128_f8f6f4 v[58:61], v[216:223], v[178:185], v[58:61]
	v_mfma_f32_16x16x128_f8f6f4 v[50:53], v[224:231], v[178:185], v[50:53]
	v_mfma_f32_16x16x128_f8f6f4 v[42:45], v[216:223], v[192:199], v[42:45]
	v_mfma_f32_16x16x128_f8f6f4 v[34:37], v[224:231], v[192:199], v[34:37]
	v_mfma_f32_16x16x128_f8f6f4 v[26:29], v[216:223], v[200:207], v[26:29]
	v_mfma_f32_16x16x128_f8f6f4 v[18:21], v[224:231], v[200:207], v[18:21]
	v_mfma_f32_16x16x128_f8f6f4 v[10:13], v[216:223], v[208:215], v[10:13]
	v_mfma_f32_16x16x128_f8f6f4 v[2:5], v[224:231], v[208:215], v[2:5]
	s_setprio 0
	s_barrier
	ds_read_b128 v[162:165], v151
	ds_read_b128 v[166:169], v152
	ds_read_b128 v[170:173], v153
	ds_read_b128 v[174:177], v154
	ds_read_b128 v[178:181], v159 offset:32768
	ds_read_b128 v[182:185], v159 offset:33792
	ds_read_b128 v[192:195], v159 offset:34816
	ds_read_b128 v[196:199], v159 offset:35840
	ds_read_b128 v[200:203], v159 offset:36864
	ds_read_b128 v[204:207], v159 offset:37888
	ds_read_b128 v[208:211], v159 offset:38912
	ds_read_b128 v[212:215], v159 offset:39936
	s_add_u32 s22, s28, 0xe0000
	s_addc_u32 s23, s29, 0
	s_mov_b32 s78, m0
	s_mov_b32 m0, s56
	s_nop 0
	global_load_lds_dwordx4 v138, s[22:23]
	s_mov_b32 m0, s78
	s_add_u32 s22, s28, 0x150000
	s_addc_u32 s23, s29, 0
	s_mov_b32 s78, m0
	s_mov_b32 m0, s57
	s_nop 0
	global_load_lds_dwordx4 v138, s[22:23]
	s_mov_b32 m0, s78
	s_waitcnt lgkmcnt(8)
	s_barrier
; __device__ __forceinline__ unsigned cvt_pk_bf16(float lo, float hi) { unsigned r; asm volatile("v_cvt_pk_bf16_f32 %0, %1, %2" : "=v"(r) : "v"(lo), "v"(hi)); return r; }
; #define PG8_STAGE(bufoff, gbase, voff) do { _Pragma("unroll") for (int _i = 0; _i < 2; ++_i) glds16_s((const void*)((const char*)(gbase) + _i * r64), (voff), ldsb + (unsigned)(bufoff) + ldsw + _i * 8192u); } while (0)
; #define PG8_WAIT_V(n) asm volatile("s_waitcnt vmcnt(" #n ")" ::: "memory")
; #define PG8_WAIT_L(n) asm volatile("s_waitcnt lgkmcnt(" #n ")" ::: "memory")
;     __device__ __forceinline__ void operator()(const f32x4 (&acc)[2][2][4][2], const Unit& u, int wr, int wc, int fr, int fq) const {
;         const int row0 = u.pm * BM + wr * 64 + fr, col0 = u.pn * BM + wc * 32 + 8 * fq;
; #pragma unroll
;         for (int ai = 0; ai < 2; ++ai)
; #pragma unroll
;             for (int m = 0; m < 4; ++m) { bf16_t* rowp = O + (size_t)(row0 + ai * HALF + m * 16) * ldc + col0;
; #pragma unroll
;                 for (int bj = 0; bj < 2; ++bj) { const f32x4 v0 = acc[ai][bj][m][0] * scale, v1 = acc[ai][bj][m][1] * scale;
;                     u32x4 w; w.x = cvt_pk_bf16(v0[0], v0[1]); w.y = cvt_pk_bf16(v0[2], v0[3]); w.z = cvt_pk_bf16(v1[0], v1[1]); w.w = cvt_pk_bf16(v1[2], v1[3]);
;                     *(u32x4*)(rowp + bj * HALF) = w; } }
;     }
; template <class Epi, class Sched, bool FP8 = false>
; __device__ __forceinline__ void gemm_phase(LAS unsigned char* lds, const int Kb, const int nt  , const Sched& S, const Epi& E) {
;     ...
;             PG8_LDB(B0, B08, 1, 0); PG8_SCHED; PG8_LDA(1, 0); PG8_STAGE(PG8_SA(0, 1), a2 + hstep, voffA);
;             PG8_WAIT_L(8); PG8_BAR; PG8_HI; PG8_WAIT_L(0); PG8_MMA(0, 0, B0, B08); PG8_BAR; PG8_LO; PG8_SCHED;
;             PG8_LDB(B1, B18, 1, 1); PG8_STAGE(PG8_SB(1, 0), b3, voffB);
;             PG8_BAR; PG8_HI; PG8_WAIT_L(0); PG8_MMA(0, 1, B1, B18); PG8_BAR; PG8_LO;
;             PG8_LDA(1, 1); PG8_STAGE(PG8_SA(1, 0), a3, voffA);
;             PG8_BAR; PG8_HI; PG8_WAIT_L(0); PG8_MMA(1, 0, B0, B08); PG8_BAR; PG8_LO; PG8_SCHED;
;             PG8_STAGE(PG8_SB(1, 1), b3 + hstep, voffB);
;             PG8_WAIT_V(6); PG8_BAR; PG8_HI; PG8_MMA(1, 1, B1, B18); PG8_BAR; PG8_LO;
;         }
;         { int l_; asm volatile("v_mbcnt_lo_u32_b32 %0, -1, 0\n\tv_mbcnt_hi_u32_b32 %0, -1, %0" : "=v"(l_));
;           E(acc, cur, wr, wc, l_ & 15, l_ >> 4); }
	s_waitcnt lgkmcnt(0)
	s_setprio 1
	v_mfma_f32_16x16x128_f8f6f4 v[130:133], v[162:169], v[178:185], v[130:133]
	v_mfma_f32_16x16x128_f8f6f4 v[126:129], v[170:177], v[178:185], v[126:129]
	v_mfma_f32_16x16x128_f8f6f4 v[114:117], v[162:169], v[192:199], v[114:117]
	v_mfma_f32_16x16x128_f8f6f4 v[110:113], v[170:177], v[192:199], v[110:113]
	v_mfma_f32_16x16x128_f8f6f4 v[98:101], v[162:169], v[200:207], v[98:101]
	v_mfma_f32_16x16x128_f8f6f4 v[94:97], v[170:177], v[200:207], v[94:97]
	v_mfma_f32_16x16x128_f8f6f4 v[82:85], v[162:169], v[208:215], v[82:85]
	v_mfma_f32_16x16x128_f8f6f4 v[78:81], v[170:177], v[208:215], v[78:81]
	s_setprio 0
	s_barrier
	ds_read_b128 v[216:219], v155
	ds_read_b128 v[220:223], v156
	s_add_u32 s22, s26, 0x80
	s_addc_u32 s23, s27, 0
	ds_read_b128 v[224:227], v157
	ds_read_b128 v[228:231], v158
	s_mov_b32 s78, m0
	s_mov_b32 m0, s59
	s_nop 0
	global_load_lds_dwordx4 v142, s[22:23]
	s_mov_b32 m0, s78
	s_add_u32 s22, s26, 0x70080
	s_addc_u32 s23, s27, 0
	s_mov_b32 s78, m0
	s_mov_b32 m0, s60
	s_nop 0
	global_load_lds_dwordx4 v142, s[22:23]
	s_mov_b32 m0, s78
	s_barrier
	s_waitcnt lgkmcnt(0)
	s_setprio 1
	v_mfma_f32_16x16x128_f8f6f4 v[122:125], v[216:223], v[178:185], v[122:125]
	v_mfma_f32_16x16x128_f8f6f4 v[118:121], v[224:231], v[178:185], v[118:121]
	v_mfma_f32_16x16x128_f8f6f4 v[106:109], v[216:223], v[192:199], v[106:109]
	v_mfma_f32_16x16x128_f8f6f4 v[102:105], v[224:231], v[192:199], v[102:105]
	v_mfma_f32_16x16x128_f8f6f4 v[90:93], v[216:223], v[200:207], v[90:93]
	v_mfma_f32_16x16x128_f8f6f4 v[86:89], v[224:231], v[200:207], v[86:89]
	v_mfma_f32_16x16x128_f8f6f4 v[74:77], v[216:223], v[208:215], v[74:77]
	v_mfma_f32_16x16x128_f8f6f4 v[70:73], v[224:231], v[208:215], v[70:73]
	s_setprio 0
	s_barrier
	ds_read_b128 v[178:181], v159 offset:49152
	ds_read_b128 v[182:185], v159 offset:50176
	ds_read_b128 v[192:195], v159 offset:51200
	ds_read_b128 v[196:199], v159 offset:52224
	ds_read_b128 v[200:203], v159 offset:53248
	ds_read_b128 v[204:207], v159 offset:54272
	ds_read_b128 v[208:211], v159 offset:55296
	ds_read_b128 v[212:215], v159 offset:56320
	s_mov_b32 s22, m0
	s_mov_b32 m0, s61
	s_nop 0
	global_load_lds_dwordx4 v138, s[30:31]
	s_mov_b32 m0, s22
	s_add_u32 s22, s28, 0x70080
	s_addc_u32 s23, s29, 0
	s_mov_b32 s28, m0
	s_mov_b32 m0, s62
	s_nop 0
	global_load_lds_dwordx4 v138, s[22:23]
	s_mov_b32 m0, s28
	s_barrier
	s_waitcnt lgkmcnt(0)
	s_setprio 1
	v_mfma_f32_16x16x128_f8f6f4 v[66:69], v[162:169], v[178:185], v[66:69]
	v_mfma_f32_16x16x128_f8f6f4 v[62:65], v[170:177], v[178:185], v[62:65]
	v_mfma_f32_16x16x128_f8f6f4 v[54:57], v[162:169], v[192:199], v[54:57]
	v_mfma_f32_16x16x128_f8f6f4 v[46:49], v[170:177], v[192:199], v[46:49]
	v_mfma_f32_16x16x128_f8f6f4 v[38:41], v[162:169], v[200:207], v[38:41]
	v_mfma_f32_16x16x128_f8f6f4 v[30:33], v[170:177], v[200:207], v[30:33]
	v_mfma_f32_16x16x128_f8f6f4 v[22:25], v[162:169], v[208:215], v[22:25]
	v_mfma_f32_16x16x128_f8f6f4 v[14:17], v[170:177], v[208:215], v[14:17]
	s_setprio 0
	s_barrier
	s_add_u32 s22, s26, 0xe0080
	s_addc_u32 s23, s27, 0
	s_mov_b32 s28, m0
	s_mov_b32 m0, s63
	s_nop 0
	global_load_lds_dwordx4 v142, s[22:23]
	s_mov_b32 m0, s28
	s_add_u32 s22, s26, 0x150080
	s_addc_u32 s23, s27, 0
	s_mov_b32 s26, m0
	s_mov_b32 m0, s64
	s_nop 0
	global_load_lds_dwordx4 v142, s[22:23]
	s_mov_b32 m0, s26
	s_add_i32 s77, s77, 2
	s_add_u32 s75, s75, 0x100
	s_addc_u32 s76, s76, 0
	s_cmp_gt_u32 s77, 53
	s_mov_b64 s[22:23], s[24:25]
	s_waitcnt vmcnt(6)
	s_barrier
	s_setprio 1
	v_mfma_f32_16x16x128_f8f6f4 v[58:61], v[216:223], v[178:185], v[58:61]
	v_mfma_f32_16x16x128_f8f6f4 v[50:53], v[224:231], v[178:185], v[50:53]
	v_mfma_f32_16x16x128_f8f6f4 v[42:45], v[216:223], v[192:199], v[42:45]
	v_mfma_f32_16x16x128_f8f6f4 v[34:37], v[224:231], v[192:199], v[34:37]
	v_mfma_f32_16x16x128_f8f6f4 v[26:29], v[216:223], v[200:207], v[26:29]
	v_mfma_f32_16x16x128_f8f6f4 v[18:21], v[224:231], v[200:207], v[18:21]
	v_mfma_f32_16x16x128_f8f6f4 v[10:13], v[216:223], v[208:215], v[10:13]
	v_mfma_f32_16x16x128_f8f6f4 v[2:5], v[224:231], v[208:215], v[2:5]
	s_setprio 0
	s_barrier
	s_cbranch_scc0 .LBB0_2851
	s_lshl_b32 s22, s74, 8
	v_mbcnt_lo_u32_b32 v6, -1, 0
	v_mbcnt_hi_u32_b32 v6, -1, v6
	s_add_i32 s22, s22, s3
	v_and_or_b32 v8, v6, 15, s22
	s_lshl_b32 s22, s73, 8
	v_ashrrev_i32_e32 v6, 1, v6
	s_or_b32 s22, s22, s58
	v_and_b32_e32 v6, -8, v6
	v_add_u32_e32 v6, s22, v6
	v_ashrrev_i32_e32 v9, 31, v8
	v_ashrrev_i32_e32 v7, 31, v6
	v_lshlrev_b64 v[134:135], 12, v[8:9]
	v_lshl_add_u64 v[134:135], s[4:5], 0, v[134:135]
	v_lshlrev_b64 v[136:137], 1, v[6:7]
	v_lshl_add_u64 v[6:7], v[134:135], 0, v[136:137]
	v_pk_mul_f32 v[132:133], v[132:133], s[6:7] op_sel_hi:[1,0]
	v_pk_mul_f32 v[130:131], v[130:131], s[6:7] op_sel_hi:[1,0]
	v_pk_mul_f32 v[134:135], v[128:129], s[6:7] op_sel_hi:[1,0]
	v_pk_mul_f32 v[128:129], v[126:127], s[6:7] op_sel_hi:[1,0]
	v_cvt_pk_bf16_f32 v126, v130, v131
	v_cvt_pk_bf16_f32 v127, v132, v133
	v_pk_mul_f32 v[122:123], v[122:123], s[6:7] op_sel_hi:[1,0]
	v_cvt_pk_bf16_f32 v128, v128, v129
	v_cvt_pk_bf16_f32 v129, v134, v135
	global_store_dwordx4 v[6:7], v[126:129], off
	v_pk_mul_f32 v[124:125], v[124:125], s[6:7] op_sel_hi:[1,0]
	v_pk_mul_f32 v[116:117], v[116:117], s[6:7] op_sel_hi:[1,0]
	v_pk_mul_f32 v[126:127], v[120:121], s[6:7] op_sel_hi:[1,0]
	v_pk_mul_f32 v[120:121], v[118:119], s[6:7] op_sel_hi:[1,0]
	v_cvt_pk_bf16_f32 v118, v122, v123
	v_cvt_pk_bf16_f32 v119, v124, v125
	v_pk_mul_f32 v[114:115], v[114:115], s[6:7] op_sel_hi:[1,0]
	v_cvt_pk_bf16_f32 v120, v120, v121
	v_cvt_pk_bf16_f32 v121, v126, v127
	global_store_dwordx4 v[6:7], v[118:121], off offset:256
; __device__ __forceinline__ unsigned cvt_pk_bf16(float lo, float hi) { unsigned r; asm volatile("v_cvt_pk_bf16_f32 %0, %1, %2" : "=v"(r) : "v"(lo), "v"(hi)); return r; }
;     __device__ __forceinline__ void operator()(const f32x4 (&acc)[2][2][4][2], const Unit& u, int wr, int wc, int fr, int fq) const {
;         const int row0 = u.pm * BM + wr * 64 + fr, col0 = u.pn * BM + wc * 32 + 8 * fq;
; #pragma unroll
;         for (int ai = 0; ai < 2; ++ai)
; #pragma unroll
;             for (int m = 0; m < 4; ++m) { bf16_t* rowp = O + (size_t)(row0 + ai * HALF + m * 16) * ldc + col0;
; #pragma unroll
;                 for (int bj = 0; bj < 2; ++bj) { const f32x4 v0 = acc[ai][bj][m][0] * scale, v1 = acc[ai][bj][m][1] * scale;
;                     u32x4 w; w.x = cvt_pk_bf16(v0[0], v0[1]); w.y = cvt_pk_bf16(v0[2], v0[3]); w.z = cvt_pk_bf16(v1[0], v1[1]); w.w = cvt_pk_bf16(v1[2], v1[3]);
;                     *(u32x4*)(rowp + bj * HALF) = w; } }
;     }
	v_pk_mul_f32 v[106:107], v[106:107], s[6:7] op_sel_hi:[1,0]
	v_pk_mul_f32 v[108:109], v[108:109], s[6:7] op_sel_hi:[1,0]
	v_or_b32_e32 v118, 16, v8
	v_ashrrev_i32_e32 v119, 31, v118
	v_lshlrev_b64 v[118:119], 12, v[118:119]
	v_lshl_add_u64 v[118:119], s[4:5], 0, v[118:119]
	v_lshl_add_u64 v[118:119], v[118:119], 0, v[136:137]
	v_pk_mul_f32 v[120:121], v[112:113], s[6:7] op_sel_hi:[1,0]
	v_pk_mul_f32 v[112:113], v[110:111], s[6:7] op_sel_hi:[1,0]
	v_cvt_pk_bf16_f32 v110, v114, v115
	v_cvt_pk_bf16_f32 v111, v116, v117
	v_pk_mul_f32 v[100:101], v[100:101], s[6:7] op_sel_hi:[1,0]
	v_cvt_pk_bf16_f32 v112, v112, v113
	v_cvt_pk_bf16_f32 v113, v120, v121
	global_store_dwordx4 v[118:119], v[110:113], off
	v_pk_mul_f32 v[98:99], v[98:99], s[6:7] op_sel_hi:[1,0]
	v_pk_mul_f32 v[92:93], v[92:93], s[6:7] op_sel_hi:[1,0]
	v_pk_mul_f32 v[110:111], v[104:105], s[6:7] op_sel_hi:[1,0]
	v_pk_mul_f32 v[104:105], v[102:103], s[6:7] op_sel_hi:[1,0]
	v_cvt_pk_bf16_f32 v102, v106, v107
	v_cvt_pk_bf16_f32 v103, v108, v109
	v_pk_mul_f32 v[90:91], v[90:91], s[6:7] op_sel_hi:[1,0]
	v_cvt_pk_bf16_f32 v104, v104, v105
	v_cvt_pk_bf16_f32 v105, v110, v111
	global_store_dwordx4 v[118:119], v[102:105], off offset:256
	v_pk_mul_f32 v[84:85], v[84:85], s[6:7] op_sel_hi:[1,0]
	v_pk_mul_f32 v[82:83], v[82:83], s[6:7] op_sel_hi:[1,0]
	v_or_b32_e32 v102, 32, v8
	v_ashrrev_i32_e32 v103, 31, v102
	v_lshlrev_b64 v[102:103], 12, v[102:103]
	v_or_b32_e32 v8, 48, v8
	v_lshl_add_u64 v[102:103], s[4:5], 0, v[102:103]
	v_ashrrev_i32_e32 v9, 31, v8
	v_lshl_add_u64 v[102:103], v[102:103], 0, v[136:137]
	v_pk_mul_f32 v[104:105], v[96:97], s[6:7] op_sel_hi:[1,0]
	v_pk_mul_f32 v[96:97], v[94:95], s[6:7] op_sel_hi:[1,0]
	v_cvt_pk_bf16_f32 v94, v98, v99
	v_cvt_pk_bf16_f32 v95, v100, v101
	v_lshlrev_b64 v[8:9], 12, v[8:9]
	v_cvt_pk_bf16_f32 v96, v96, v97
	v_cvt_pk_bf16_f32 v97, v104, v105
	global_store_dwordx4 v[102:103], v[94:97], off
	v_lshl_add_u64 v[8:9], s[4:5], 0, v[8:9]
	v_lshl_add_u64 v[8:9], v[8:9], 0, v[136:137]
	v_pk_mul_f32 v[94:95], v[88:89], s[6:7] op_sel_hi:[1,0]
	v_pk_mul_f32 v[88:89], v[86:87], s[6:7] op_sel_hi:[1,0]
	v_cvt_pk_bf16_f32 v86, v90, v91
	v_cvt_pk_bf16_f32 v87, v92, v93
	v_pk_mul_f32 v[76:77], v[76:77], s[6:7] op_sel_hi:[1,0]
	v_cvt_pk_bf16_f32 v88, v88, v89
	v_cvt_pk_bf16_f32 v89, v94, v95
	global_store_dwordx4 v[102:103], v[86:89], off offset:256
	v_pk_mul_f32 v[74:75], v[74:75], s[6:7] op_sel_hi:[1,0]
	v_pk_mul_f32 v[66:67], v[66:67], s[6:7] op_sel_hi:[1,0]
	v_pk_mul_f32 v[86:87], v[80:81], s[6:7] op_sel_hi:[1,0]
	v_pk_mul_f32 v[80:81], v[78:79], s[6:7] op_sel_hi:[1,0]
	v_cvt_pk_bf16_f32 v78, v82, v83
	v_cvt_pk_bf16_f32 v79, v84, v85
	v_pk_mul_f32 v[68:69], v[68:69], s[6:7] op_sel_hi:[1,0]
	v_cvt_pk_bf16_f32 v80, v80, v81
	v_cvt_pk_bf16_f32 v81, v86, v87
	global_store_dwordx4 v[8:9], v[78:81], off
	v_pk_mul_f32 v[60:61], v[60:61], s[6:7] op_sel_hi:[1,0]
	v_pk_mul_f32 v[58:59], v[58:59], s[6:7] op_sel_hi:[1,0]
	v_pk_mul_f32 v[78:79], v[72:73], s[6:7] op_sel_hi:[1,0]
	v_pk_mul_f32 v[72:73], v[70:71], s[6:7] op_sel_hi:[1,0]
	v_cvt_pk_bf16_f32 v70, v74, v75
	v_cvt_pk_bf16_f32 v71, v76, v77
	v_pk_mul_f32 v[44:45], v[44:45], s[6:7] op_sel_hi:[1,0]
	v_cvt_pk_bf16_f32 v72, v72, v73
	v_cvt_pk_bf16_f32 v73, v78, v79
	global_store_dwordx4 v[8:9], v[70:73], off offset:256
	v_lshl_add_u64 v[8:9], v[6:7], 0, s[8:9]
	v_pk_mul_f32 v[42:43], v[42:43], s[6:7] op_sel_hi:[1,0]
	v_pk_mul_f32 v[70:71], v[64:65], s[6:7] op_sel_hi:[1,0]
	v_pk_mul_f32 v[64:65], v[62:63], s[6:7] op_sel_hi:[1,0]
	v_cvt_pk_bf16_f32 v62, v66, v67
	v_add_co_u32_e32 v66, vcc, s67, v6
	v_cvt_pk_bf16_f32 v63, v68, v69
	v_cvt_pk_bf16_f32 v64, v64, v65
	v_cvt_pk_bf16_f32 v65, v70, v71
	v_pk_mul_f32 v[28:29], v[28:29], s[6:7] op_sel_hi:[1,0]
	s_nop 0
	v_addc_co_u32_e32 v67, vcc, 0, v7, vcc
	global_store_dwordx4 v[66:67], v[62:65], off
	v_pk_mul_f32 v[26:27], v[26:27], s[6:7] op_sel_hi:[1,0]
	s_mov_b32 s73, s71
	v_pk_mul_f32 v[62:63], v[52:53], s[6:7] op_sel_hi:[1,0]
	v_pk_mul_f32 v[52:53], v[50:51], s[6:7] op_sel_hi:[1,0]
	v_cvt_pk_bf16_f32 v50, v58, v59
	v_cvt_pk_bf16_f32 v51, v60, v61
	s_mov_b32 s74, s72
	v_cvt_pk_bf16_f32 v52, v52, v53
	v_cvt_pk_bf16_f32 v53, v62, v63
	global_store_dwordx4 v[8:9], v[50:53], off offset:256
	v_lshl_add_u64 v[8:9], v[6:7], 0, s[10:11]
	s_mov_b64 s[24:25], s[20:21]
	v_pk_mul_f32 v[50:51], v[56:57], s[6:7] op_sel_hi:[1,0]
	v_pk_mul_f32 v[52:53], v[54:55], s[6:7] op_sel_hi:[1,0]
	v_pk_mul_f32 v[54:55], v[48:49], s[6:7] op_sel_hi:[1,0]
	v_pk_mul_f32 v[48:49], v[46:47], s[6:7] op_sel_hi:[1,0]
	v_cvt_pk_bf16_f32 v46, v52, v53
	v_cvt_pk_bf16_f32 v47, v50, v51
	v_add_co_u32_e32 v50, vcc, s68, v6
	v_cvt_pk_bf16_f32 v48, v48, v49
	v_cvt_pk_bf16_f32 v49, v54, v55
	s_mov_b64 s[22:23], s[18:19]
	s_nop 0
	v_addc_co_u32_e32 v51, vcc, 0, v7, vcc
	global_store_dwordx4 v[50:51], v[46:49], off
	v_readlane_b32 s79, v241, 49
	v_pk_mul_f32 v[10:11], v[10:11], s[6:7] op_sel_hi:[1,0]
	v_pk_mul_f32 v[46:47], v[36:37], s[6:7] op_sel_hi:[1,0]
	v_pk_mul_f32 v[36:37], v[34:35], s[6:7] op_sel_hi:[1,0]
	v_cvt_pk_bf16_f32 v34, v42, v43
	v_cvt_pk_bf16_f32 v35, v44, v45
	s_nop 0
	v_cvt_pk_bf16_f32 v36, v36, v37
	v_cvt_pk_bf16_f32 v37, v46, v47
	global_store_dwordx4 v[8:9], v[34:37], off offset:256
	v_lshl_add_u64 v[8:9], v[6:7], 0, s[12:13]
	s_nop 0
	v_pk_mul_f32 v[34:35], v[40:41], s[6:7] op_sel_hi:[1,0]
	v_pk_mul_f32 v[36:37], v[38:39], s[6:7] op_sel_hi:[1,0]
	v_pk_mul_f32 v[38:39], v[32:33], s[6:7] op_sel_hi:[1,0]
	v_pk_mul_f32 v[32:33], v[30:31], s[6:7] op_sel_hi:[1,0]
	v_cvt_pk_bf16_f32 v30, v36, v37
	v_cvt_pk_bf16_f32 v31, v34, v35
	v_add_co_u32_e32 v34, vcc, s69, v6
	v_cvt_pk_bf16_f32 v32, v32, v33
	v_cvt_pk_bf16_f32 v33, v38, v39
	s_nop 1
	v_addc_co_u32_e32 v35, vcc, 0, v7, vcc
	global_store_dwordx4 v[34:35], v[30:33], off
	s_nop 1
	v_pk_mul_f32 v[30:31], v[20:21], s[6:7] op_sel_hi:[1,0]
	v_pk_mul_f32 v[20:21], v[18:19], s[6:7] op_sel_hi:[1,0]
	v_cvt_pk_bf16_f32 v18, v26, v27
	v_cvt_pk_bf16_f32 v19, v28, v29
	s_nop 0
	v_cvt_pk_bf16_f32 v20, v20, v21
	v_cvt_pk_bf16_f32 v21, v30, v31
	global_store_dwordx4 v[8:9], v[18:21], off offset:256
	v_lshl_add_u64 v[8:9], v[6:7], 0, s[14:15]
	v_add_co_u32_e32 v6, vcc, s70, v6
	v_pk_mul_f32 v[20:21], v[22:23], s[6:7] op_sel_hi:[1,0]
	v_pk_mul_f32 v[22:23], v[16:17], s[6:7] op_sel_hi:[1,0]
	v_pk_mul_f32 v[16:17], v[14:15], s[6:7] op_sel_hi:[1,0]
	v_addc_co_u32_e32 v7, vcc, 0, v7, vcc
	v_pk_mul_f32 v[18:19], v[24:25], s[6:7] op_sel_hi:[1,0]
	v_cvt_pk_bf16_f32 v14, v20, v21
	s_and_b64 vcc, exec, s[16:17]
	v_cvt_pk_bf16_f32 v15, v18, v19
	v_cvt_pk_bf16_f32 v16, v16, v17
	v_cvt_pk_bf16_f32 v17, v22, v23
	global_store_dwordx4 v[6:7], v[14:17], off
	v_pk_mul_f32 v[6:7], v[12:13], s[6:7] op_sel_hi:[1,0]
	v_pk_mul_f32 v[12:13], v[4:5], s[6:7] op_sel_hi:[1,0]
	v_pk_mul_f32 v[4:5], v[2:3], s[6:7] op_sel_hi:[1,0]
	v_cvt_pk_bf16_f32 v2, v10, v11
	v_cvt_pk_bf16_f32 v3, v6, v7
	s_nop 0
	v_cvt_pk_bf16_f32 v4, v4, v5
	v_cvt_pk_bf16_f32 v5, v12, v13
	global_store_dwordx4 v[8:9], v[2:5], off offset:256
	s_cbranch_vccz .LBB0_2848
; #define PG8_WAIT_V(n) asm volatile("s_waitcnt vmcnt(" #n ")" ::: "memory")
; #define PG8_BAR __builtin_amdgcn_s_barrier()
; template <class Epi, class Sched, bool FP8 = false>
; __device__ __forceinline__ void gemm_phase(LAS unsigned char* lds, const int Kb, const int nt  , const Sched& S, const Epi& E) {
;     ...
;     PG8_WAIT_V(0);
;     if (wr == 0) PG8_BAR;
;     PG8_BAR;
	s_waitcnt vmcnt(0)
	s_cmpk_gt_u32 s7, 0xff
	s_cbranch_scc1 .LBB0_2855
	s_barrier

; #define PG8_STAGE(bufoff, gbase, voff) do { _Pragma("unroll") for (int _i = 0; _i < 2; ++_i) glds16_s((const void*)((const char*)(gbase) + _i * r64), (voff), ldsb + (unsigned)(bufoff) + ldsw + _i * 8192u); } while (0)
; #define PG8_LDA(b, h) do { _Pragma("unroll") for (int m = 0; m < 4; ++m) { const int o_ = PG8_SA(b, h) + aoff + m * 2048; \
;         if constexpr (FP8) A8[m] = PG8_CAT8(o_); else { At[m][0] = PG8_LD16(o_); At[m][1] = PG8_LD16(o_ + 1024); } } } while (0)
; #define PG8_LDB(X, X8, b, h) do { _Pragma("unroll") for (int n = 0; n < 2; ++n) { const int o_ = PG8_SB(b, h) + boff + n * 2048; \
;         if constexpr (FP8) X8[n] = PG8_CAT8(o_); else { X[n][0] = PG8_LD16(o_); X[n][1] = PG8_LD16(o_ + 1024); } } } while (0)
; #define PG8_WAIT_V(n) asm volatile("s_waitcnt vmcnt(" #n ")" ::: "memory")
; #define PG8_WAIT_L(n) asm volatile("s_waitcnt lgkmcnt(" #n ")" ::: "memory")
; #define PG8_BAR __builtin_amdgcn_s_barrier()
; template <class Epi, class Sched, bool FP8 = false>
; __device__ __forceinline__ void gemm_phase(LAS unsigned char* lds, const int Kb, const int nt  , const Sched& S, const Epi& E) {
;     ...
;         for (int t = 0; t < nt; t += 2) {
;             const bool last = (t == nt - 2);
;             const char* a1 = cA + (size_t)(t + 1) * kstep;
;             const char* a2 = last ? nA : cA + (size_t)(t + 2) * kstep; const char* b2 = last ? nB : cB + (size_t)(t + 2) * kstep;
;             const char* a3 = a2 + kstep; const char* b3 = b2 + kstep;
;             PG8_LDB(B0, B08, 0, 0); PG8_SCHED; PG8_LDA(0, 0); PG8_STAGE(PG8_SA(1, 1), a1 + hstep, voffA);
;             PG8_WAIT_L(8); PG8_BAR; PG8_HI; PG8_WAIT_L(0); PG8_MMA(0, 0, B0, B08); PG8_BAR; PG8_LO; PG8_SCHED;
;             PG8_LDB(B1, B18, 0, 1); PG8_STAGE(PG8_SB(0, 0), b2, voffB);
;             PG8_BAR; PG8_HI; PG8_WAIT_L(0); PG8_MMA(0, 1, B1, B18); PG8_BAR; PG8_LO;
;             PG8_LDA(0, 1); PG8_STAGE(PG8_SA(0, 0), a2, voffA);
;             PG8_BAR; PG8_HI; PG8_WAIT_L(0); PG8_MMA(1, 0, B0, B08); PG8_BAR; PG8_LO; PG8_SCHED;
;             PG8_STAGE(PG8_SB(0, 1), b2 + hstep, voffB);
;             PG8_WAIT_V(6); PG8_BAR; PG8_HI; PG8_MMA(1, 1, B1, B18); PG8_BAR; PG8_LO;
;             PG8_LDB(B0, B08, 1, 0); PG8_SCHED; PG8_LDA(1, 0); PG8_STAGE(PG8_SA(0, 1), a2 + hstep, voffA);
;             PG8_WAIT_L(8); PG8_BAR; PG8_HI; PG8_WAIT_L(0); PG8_MMA(0, 0, B0, B08); PG8_BAR; PG8_LO; PG8_SCHED;
.LBB0_2865:
	ds_read_b128 v[156:159], v136
	ds_read_b128 v[160:163], v137
	ds_read_b128 v[164:167], v139
	ds_read_b128 v[168:171], v140
	s_add_u32 s24, s22, 0x100
	s_addc_u32 s25, s23, 0
	s_cmp_eq_u32 s73, 10
	s_cselect_b32 s28, s18, s24
	s_cselect_b32 s29, s19, s25
	s_cselect_b32 s26, s20, s71
	s_cselect_b32 s27, s21, s72
	s_add_u32 s30, s28, 0x80
	s_addc_u32 s31, s29, 0
	ds_read_b128 v[172:175], v153
	ds_read_b128 v[176:179], v153 offset:1024
	ds_read_b128 v[180:183], v153 offset:2048
	ds_read_b128 v[184:187], v153 offset:3072
	ds_read_b128 v[192:195], v153 offset:4096
	ds_read_b128 v[196:199], v153 offset:5120
	ds_read_b128 v[200:203], v153 offset:6144
	ds_read_b128 v[204:207], v153 offset:7168
	s_add_u32 s74, s22, 0xe0080
	s_addc_u32 s75, s23, 0
	s_mov_b32 s76, m0
	s_mov_b32 m0, s61
	s_nop 0
	global_load_lds_dwordx4 v138, s[74:75]
	s_mov_b32 m0, s76
	s_add_u32 s22, s22, 0x150080
	s_addc_u32 s23, s23, 0
	s_mov_b32 s74, m0
	s_mov_b32 m0, s62
	s_nop 0
	global_load_lds_dwordx4 v138, s[22:23]
	s_mov_b32 m0, s74
	s_waitcnt lgkmcnt(8)
	s_barrier
	s_waitcnt lgkmcnt(0)
	s_setprio 1
	v_mfma_f32_16x16x128_f8f6f4 v[128:131], v[156:163], v[172:179], v[128:131]
	v_mfma_f32_16x16x128_f8f6f4 v[124:127], v[164:171], v[172:179], v[124:127]
	v_mfma_f32_16x16x128_f8f6f4 v[116:119], v[156:163], v[180:187], v[116:119]
	v_mfma_f32_16x16x128_f8f6f4 v[108:111], v[164:171], v[180:187], v[108:111]
	v_mfma_f32_16x16x128_f8f6f4 v[100:103], v[156:163], v[192:199], v[100:103]
	v_mfma_f32_16x16x128_f8f6f4 v[92:95], v[164:171], v[192:199], v[92:95]
	v_mfma_f32_16x16x128_f8f6f4 v[84:87], v[156:163], v[200:207], v[84:87]
	v_mfma_f32_16x16x128_f8f6f4 v[76:79], v[164:171], v[200:207], v[76:79]
	s_setprio 0
	s_barrier
	ds_read_b128 v[208:211], v141
	ds_read_b128 v[212:215], v142
	ds_read_b128 v[216:219], v143
	ds_read_b128 v[220:223], v144
	s_mov_b32 s22, m0
	s_mov_b32 m0, s46
	s_nop 0
	global_load_lds_dwordx4 v138, s[26:27]
	s_mov_b32 m0, s22
	s_add_u32 s22, s26, 0x70000
	s_addc_u32 s23, s27, 0
	s_mov_b32 s74, m0
	s_mov_b32 m0, s47
	s_nop 0
	global_load_lds_dwordx4 v138, s[22:23]
	s_mov_b32 m0, s74
	s_barrier
	s_waitcnt lgkmcnt(0)
	s_setprio 1
	v_mfma_f32_16x16x128_f8f6f4 v[120:123], v[208:215], v[172:179], v[120:123]
	v_mfma_f32_16x16x128_f8f6f4 v[112:115], v[216:223], v[172:179], v[112:115]
	v_mfma_f32_16x16x128_f8f6f4 v[104:107], v[208:215], v[180:187], v[104:107]
	v_mfma_f32_16x16x128_f8f6f4 v[96:99], v[216:223], v[180:187], v[96:99]
	v_mfma_f32_16x16x128_f8f6f4 v[88:91], v[208:215], v[192:199], v[88:91]
	v_mfma_f32_16x16x128_f8f6f4 v[80:83], v[216:223], v[192:199], v[80:83]
	v_mfma_f32_16x16x128_f8f6f4 v[72:75], v[208:215], v[200:207], v[72:75]
	v_mfma_f32_16x16x128_f8f6f4 v[68:71], v[216:223], v[200:207], v[68:71]
	s_setprio 0
	s_barrier
	ds_read_b128 v[172:175], v153 offset:16384
	ds_read_b128 v[176:179], v153 offset:17408
	ds_read_b128 v[180:183], v153 offset:18432
	ds_read_b128 v[184:187], v153 offset:19456
	ds_read_b128 v[192:195], v153 offset:20480
	ds_read_b128 v[196:199], v153 offset:21504
	ds_read_b128 v[200:203], v153 offset:22528
	ds_read_b128 v[204:207], v153 offset:23552
	s_mov_b32 s22, m0
	s_mov_b32 m0, s45
	s_nop 0
	global_load_lds_dwordx4 v138, s[28:29]
	s_mov_b32 m0, s22
	s_add_u32 s22, s28, 0x70000
	s_addc_u32 s23, s29, 0
	s_mov_b32 s74, m0
	s_mov_b32 m0, s48
	s_nop 0
	global_load_lds_dwordx4 v138, s[22:23]
	s_mov_b32 m0, s74
	s_barrier
	s_waitcnt lgkmcnt(0)
	s_setprio 1
	v_mfma_f32_16x16x128_f8f6f4 v[64:67], v[156:163], v[172:179], v[64:67]
	v_mfma_f32_16x16x128_f8f6f4 v[60:63], v[164:171], v[172:179], v[60:63]
	v_mfma_f32_16x16x128_f8f6f4 v[56:59], v[156:163], v[180:187], v[56:59]
	v_mfma_f32_16x16x128_f8f6f4 v[48:51], v[164:171], v[180:187], v[48:51]
	v_mfma_f32_16x16x128_f8f6f4 v[40:43], v[156:163], v[192:199], v[40:43]
	v_mfma_f32_16x16x128_f8f6f4 v[32:35], v[164:171], v[192:199], v[32:35]
	v_mfma_f32_16x16x128_f8f6f4 v[24:27], v[156:163], v[200:207], v[24:27]
	v_mfma_f32_16x16x128_f8f6f4 v[12:15], v[164:171], v[200:207], v[12:15]
	s_setprio 0
	s_barrier
	s_add_u32 s22, s26, 0xe0000
	s_addc_u32 s23, s27, 0
	s_mov_b32 s74, m0
	s_mov_b32 m0, s49
	s_nop 0
	global_load_lds_dwordx4 v138, s[22:23]
	s_mov_b32 m0, s74
	s_add_u32 s22, s26, 0x150000
	s_addc_u32 s23, s27, 0
	s_mov_b32 s74, m0
	s_mov_b32 m0, s50
	s_nop 0
	global_load_lds_dwordx4 v138, s[22:23]
	s_mov_b32 m0, s74
	s_waitcnt vmcnt(6)
	s_barrier
	s_setprio 1
	v_mfma_f32_16x16x128_f8f6f4 v[52:55], v[208:215], v[172:179], v[52:55]
	v_mfma_f32_16x16x128_f8f6f4 v[44:47], v[216:223], v[172:179], v[44:47]
	v_mfma_f32_16x16x128_f8f6f4 v[36:39], v[208:215], v[180:187], v[36:39]
	v_mfma_f32_16x16x128_f8f6f4 v[28:31], v[216:223], v[180:187], v[28:31]
	v_mfma_f32_16x16x128_f8f6f4 v[20:23], v[208:215], v[192:199], v[20:23]
	v_mfma_f32_16x16x128_f8f6f4 v[16:19], v[216:223], v[192:199], v[16:19]
	v_mfma_f32_16x16x128_f8f6f4 v[8:11], v[208:215], v[200:207], v[8:11]
	v_mfma_f32_16x16x128_f8f6f4 v[0:3], v[216:223], v[200:207], v[0:3]
	s_setprio 0
	s_barrier
	ds_read_b128 v[156:159], v145
	ds_read_b128 v[160:163], v146
	ds_read_b128 v[164:167], v147
	ds_read_b128 v[168:171], v148
	ds_read_b128 v[172:175], v153 offset:32768
	ds_read_b128 v[176:179], v153 offset:33792
	ds_read_b128 v[180:183], v153 offset:34816
	ds_read_b128 v[184:187], v153 offset:35840
	ds_read_b128 v[192:195], v153 offset:36864
	ds_read_b128 v[196:199], v153 offset:37888
	ds_read_b128 v[200:203], v153 offset:38912
	ds_read_b128 v[204:207], v153 offset:39936
	s_add_u32 s22, s28, 0xe0000
	s_addc_u32 s23, s29, 0
	s_mov_b32 s74, m0
	s_mov_b32 m0, s51
	s_nop 0
	global_load_lds_dwordx4 v138, s[22:23]
	s_mov_b32 m0, s74
	s_add_u32 s22, s28, 0x150000
	s_addc_u32 s23, s29, 0
	s_mov_b32 s74, m0
	s_mov_b32 m0, s52
	s_nop 0
	global_load_lds_dwordx4 v138, s[22:23]
	s_mov_b32 m0, s74
	s_waitcnt lgkmcnt(8)
	s_barrier
; #define PG8_STAGE(bufoff, gbase, voff) do { _Pragma("unroll") for (int _i = 0; _i < 2; ++_i) glds16_s((const void*)((const char*)(gbase) + _i * r64), (voff), ldsb + (unsigned)(bufoff) + ldsw + _i * 8192u); } while (0)
; #define PG8_WAIT_V(n) asm volatile("s_waitcnt vmcnt(" #n ")" ::: "memory")
; #define PG8_WAIT_L(n) asm volatile("s_waitcnt lgkmcnt(" #n ")" ::: "memory")
; #define PG8_BAR __builtin_amdgcn_s_barrier()
;     __device__ __forceinline__ void operator()(const f32x4 (&acc)[2][2][4][2], const Unit& u, int wr, int wc, int fr, int fq) const {
;         const int row0 = u.pm * BM + wr * 64 + fr, col0 = u.pn * BM + wc * 32 + 4 * fq;
;         f32x4 cs[2][2];
; #pragma unroll
;         for (int bj = 0; bj < 2; ++bj)
; #pragma unroll
;             for (int n = 0; n < 2; ++n) cs[bj][n] = (cscale ? *(const f32x4*)(cscale + col0 + bj * HALF + n * 16) : (f32x4){1.f, 1.f, 1.f, 1.f}) * ascale;
; #pragma unroll
;         for (int ai = 0; ai < 2; ++ai)
; #pragma unroll
;             for (int m = 0; m < 4; ++m) { const size_t off = (size_t)(row0 + ai * HALF + m * 16) * ldc + col0;
; #pragma unroll
;                 for (int bj = 0; bj < 2; ++bj)
; #pragma unroll
;                     for (int n = 0; n < 2; ++n) { f32x4 v = acc[ai][bj][m][n] * cs[bj][n];
;                         if (res) v += *(const f32x4*)(res + off + bj * HALF + n * 16);
;                         *(f32x4*)(out + off + bj * HALF + n * 16) = v; }
; template <class Epi, class Sched, bool FP8 = false>
; __device__ __forceinline__ void gemm_phase(LAS unsigned char* lds, const int Kb, const int nt  , const Sched& S, const Epi& E) {
;     ...
;             PG8_WAIT_L(8); PG8_BAR; PG8_HI; PG8_WAIT_L(0); PG8_MMA(0, 0, B0, B08); PG8_BAR; PG8_LO; PG8_SCHED;
;             PG8_LDB(B1, B18, 1, 1); PG8_STAGE(PG8_SB(1, 0), b3, voffB);
;             PG8_BAR; PG8_HI; PG8_WAIT_L(0); PG8_MMA(0, 1, B1, B18); PG8_BAR; PG8_LO;
;             PG8_LDA(1, 1); PG8_STAGE(PG8_SA(1, 0), a3, voffA);
;             PG8_BAR; PG8_HI; PG8_WAIT_L(0); PG8_MMA(1, 0, B0, B08); PG8_BAR; PG8_LO; PG8_SCHED;
;             PG8_STAGE(PG8_SB(1, 1), b3 + hstep, voffB);
;             PG8_WAIT_V(6); PG8_BAR; PG8_HI; PG8_MMA(1, 1, B1, B18); PG8_BAR; PG8_LO;
;         }
;         { int l_; asm volatile("v_mbcnt_lo_u32_b32 %0, -1, 0\n\tv_mbcnt_hi_u32_b32 %0, -1, %0" : "=v"(l_));
;           E(acc, cur, wr, wc, l_ & 15, l_ >> 4); }
	s_waitcnt lgkmcnt(0)
	s_setprio 1
	v_mfma_f32_16x16x128_f8f6f4 v[128:131], v[156:163], v[172:179], v[128:131]
	v_mfma_f32_16x16x128_f8f6f4 v[124:127], v[164:171], v[172:179], v[124:127]
	v_mfma_f32_16x16x128_f8f6f4 v[116:119], v[156:163], v[180:187], v[116:119]
	v_mfma_f32_16x16x128_f8f6f4 v[108:111], v[164:171], v[180:187], v[108:111]
	v_mfma_f32_16x16x128_f8f6f4 v[100:103], v[156:163], v[192:199], v[100:103]
	v_mfma_f32_16x16x128_f8f6f4 v[92:95], v[164:171], v[192:199], v[92:95]
	v_mfma_f32_16x16x128_f8f6f4 v[84:87], v[156:163], v[200:207], v[84:87]
	v_mfma_f32_16x16x128_f8f6f4 v[76:79], v[164:171], v[200:207], v[76:79]
	s_setprio 0
	s_barrier
	ds_read_b128 v[208:211], v149
	ds_read_b128 v[212:215], v150
	s_add_u32 s22, s26, 0x80
	s_addc_u32 s23, s27, 0
	ds_read_b128 v[216:219], v151
	ds_read_b128 v[220:223], v152
	s_mov_b32 s74, m0
	s_mov_b32 m0, s55
	s_nop 0
	global_load_lds_dwordx4 v138, s[22:23]
	s_mov_b32 m0, s74
	s_add_u32 s22, s26, 0x70080
	s_addc_u32 s23, s27, 0
	s_mov_b32 s74, m0
	s_mov_b32 m0, s56
	s_nop 0
	global_load_lds_dwordx4 v138, s[22:23]
	s_mov_b32 m0, s74
	s_barrier
	s_waitcnt lgkmcnt(0)
	s_setprio 1
	v_mfma_f32_16x16x128_f8f6f4 v[120:123], v[208:215], v[172:179], v[120:123]
	v_mfma_f32_16x16x128_f8f6f4 v[112:115], v[216:223], v[172:179], v[112:115]
	v_mfma_f32_16x16x128_f8f6f4 v[104:107], v[208:215], v[180:187], v[104:107]
	v_mfma_f32_16x16x128_f8f6f4 v[96:99], v[216:223], v[180:187], v[96:99]
	v_mfma_f32_16x16x128_f8f6f4 v[88:91], v[208:215], v[192:199], v[88:91]
	v_mfma_f32_16x16x128_f8f6f4 v[80:83], v[216:223], v[192:199], v[80:83]
	v_mfma_f32_16x16x128_f8f6f4 v[72:75], v[208:215], v[200:207], v[72:75]
	v_mfma_f32_16x16x128_f8f6f4 v[68:71], v[216:223], v[200:207], v[68:71]
	s_setprio 0
	s_barrier
	ds_read_b128 v[172:175], v153 offset:49152
	ds_read_b128 v[176:179], v153 offset:50176
	ds_read_b128 v[180:183], v153 offset:51200
	ds_read_b128 v[184:187], v153 offset:52224
	ds_read_b128 v[192:195], v153 offset:53248
	ds_read_b128 v[196:199], v153 offset:54272
	ds_read_b128 v[200:203], v153 offset:55296
	ds_read_b128 v[204:207], v153 offset:56320
	s_mov_b32 s22, m0
	s_mov_b32 m0, s57
	s_nop 0
	global_load_lds_dwordx4 v138, s[30:31]
	s_mov_b32 m0, s22
	s_add_u32 s22, s28, 0x70080
	s_addc_u32 s23, s29, 0
	s_mov_b32 s28, m0
	s_mov_b32 m0, s58
	s_nop 0
	global_load_lds_dwordx4 v138, s[22:23]
	s_mov_b32 m0, s28
	s_barrier
	s_waitcnt lgkmcnt(0)
	s_setprio 1
	v_mfma_f32_16x16x128_f8f6f4 v[64:67], v[156:163], v[172:179], v[64:67]
	v_mfma_f32_16x16x128_f8f6f4 v[60:63], v[164:171], v[172:179], v[60:63]
	v_mfma_f32_16x16x128_f8f6f4 v[56:59], v[156:163], v[180:187], v[56:59]
	v_mfma_f32_16x16x128_f8f6f4 v[48:51], v[164:171], v[180:187], v[48:51]
	v_mfma_f32_16x16x128_f8f6f4 v[40:43], v[156:163], v[192:199], v[40:43]
	v_mfma_f32_16x16x128_f8f6f4 v[32:35], v[164:171], v[192:199], v[32:35]
	v_mfma_f32_16x16x128_f8f6f4 v[24:27], v[156:163], v[200:207], v[24:27]
	v_mfma_f32_16x16x128_f8f6f4 v[12:15], v[164:171], v[200:207], v[12:15]
	s_setprio 0
	s_barrier
	s_add_u32 s22, s26, 0xe0080
	s_addc_u32 s23, s27, 0
	s_mov_b32 s28, m0
	s_mov_b32 m0, s59
	s_nop 0
	global_load_lds_dwordx4 v138, s[22:23]
	s_mov_b32 m0, s28
	s_add_u32 s22, s26, 0x150080
	s_addc_u32 s23, s27, 0
	s_mov_b32 s26, m0
	s_mov_b32 m0, s60
	s_nop 0
	global_load_lds_dwordx4 v138, s[22:23]
	s_mov_b32 m0, s26
	s_add_i32 s73, s73, 2
	s_add_u32 s71, s71, 0x100
	s_addc_u32 s72, s72, 0
	s_cmp_gt_u32 s73, 11
	s_mov_b64 s[22:23], s[24:25]
	s_waitcnt vmcnt(6)
	s_barrier
	s_setprio 1
	v_mfma_f32_16x16x128_f8f6f4 v[52:55], v[208:215], v[172:179], v[52:55]
	v_mfma_f32_16x16x128_f8f6f4 v[44:47], v[216:223], v[172:179], v[44:47]
	v_mfma_f32_16x16x128_f8f6f4 v[36:39], v[208:215], v[180:187], v[36:39]
	v_mfma_f32_16x16x128_f8f6f4 v[28:31], v[216:223], v[180:187], v[28:31]
	v_mfma_f32_16x16x128_f8f6f4 v[20:23], v[208:215], v[192:199], v[20:23]
	v_mfma_f32_16x16x128_f8f6f4 v[16:19], v[216:223], v[192:199], v[16:19]
	v_mfma_f32_16x16x128_f8f6f4 v[8:11], v[208:215], v[200:207], v[8:11]
	v_mfma_f32_16x16x128_f8f6f4 v[0:3], v[216:223], v[200:207], v[0:3]
	s_setprio 0
	s_barrier
	s_cbranch_scc0 .LBB0_2865
	s_lshl_b32 s22, s70, 8
	v_mbcnt_lo_u32_b32 v6, -1, 0
	v_mbcnt_hi_u32_b32 v6, -1, v6
	s_add_i32 s22, s22, s53
	s_lshl_b32 s23, s69, 8
	v_ashrrev_i32_e32 v4, 2, v6
	s_or_b32 s23, s23, s54
	v_and_b32_e32 v4, -4, v4
	v_and_or_b32 v6, v6, 15, s22
	v_add_u32_e32 v4, s23, v4
	v_ashrrev_i32_e32 v7, 31, v6
	v_ashrrev_i32_e32 v5, 31, v4
	v_lshlrev_b64 v[132:133], 13, v[6:7]
	v_lshl_add_u64 v[132:133], s[4:5], 0, v[132:133]
	v_lshlrev_b64 v[134:135], 2, v[4:5]
	v_lshl_add_u64 v[4:5], v[132:133], 0, v[134:135]
	v_pk_mul_f32 v[122:123], v[122:123], s[6:7] op_sel_hi:[1,0]
	v_pk_mul_f32 v[120:121], v[120:121], s[6:7] op_sel_hi:[1,0]
	global_store_dwordx4 v[4:5], v[120:123], off offset:512
	v_pk_mul_f32 v[114:115], v[114:115], s[6:7] op_sel_hi:[1,0]
	v_pk_mul_f32 v[112:113], v[112:113], s[6:7] op_sel_hi:[1,0]
	v_or_b32_e32 v120, 16, v6
	v_ashrrev_i32_e32 v121, 31, v120
	global_store_dwordx4 v[4:5], v[112:115], off offset:576
	v_pk_mul_f32 v[130:131], v[130:131], s[6:7] op_sel_hi:[1,0]
	v_pk_mul_f32 v[128:129], v[128:129], s[6:7] op_sel_hi:[1,0]
	v_pk_mul_f32 v[112:113], v[116:117], s[6:7] op_sel_hi:[1,0]
	v_lshlrev_b64 v[116:117], 13, v[120:121]
	v_pk_mul_f32 v[126:127], v[126:127], s[6:7] op_sel_hi:[1,0]
	v_pk_mul_f32 v[124:125], v[124:125], s[6:7] op_sel_hi:[1,0]
	v_lshl_add_u64 v[116:117], s[4:5], 0, v[116:117]
	global_store_dwordx4 v[4:5], v[128:131], off
	global_store_dwordx4 v[4:5], v[124:127], off offset:64
	v_lshl_add_u64 v[116:117], v[116:117], 0, v[134:135]
	v_pk_mul_f32 v[106:107], v[106:107], s[6:7] op_sel_hi:[1,0]
; #define PG8_WAIT_V(n) asm volatile("s_waitcnt vmcnt(" #n ")" ::: "memory")
; #define PG8_BAR __builtin_amdgcn_s_barrier()
;     __device__ __forceinline__ void operator()(const f32x4 (&acc)[2][2][4][2], const Unit& u, int wr, int wc, int fr, int fq) const {
;     ...
;         for (int ai = 0; ai < 2; ++ai)
; #pragma unroll
;             for (int m = 0; m < 4; ++m) { const size_t off = (size_t)(row0 + ai * HALF + m * 16) * ldc + col0;
; #pragma unroll
;                 for (int bj = 0; bj < 2; ++bj)
; #pragma unroll
;                     for (int n = 0; n < 2; ++n) { f32x4 v = acc[ai][bj][m][n] * cs[bj][n];
;                         if (res) v += *(const f32x4*)(res + off + bj * HALF + n * 16);
;                         *(f32x4*)(out + off + bj * HALF + n * 16) = v; }
;                 asm volatile("" ::: "memory"); }
;     }
; template <class Epi, class Sched, bool FP8 = false>
; __device__ __forceinline__ void gemm_phase(LAS unsigned char* lds, const int Kb, const int nt  , const Sched& S, const Epi& E) {
;     ...
;         if (!has_next) break;
; #pragma unroll
;         for (int a = 0; a < 2; ++a)
; #pragma unroll
;             for (int b = 0; b < 2; ++b)
; #pragma unroll
;                 for (int m = 0; m < 4; ++m)
; #pragma unroll
;                     for (int n = 0; n < 2; ++n) acc[a][b][m][n] = (f32x4){0.f, 0.f, 0.f, 0.f};
;         cur = nxt; cA = nA; cB = nB; ++ui;
;     }
;     PG8_WAIT_V(0);
;     if (wr == 0) PG8_BAR;
;     PG8_BAR;
	v_pk_mul_f32 v[104:105], v[104:105], s[6:7] op_sel_hi:[1,0]
	global_store_dwordx4 v[116:117], v[104:107], off offset:512
	v_pk_mul_f32 v[98:99], v[98:99], s[6:7] op_sel_hi:[1,0]
	v_pk_mul_f32 v[96:97], v[96:97], s[6:7] op_sel_hi:[1,0]
	v_or_b32_e32 v104, 32, v6
	v_ashrrev_i32_e32 v105, 31, v104
	v_or_b32_e32 v6, 48, v6
	global_store_dwordx4 v[116:117], v[96:99], off offset:576
	v_ashrrev_i32_e32 v7, 31, v6
	v_pk_mul_f32 v[114:115], v[118:119], s[6:7] op_sel_hi:[1,0]
	v_pk_mul_f32 v[96:97], v[100:101], s[6:7] op_sel_hi:[1,0]
	v_lshlrev_b64 v[100:101], 13, v[104:105]
	v_pk_mul_f32 v[110:111], v[110:111], s[6:7] op_sel_hi:[1,0]
	v_pk_mul_f32 v[108:109], v[108:109], s[6:7] op_sel_hi:[1,0]
	v_lshl_add_u64 v[100:101], s[4:5], 0, v[100:101]
	v_lshlrev_b64 v[6:7], 13, v[6:7]
	global_store_dwordx4 v[116:117], v[112:115], off
	global_store_dwordx4 v[116:117], v[108:111], off offset:64
	v_pk_mul_f32 v[98:99], v[102:103], s[6:7] op_sel_hi:[1,0]
	v_lshl_add_u64 v[100:101], v[100:101], 0, v[134:135]
	v_pk_mul_f32 v[94:95], v[94:95], s[6:7] op_sel_hi:[1,0]
	v_pk_mul_f32 v[92:93], v[92:93], s[6:7] op_sel_hi:[1,0]
	v_pk_mul_f32 v[90:91], v[90:91], s[6:7] op_sel_hi:[1,0]
	v_pk_mul_f32 v[88:89], v[88:89], s[6:7] op_sel_hi:[1,0]
	v_pk_mul_f32 v[82:83], v[82:83], s[6:7] op_sel_hi:[1,0]
	v_pk_mul_f32 v[80:81], v[80:81], s[6:7] op_sel_hi:[1,0]
	v_lshl_add_u64 v[6:7], s[4:5], 0, v[6:7]
	global_store_dwordx4 v[100:101], v[96:99], off
	global_store_dwordx4 v[100:101], v[92:95], off offset:64
	global_store_dwordx4 v[100:101], v[88:91], off offset:512
	global_store_dwordx4 v[100:101], v[80:83], off offset:576
	v_lshl_add_u64 v[6:7], v[6:7], 0, v[134:135]
	v_pk_mul_f32 v[70:71], v[70:71], s[6:7] op_sel_hi:[1,0]
	v_pk_mul_f32 v[68:69], v[68:69], s[6:7] op_sel_hi:[1,0]
	v_pk_mul_f32 v[82:83], v[86:87], s[6:7] op_sel_hi:[1,0]
	v_pk_mul_f32 v[80:81], v[84:85], s[6:7] op_sel_hi:[1,0]
	v_pk_mul_f32 v[78:79], v[78:79], s[6:7] op_sel_hi:[1,0]
	v_pk_mul_f32 v[76:77], v[76:77], s[6:7] op_sel_hi:[1,0]
	v_pk_mul_f32 v[74:75], v[74:75], s[6:7] op_sel_hi:[1,0]
	v_pk_mul_f32 v[72:73], v[72:73], s[6:7] op_sel_hi:[1,0]
	global_store_dwordx4 v[6:7], v[68:71], off offset:576
	global_store_dwordx4 v[6:7], v[80:83], off
	global_store_dwordx4 v[6:7], v[76:79], off offset:64
	v_add_co_u32_e32 v68, vcc, s63, v4
	global_store_dwordx4 v[6:7], v[72:75], off offset:512
	v_lshl_add_u64 v[6:7], v[4:5], 0, s[8:9]
	v_addc_co_u32_e32 v69, vcc, 0, v5, vcc
	v_pk_mul_f32 v[54:55], v[54:55], s[6:7] op_sel_hi:[1,0]
	v_pk_mul_f32 v[52:53], v[52:53], s[6:7] op_sel_hi:[1,0]
	v_pk_mul_f32 v[66:67], v[66:67], s[6:7] op_sel_hi:[1,0]
	v_pk_mul_f32 v[64:65], v[64:65], s[6:7] op_sel_hi:[1,0]
	v_pk_mul_f32 v[62:63], v[62:63], s[6:7] op_sel_hi:[1,0]
	v_pk_mul_f32 v[60:61], v[60:61], s[6:7] op_sel_hi:[1,0]
	global_store_dwordx4 v[6:7], v[52:55], off offset:512
	v_pk_mul_f32 v[46:47], v[46:47], s[6:7] op_sel_hi:[1,0]
	v_pk_mul_f32 v[44:45], v[44:45], s[6:7] op_sel_hi:[1,0]
	v_add_co_u32_e32 v52, vcc, s64, v4
	global_store_dwordx4 v[68:69], v[64:67], off
	global_store_dwordx4 v[6:7], v[60:63], off offset:64
	global_store_dwordx4 v[6:7], v[44:47], off offset:576
	v_lshl_add_u64 v[6:7], v[4:5], 0, s[10:11]
	v_addc_co_u32_e32 v53, vcc, 0, v5, vcc
	v_pk_mul_f32 v[46:47], v[58:59], s[6:7] op_sel_hi:[1,0]
	v_pk_mul_f32 v[44:45], v[56:57], s[6:7] op_sel_hi:[1,0]
	v_pk_mul_f32 v[38:39], v[38:39], s[6:7] op_sel_hi:[1,0]
	v_pk_mul_f32 v[36:37], v[36:37], s[6:7] op_sel_hi:[1,0]
	global_store_dwordx4 v[52:53], v[44:47], off
	global_store_dwordx4 v[6:7], v[36:39], off offset:512
	v_pk_mul_f32 v[30:31], v[30:31], s[6:7] op_sel_hi:[1,0]
	v_pk_mul_f32 v[46:47], v[50:51], s[6:7] op_sel_hi:[1,0]
	v_pk_mul_f32 v[44:45], v[48:49], s[6:7] op_sel_hi:[1,0]
	v_pk_mul_f32 v[28:29], v[28:29], s[6:7] op_sel_hi:[1,0]
	v_add_co_u32_e32 v36, vcc, s65, v4
	global_store_dwordx4 v[6:7], v[44:47], off offset:64
	global_store_dwordx4 v[6:7], v[28:31], off offset:576
	v_lshl_add_u64 v[6:7], v[4:5], 0, s[12:13]
	v_addc_co_u32_e32 v37, vcc, 0, v5, vcc
	v_pk_mul_f32 v[30:31], v[42:43], s[6:7] op_sel_hi:[1,0]
	v_pk_mul_f32 v[28:29], v[40:41], s[6:7] op_sel_hi:[1,0]
	v_pk_mul_f32 v[22:23], v[22:23], s[6:7] op_sel_hi:[1,0]
	v_pk_mul_f32 v[20:21], v[20:21], s[6:7] op_sel_hi:[1,0]
	global_store_dwordx4 v[36:37], v[28:31], off
	global_store_dwordx4 v[6:7], v[20:23], off offset:512
	v_pk_mul_f32 v[18:19], v[18:19], s[6:7] op_sel_hi:[1,0]
	v_pk_mul_f32 v[30:31], v[34:35], s[6:7] op_sel_hi:[1,0]
	v_pk_mul_f32 v[28:29], v[32:33], s[6:7] op_sel_hi:[1,0]
	v_pk_mul_f32 v[16:17], v[16:17], s[6:7] op_sel_hi:[1,0]
	v_lshl_add_u64 v[20:21], v[4:5], 0, s[14:15]
	v_add_co_u32_e32 v4, vcc, s66, v4
	global_store_dwordx4 v[6:7], v[28:31], off offset:64
	global_store_dwordx4 v[6:7], v[16:19], off offset:576
	v_addc_co_u32_e32 v5, vcc, 0, v5, vcc
	s_nop 0
	v_pk_mul_f32 v[18:19], v[26:27], s[6:7] op_sel_hi:[1,0]
	v_pk_mul_f32 v[16:17], v[24:25], s[6:7] op_sel_hi:[1,0]
	global_store_dwordx4 v[4:5], v[16:19], off
	v_pk_mul_f32 v[6:7], v[14:15], s[6:7] op_sel_hi:[1,0]
	v_pk_mul_f32 v[4:5], v[12:13], s[6:7] op_sel_hi:[1,0]
	global_store_dwordx4 v[20:21], v[4:7], off offset:64
	v_pk_mul_f32 v[2:3], v[2:3], s[6:7] op_sel_hi:[1,0]
	v_pk_mul_f32 v[0:1], v[0:1], s[6:7] op_sel_hi:[1,0]
	v_pk_mul_f32 v[6:7], v[10:11], s[6:7] op_sel_hi:[1,0]
	v_pk_mul_f32 v[4:5], v[8:9], s[6:7] op_sel_hi:[1,0]
	global_store_dwordx4 v[20:21], v[4:7], off offset:512
	global_store_dwordx4 v[20:21], v[0:3], off offset:576
	s_and_b64 vcc, exec, s[16:17]
	s_mov_b32 s69, s67
	s_mov_b32 s70, s68
	s_mov_b64 s[24:25], s[20:21]
	s_mov_b64 s[22:23], s[18:19]
	s_cbranch_vccz .LBB0_2862
	s_waitcnt vmcnt(0)
	s_cmpk_gt_u32 s7, 0xff
	s_cbranch_scc1 .LBB0_2869
	s_barrier

; __global__ void __launch_bounds__(NTHREADS, 2) mega_fwd(Args args) {
;     extern __shared__ __attribute__((aligned(16))) unsigned char lds_raw[];
	.amdhsa_kernel _Z8mega_fwd4Args
		.amdhsa_group_segment_fixed_size 0
		.amdhsa_private_segment_fixed_size 0
		.amdhsa_kernarg_size 448
		.amdhsa_user_sgpr_count 2
		.amdhsa_user_sgpr_dispatch_ptr 0
		.amdhsa_user_sgpr_queue_ptr 0
		.amdhsa_user_sgpr_kernarg_segment_ptr 1
		.amdhsa_user_sgpr_dispatch_id 0
		.amdhsa_user_sgpr_kernarg_preload_length 0
		.amdhsa_user_sgpr_kernarg_preload_offset 0
		.amdhsa_user_sgpr_private_segment_size 0
		.amdhsa_uses_dynamic_stack 0
		.amdhsa_enable_private_segment 0
		.amdhsa_system_sgpr_workgroup_id_x 1
		.amdhsa_system_sgpr_workgroup_id_y 0
		.amdhsa_system_sgpr_workgroup_id_z 0
		.amdhsa_system_sgpr_workgroup_info 0
		.amdhsa_system_vgpr_workitem_id 0
		.amdhsa_next_free_vgpr 242
		.amdhsa_next_free_sgpr 100
		.amdhsa_accum_offset 244
		.amdhsa_reserve_vcc 1
		.amdhsa_float_round_mode_32 0
		.amdhsa_float_round_mode_16_64 0
		.amdhsa_float_denorm_mode_32 3
		.amdhsa_float_denorm_mode_16_64 3
		.amdhsa_dx10_clamp 1
		.amdhsa_ieee_mode 1
		.amdhsa_fp16_overflow 0
		.amdhsa_tg_split 0
		.amdhsa_exception_fp_ieee_invalid_op 0
		.amdhsa_exception_fp_denorm_src 0
		.amdhsa_exception_fp_ieee_div_zero 0
		.amdhsa_exception_fp_ieee_overflow 0
		.amdhsa_exception_fp_ieee_underflow 0
		.amdhsa_exception_fp_ieee_inexact 0
		.amdhsa_exception_int_div_zero 0
	.end_amdhsa_kernel

; __global__ void __launch_bounds__(NTHREADS, 2) mega_fwd(Args args) {
;     extern __shared__ __attribute__((aligned(16))) unsigned char lds_raw[];
amdhsa.kernels:
  - .agpr_count:     0
    .args:
      - .offset:         0
        .size:           192
        .value_kind:     by_value
      - .offset:         192
        .size:           4
        .value_kind:     hidden_block_count_x
      - .offset:         196
        .size:           4
        .value_kind:     hidden_block_count_y
      - .offset:         200
        .size:           4
        .value_kind:     hidden_block_count_z
      - .offset:         204
        .size:           2
        .value_kind:     hidden_group_size_x
      - .offset:         206
        .size:           2
        .value_kind:     hidden_group_size_y
      - .offset:         208
        .size:           2
        .value_kind:     hidden_group_size_z
      - .offset:         210
        .size:           2
        .value_kind:     hidden_remainder_x
      - .offset:         212
        .size:           2
        .value_kind:     hidden_remainder_y
      - .offset:         214
        .size:           2
        .value_kind:     hidden_remainder_z
      - .offset:         232
        .size:           8
        .value_kind:     hidden_global_offset_x
      - .offset:         240
        .size:           8
        .value_kind:     hidden_global_offset_y
      - .offset:         248
        .size:           8
        .value_kind:     hidden_global_offset_z
      - .offset:         256
        .size:           2
        .value_kind:     hidden_grid_dims
      - .offset:         312
        .size:           4
        .value_kind:     hidden_dynamic_lds_size
    .group_segment_fixed_size: 0
    .kernarg_segment_align: 8
    .kernarg_segment_size: 448
    .language:       OpenCL C
    .language_version:
      - 2
      - 0
    .max_flat_workgroup_size: 512
    .name:           _Z8mega_fwd4Args
    .private_segment_fixed_size: 0
    .sgpr_count:     106
    .sgpr_spill_count: 332
    .symbol:         _Z8mega_fwd4Args.kd
    .uniform_work_group_size: 1
    .uses_dynamic_stack: false
    .vgpr_count:     242
    .vgpr_spill_count: 0
    .wavefront_size: 64
